# K-loop load sections reordered: LDS-DMA tile loads issued before the fragment ds_reads (on top of setprio/waitcnt trim)
# baseline (speedup 1.0000x reference)
; #define PG8_STAGE(bufoff, gbase, voff) do { _Pragma("unroll") for (int _i = 0; _i < 2; ++_i) \
;         __builtin_amdgcn_global_load_lds((const unsigned*)((const char*)(gbase) + (voff)[_i]), (PG8_LAS unsigned*)(lds + (bufoff) + ldsw + _i * 8192), 16, 0, 0); } while (0)
; #define PG8_LDA(dst, b, h) do { _Pragma("unroll") for (int m = 0; m < 4; ++m) _Pragma("unroll") for (int k = 0; k < 2; ++k) dst[m][k] = *(const PG8_LAS bf16x8*)(lds + PG8_SA(b, h) + aoff + m * 2048 + k * 1024); } while (0)
; #define PG8_LDB(dst, b, h) do { _Pragma("unroll") for (int n = 0; n < 2; ++n) _Pragma("unroll") for (int k = 0; k < 2; ++k) dst[n][k] = *(const PG8_LAS bf16x8*)(lds + PG8_SB(b, h) + boff + n * 2048 + k * 1024); } while (0)
; #define PG8_MMA(ai, bj, At, Bt) do { __builtin_amdgcn_s_setprio(1); _Pragma("unroll") for (int m = 0; m < 4; ++m) _Pragma("unroll") for (int n = 0; n < 2; ++n) _Pragma("unroll") for (int k = 0; k < 2; ++k) \
;         acc[ai][bj][m][n] = __builtin_amdgcn_mfma_f32_16x16x32_bf16(Bt[n][k], At[m][k], acc[ai][bj][m][n], 0, 0, 0); __builtin_amdgcn_s_setprio(0); } while (0)
; #define PG8_BAR __builtin_amdgcn_s_barrier()
; template <class Epi, class Sched, bool ALIGN_EPI = false>
; __device__ __forceinline__ void gemm_phase(PG8_LAS unsigned char* lds, const Gemm g, const Sched& S, const Epi& E) {
;     ...
;             const bool last = (t == nt - 2);
;             const char* a1 = cA + (size_t)(t + 1) * kstep;
;             const char* a2 = last ? nA : cA + (size_t)(t + 2) * kstep; const char* b2 = last ? nB : cB + (size_t)(t + 2) * kstep;
;             const char* a3 = a2 + kstep; const char* b3 = b2 + kstep;
;             unsigned w0[2], w1[2];
; #pragma unroll
;             for (int i = 0; i < 2; ++i) { w0[i] = (Sched::GATHER && last) ? vn0[i] : vc0[i]; w1[i] = (Sched::GATHER && last) ? vn1[i] : vc1[i]; }
;             if (last && has_next) S.a_ready(nxt);
;             PG8_LDB(B0, 0, 0); PG8_LDB(B1, 0, 1); PG8_SCHED; PG8_LDA(At, 0, 0); PG8_STAGE(PG8_SA(1, 1), a1 + hstepA, vc1);
;             PG8_WAIT_V(8); PG8_WAIT_L(0); PG8_BAR; PG8_MMA(0, 0, At, B0); PG8_MMA(0, 1, At, B1); PG8_BAR; PG8_SCHED;
;             PG8_LDA(At, 0, 1); PG8_STAGE(PG8_SB(0, 0), b2, voffB); PG8_STAGE(PG8_SB(0, 1), b2 + hstep, voffB); PG8_STAGE(PG8_SA(0, 0), a2, w0);
;             PG8_WAIT_V(8); PG8_WAIT_L(0); PG8_BAR; PG8_MMA(1, 0, At, B0); PG8_MMA(1, 1, At, B1); PG8_BAR; PG8_SCHED;
.LBB0_247:
	s_add_u32 s52, s50, 0xfff80080
	s_addc_u32 s53, s51, -1
	s_cmp_eq_u32 s80, 28
	s_cselect_b32 s55, s9, s53
	s_cselect_b32 s54, s76, s52
	s_cselect_b32 s53, s45, s79
	s_cselect_b32 s52, s77, s78
	v_lshl_add_u64 v[160:161], s[50:51], 0, v[172:173]
	s_add_i32 m0, s59, 0xc000
	s_nop 0
	global_load_lds_dwordx4 v[160:161], off
	v_lshl_add_u64 v[160:161], s[50:51], 0, v[174:175]
	s_add_i32 m0, s59, 0xe000
	s_nop 0
	global_load_lds_dwordx4 v[160:161], off
	ds_read_b128 v[132:135], v191
	ds_read_b128 v[136:139], v191 offset:1024
	ds_read_b128 v[140:143], v191 offset:2048
	ds_read_b128 v[144:147], v191 offset:3072
	ds_read_b128 v[148:151], v193
	ds_read_b128 v[152:155], v193 offset:1024
	ds_read_b128 v[156:159], v193 offset:2048
	ds_read_b128 v[196:199], v193 offset:3072
	ds_read_b128 v[204:207], v195
	ds_read_b128 v[210:213], v195 offset:1024
	ds_read_b128 v[214:217], v195 offset:2048
	ds_read_b128 v[218:221], v195 offset:3072
	ds_read_b128 v[222:225], v195 offset:4096
	ds_read_b128 v[226:229], v195 offset:5120
	ds_read_b128 v[230:233], v195 offset:6144
	ds_read_b128 v[234:237], v195 offset:7168
	s_waitcnt vmcnt(8)
	s_waitcnt lgkmcnt(0)
	s_barrier
	v_mfma_f32_16x16x32_bf16 v[126:129], v[132:135], v[204:207], v[126:129]
	v_mfma_f32_16x16x32_bf16 v[122:125], v[140:143], v[204:207], v[122:125]
	v_mfma_f32_16x16x32_bf16 v[110:113], v[132:135], v[214:217], v[110:113]
	v_mfma_f32_16x16x32_bf16 v[106:109], v[140:143], v[214:217], v[106:109]
	v_mfma_f32_16x16x32_bf16 v[94:97], v[132:135], v[222:225], v[94:97]
	v_mfma_f32_16x16x32_bf16 v[90:93], v[140:143], v[222:225], v[90:93]
	v_mfma_f32_16x16x32_bf16 v[78:81], v[132:135], v[230:233], v[78:81]
	v_mfma_f32_16x16x32_bf16 v[74:77], v[140:143], v[230:233], v[74:77]
	v_mfma_f32_16x16x32_bf16 v[126:129], v[136:139], v[210:213], v[126:129]
	v_mfma_f32_16x16x32_bf16 v[122:125], v[144:147], v[210:213], v[122:125]
	v_mfma_f32_16x16x32_bf16 v[110:113], v[136:139], v[218:221], v[110:113]
	v_mfma_f32_16x16x32_bf16 v[106:109], v[144:147], v[218:221], v[106:109]
	v_mfma_f32_16x16x32_bf16 v[94:97], v[136:139], v[226:229], v[94:97]
	v_mfma_f32_16x16x32_bf16 v[90:93], v[144:147], v[226:229], v[90:93]
	v_mfma_f32_16x16x32_bf16 v[78:81], v[136:139], v[234:237], v[78:81]
	v_mfma_f32_16x16x32_bf16 v[74:77], v[144:147], v[234:237], v[74:77]
	v_mfma_f32_16x16x32_bf16 v[118:121], v[148:151], v[204:207], v[118:121]
	v_mfma_f32_16x16x32_bf16 v[114:117], v[156:159], v[204:207], v[114:117]
	v_mfma_f32_16x16x32_bf16 v[102:105], v[148:151], v[214:217], v[102:105]
	v_mfma_f32_16x16x32_bf16 v[98:101], v[156:159], v[214:217], v[98:101]
	v_mfma_f32_16x16x32_bf16 v[86:89], v[148:151], v[222:225], v[86:89]
	v_mfma_f32_16x16x32_bf16 v[82:85], v[156:159], v[222:225], v[82:85]
	v_mfma_f32_16x16x32_bf16 v[70:73], v[148:151], v[230:233], v[70:73]
	v_mfma_f32_16x16x32_bf16 v[66:69], v[156:159], v[230:233], v[66:69]
	v_mfma_f32_16x16x32_bf16 v[118:121], v[152:155], v[210:213], v[118:121]
	v_mfma_f32_16x16x32_bf16 v[114:117], v[196:199], v[210:213], v[114:117]
	v_mfma_f32_16x16x32_bf16 v[102:105], v[152:155], v[218:221], v[102:105]
	v_mfma_f32_16x16x32_bf16 v[98:101], v[196:199], v[218:221], v[98:101]
	v_mfma_f32_16x16x32_bf16 v[86:89], v[152:155], v[226:229], v[86:89]
	v_mfma_f32_16x16x32_bf16 v[82:85], v[196:199], v[226:229], v[82:85]
	v_mfma_f32_16x16x32_bf16 v[70:73], v[152:155], v[234:237], v[70:73]
	v_mfma_f32_16x16x32_bf16 v[66:69], v[196:199], v[234:237], v[66:69]
	s_barrier
	s_add_i32 s81, s67, s57
	v_lshl_add_u64 v[160:161], s[52:53], 0, v[164:165]
	s_mov_b32 m0, s81
	s_nop 0
	global_load_lds_dwordx4 v[160:161], off
	s_add_i32 m0, s81, 0x2000
	s_add_u32 s82, s52, 0x80000
	v_lshl_add_u64 v[200:201], s[52:53], 0, v[168:169]
	s_addc_u32 s83, s53, 0
	s_add_i32 s81, s68, s57
	global_load_lds_dwordx4 v[200:201], off
	v_lshl_add_u64 v[238:239], s[82:83], 0, v[164:165]
	s_mov_b32 m0, s81
	v_lshl_add_u64 v[240:241], s[54:55], 0, v[166:167]
	global_load_lds_dwordx4 v[238:239], off
	v_lshl_add_u64 v[238:239], s[82:83], 0, v[168:169]
	s_add_i32 m0, s81, 0x2000
	s_nop 0
	global_load_lds_dwordx4 v[238:239], off
	v_lshl_add_u64 v[238:239], s[54:55], 0, v[162:163]
	s_mov_b32 m0, s59
	s_nop 0
	global_load_lds_dwordx4 v[238:239], off
	s_mov_b32 m0, s60
	s_nop 0
	global_load_lds_dwordx4 v[240:241], off
	ds_read_b128 v[204:207], v195 offset:16384
	ds_read_b128 v[210:213], v195 offset:17408
	ds_read_b128 v[214:217], v195 offset:18432
	ds_read_b128 v[218:221], v195 offset:19456
	ds_read_b128 v[222:225], v195 offset:20480
	ds_read_b128 v[226:229], v195 offset:21504
	ds_read_b128 v[230:233], v195 offset:22528
	ds_read_b128 v[234:237], v195 offset:23552
	s_waitcnt vmcnt(8)
	s_waitcnt lgkmcnt(0)
	s_barrier
; #define PG8_STAGE(bufoff, gbase, voff) do { _Pragma("unroll") for (int _i = 0; _i < 2; ++_i) \
;         __builtin_amdgcn_global_load_lds((const unsigned*)((const char*)(gbase) + (voff)[_i]), (PG8_LAS unsigned*)(lds + (bufoff) + ldsw + _i * 8192), 16, 0, 0); } while (0)
; #define PG8_LDA(dst, b, h) do { _Pragma("unroll") for (int m = 0; m < 4; ++m) _Pragma("unroll") for (int k = 0; k < 2; ++k) dst[m][k] = *(const PG8_LAS bf16x8*)(lds + PG8_SA(b, h) + aoff + m * 2048 + k * 1024); } while (0)
; #define PG8_LDB(dst, b, h) do { _Pragma("unroll") for (int n = 0; n < 2; ++n) _Pragma("unroll") for (int k = 0; k < 2; ++k) dst[n][k] = *(const PG8_LAS bf16x8*)(lds + PG8_SB(b, h) + boff + n * 2048 + k * 1024); } while (0)
; #define PG8_MMA(ai, bj, At, Bt) do { __builtin_amdgcn_s_setprio(1); _Pragma("unroll") for (int m = 0; m < 4; ++m) _Pragma("unroll") for (int n = 0; n < 2; ++n) _Pragma("unroll") for (int k = 0; k < 2; ++k) \
;         acc[ai][bj][m][n] = __builtin_amdgcn_mfma_f32_16x16x32_bf16(Bt[n][k], At[m][k], acc[ai][bj][m][n], 0, 0, 0); __builtin_amdgcn_s_setprio(0); } while (0)
; #define PG8_WAIT_V(n) asm volatile("s_waitcnt vmcnt(" #n ")" ::: "memory")
; #define PG8_WAIT_L(n) asm volatile("s_waitcnt lgkmcnt(" #n ")" ::: "memory")
; #define PG8_BAR __builtin_amdgcn_s_barrier()
; #define PG8_SCHED __builtin_amdgcn_sched_barrier(0)
; template <class Epi, class Sched, bool ALIGN_EPI = false>
; __device__ __forceinline__ void gemm_phase(PG8_LAS unsigned char* lds, const Gemm g, const Sched& S, const Epi& E) {
;     ...
;             PG8_WAIT_V(8); PG8_WAIT_L(0); PG8_BAR; PG8_MMA(1, 0, At, B0); PG8_MMA(1, 1, At, B1); PG8_BAR; PG8_SCHED;
;             PG8_LDB(B0, 1, 0); PG8_LDB(B1, 1, 1); PG8_SCHED; PG8_LDA(At, 1, 0); PG8_STAGE(PG8_SA(0, 1), a2 + hstepA, w1);
;             PG8_WAIT_V(8); PG8_WAIT_L(0); PG8_BAR; PG8_MMA(0, 0, At, B0); PG8_MMA(0, 1, At, B1); PG8_BAR; PG8_SCHED;
	v_mfma_f32_16x16x32_bf16 v[54:57], v[132:135], v[204:207], v[54:57]
	v_mfma_f32_16x16x32_bf16 v[50:53], v[140:143], v[204:207], v[50:53]
	v_mfma_f32_16x16x32_bf16 v[38:41], v[132:135], v[214:217], v[38:41]
	v_mfma_f32_16x16x32_bf16 v[34:37], v[140:143], v[214:217], v[34:37]
	v_mfma_f32_16x16x32_bf16 v[22:25], v[132:135], v[222:225], v[22:25]
	v_mfma_f32_16x16x32_bf16 v[18:21], v[140:143], v[222:225], v[18:21]
	v_mfma_f32_16x16x32_bf16 v[6:9], v[132:135], v[230:233], v[6:9]
	v_mfma_f32_16x16x32_bf16 v[2:5], v[140:143], v[230:233], v[2:5]
	v_mfma_f32_16x16x32_bf16 v[54:57], v[136:139], v[210:213], v[54:57]
	v_mfma_f32_16x16x32_bf16 v[50:53], v[144:147], v[210:213], v[50:53]
	v_mfma_f32_16x16x32_bf16 v[38:41], v[136:139], v[218:221], v[38:41]
	v_mfma_f32_16x16x32_bf16 v[34:37], v[144:147], v[218:221], v[34:37]
	v_mfma_f32_16x16x32_bf16 v[22:25], v[136:139], v[226:229], v[22:25]
	v_mfma_f32_16x16x32_bf16 v[18:21], v[144:147], v[226:229], v[18:21]
	v_mfma_f32_16x16x32_bf16 v[6:9], v[136:139], v[234:237], v[6:9]
	v_mfma_f32_16x16x32_bf16 v[2:5], v[144:147], v[234:237], v[2:5]
	v_mfma_f32_16x16x32_bf16 v[58:61], v[148:151], v[204:207], v[58:61]
	v_mfma_f32_16x16x32_bf16 v[62:65], v[156:159], v[204:207], v[62:65]
	v_mfma_f32_16x16x32_bf16 v[42:45], v[148:151], v[214:217], v[42:45]
	v_mfma_f32_16x16x32_bf16 v[46:49], v[156:159], v[214:217], v[46:49]
	v_mfma_f32_16x16x32_bf16 v[26:29], v[148:151], v[222:225], v[26:29]
	v_mfma_f32_16x16x32_bf16 v[30:33], v[156:159], v[222:225], v[30:33]
	v_mfma_f32_16x16x32_bf16 v[10:13], v[148:151], v[230:233], v[10:13]
	v_mfma_f32_16x16x32_bf16 v[14:17], v[156:159], v[230:233], v[14:17]
	v_mfma_f32_16x16x32_bf16 v[58:61], v[152:155], v[210:213], v[58:61]
	v_mfma_f32_16x16x32_bf16 v[62:65], v[196:199], v[210:213], v[62:65]
	v_mfma_f32_16x16x32_bf16 v[42:45], v[152:155], v[218:221], v[42:45]
	v_mfma_f32_16x16x32_bf16 v[46:49], v[196:199], v[218:221], v[46:49]
	v_mfma_f32_16x16x32_bf16 v[26:29], v[152:155], v[226:229], v[26:29]
	v_mfma_f32_16x16x32_bf16 v[30:33], v[196:199], v[226:229], v[30:33]
	v_mfma_f32_16x16x32_bf16 v[10:13], v[152:155], v[234:237], v[10:13]
	v_mfma_f32_16x16x32_bf16 v[14:17], v[196:199], v[234:237], v[14:17]
	s_barrier
	s_add_i32 s81, 0, 0x18000
	s_add_i32 s82, 0, 0x1c000
	s_add_u32 s54, s54, 0x80000
	s_addc_u32 s55, s55, 0
	s_mov_b32 m0, s61
	v_lshl_add_u64 v[242:243], s[54:55], 0, v[162:163]
	global_load_lds_dwordx4 v[242:243], off
	v_lshl_add_u64 v[242:243], s[54:55], 0, v[166:167]
	s_mov_b32 m0, s62
	s_nop 0
	global_load_lds_dwordx4 v[242:243], off
	v_add_u32_e32 v131, s81, v181
	ds_read_b128 v[132:135], v131
	ds_read_b128 v[136:139], v131 offset:1024
	ds_read_b128 v[140:143], v131 offset:2048
	ds_read_b128 v[144:147], v131 offset:3072
	v_add_u32_e32 v131, s82, v181
	ds_read_b128 v[148:151], v131
	ds_read_b128 v[152:155], v131 offset:1024
	ds_read_b128 v[156:159], v131 offset:2048
	ds_read_b128 v[196:199], v131 offset:3072
	ds_read_b128 v[204:207], v195 offset:32768
	ds_read_b128 v[210:213], v195 offset:33792
	ds_read_b128 v[214:217], v195 offset:34816
	ds_read_b128 v[218:221], v195 offset:35840
	ds_read_b128 v[222:225], v195 offset:36864
	ds_read_b128 v[226:229], v195 offset:37888
	ds_read_b128 v[230:233], v195 offset:38912
	ds_read_b128 v[234:237], v195 offset:39936
	s_waitcnt vmcnt(8)
	s_waitcnt lgkmcnt(0)
	s_barrier
	v_mfma_f32_16x16x32_bf16 v[126:129], v[132:135], v[204:207], v[126:129]
	v_mfma_f32_16x16x32_bf16 v[122:125], v[140:143], v[204:207], v[122:125]
	v_mfma_f32_16x16x32_bf16 v[110:113], v[132:135], v[214:217], v[110:113]
	v_mfma_f32_16x16x32_bf16 v[106:109], v[140:143], v[214:217], v[106:109]
	v_mfma_f32_16x16x32_bf16 v[94:97], v[132:135], v[222:225], v[94:97]
	v_mfma_f32_16x16x32_bf16 v[90:93], v[140:143], v[222:225], v[90:93]
	v_mfma_f32_16x16x32_bf16 v[78:81], v[132:135], v[230:233], v[78:81]
	v_mfma_f32_16x16x32_bf16 v[74:77], v[140:143], v[230:233], v[74:77]
	v_mfma_f32_16x16x32_bf16 v[126:129], v[136:139], v[210:213], v[126:129]
	v_mfma_f32_16x16x32_bf16 v[122:125], v[144:147], v[210:213], v[122:125]
	v_mfma_f32_16x16x32_bf16 v[110:113], v[136:139], v[218:221], v[110:113]
	v_mfma_f32_16x16x32_bf16 v[106:109], v[144:147], v[218:221], v[106:109]
	v_mfma_f32_16x16x32_bf16 v[94:97], v[136:139], v[226:229], v[94:97]
	v_mfma_f32_16x16x32_bf16 v[90:93], v[144:147], v[226:229], v[90:93]
	v_mfma_f32_16x16x32_bf16 v[78:81], v[136:139], v[234:237], v[78:81]
	v_mfma_f32_16x16x32_bf16 v[74:77], v[144:147], v[234:237], v[74:77]
	v_mfma_f32_16x16x32_bf16 v[118:121], v[148:151], v[204:207], v[118:121]
	v_mfma_f32_16x16x32_bf16 v[114:117], v[156:159], v[204:207], v[114:117]
	v_mfma_f32_16x16x32_bf16 v[102:105], v[148:151], v[214:217], v[102:105]
	v_mfma_f32_16x16x32_bf16 v[98:101], v[156:159], v[214:217], v[98:101]
	v_mfma_f32_16x16x32_bf16 v[86:89], v[148:151], v[222:225], v[86:89]
	v_mfma_f32_16x16x32_bf16 v[82:85], v[156:159], v[222:225], v[82:85]
	v_mfma_f32_16x16x32_bf16 v[70:73], v[148:151], v[230:233], v[70:73]
	v_mfma_f32_16x16x32_bf16 v[66:69], v[156:159], v[230:233], v[66:69]
	v_mfma_f32_16x16x32_bf16 v[118:121], v[152:155], v[210:213], v[118:121]
	v_mfma_f32_16x16x32_bf16 v[114:117], v[196:199], v[210:213], v[114:117]
	v_mfma_f32_16x16x32_bf16 v[102:105], v[152:155], v[218:221], v[102:105]
	v_mfma_f32_16x16x32_bf16 v[98:101], v[196:199], v[218:221], v[98:101]
	v_mfma_f32_16x16x32_bf16 v[86:89], v[152:155], v[226:229], v[86:89]
	v_mfma_f32_16x16x32_bf16 v[82:85], v[196:199], v[226:229], v[82:85]
	v_mfma_f32_16x16x32_bf16 v[70:73], v[152:155], v[234:237], v[70:73]
	v_mfma_f32_16x16x32_bf16 v[66:69], v[196:199], v[234:237], v[66:69]
	s_barrier
; #define PG8_STAGE(bufoff, gbase, voff) do { _Pragma("unroll") for (int _i = 0; _i < 2; ++_i) \
;         __builtin_amdgcn_global_load_lds((const unsigned*)((const char*)(gbase) + (voff)[_i]), (PG8_LAS unsigned*)(lds + (bufoff) + ldsw + _i * 8192), 16, 0, 0); } while (0)
; #define PG8_LDA(dst, b, h) do { _Pragma("unroll") for (int m = 0; m < 4; ++m) _Pragma("unroll") for (int k = 0; k < 2; ++k) dst[m][k] = *(const PG8_LAS bf16x8*)(lds + PG8_SA(b, h) + aoff + m * 2048 + k * 1024); } while (0)
; #define PG8_MMA(ai, bj, At, Bt) do { __builtin_amdgcn_s_setprio(1); _Pragma("unroll") for (int m = 0; m < 4; ++m) _Pragma("unroll") for (int n = 0; n < 2; ++n) _Pragma("unroll") for (int k = 0; k < 2; ++k) \
;         acc[ai][bj][m][n] = __builtin_amdgcn_mfma_f32_16x16x32_bf16(Bt[n][k], At[m][k], acc[ai][bj][m][n], 0, 0, 0); __builtin_amdgcn_s_setprio(0); } while (0)
; #define PG8_WAIT_V(n) asm volatile("s_waitcnt vmcnt(" #n ")" ::: "memory")
; #define PG8_WAIT_L(n) asm volatile("s_waitcnt lgkmcnt(" #n ")" ::: "memory")
; #define PG8_BAR __builtin_amdgcn_s_barrier()
; #define PG8_SCHED __builtin_amdgcn_sched_barrier(0)
; template <class Epi, class Sched, bool ALIGN_EPI = false>
; __device__ __forceinline__ void gemm_phase(PG8_LAS unsigned char* lds, const Gemm g, const Sched& S, const Epi& E) {
;     ...
;             PG8_LDA(At, 1, 1); PG8_STAGE(PG8_SB(1, 0), b3, voffB); PG8_STAGE(PG8_SB(1, 1), b3 + hstep, voffB); PG8_STAGE(PG8_SA(1, 0), a3, w0);
;             PG8_WAIT_V(8); PG8_WAIT_L(0); PG8_BAR; PG8_MMA(1, 0, At, B0); PG8_MMA(1, 1, At, B1); PG8_BAR; PG8_SCHED;
;             if constexpr (Epi::KSCALE) { if (((t + 2) & 7) == 0 && t + 2 < nt) { E.kscale(acc, pf, ((t + 2) >> 3) - 1, wr, fr); PG8_SCHED; } }
;         }
	s_add_i32 s54, s81, s57
	v_lshl_add_u64 v[160:161], v[160:161], 0, s[20:21]
	s_mov_b32 m0, s54
	s_nop 0
	global_load_lds_dwordx4 v[160:161], off
	s_add_i32 m0, s54, 0x2000
	s_add_u32 s52, s52, 0x80080
	v_lshl_add_u64 v[160:161], v[200:201], 0, s[20:21]
	s_addc_u32 s53, s53, 0
	s_add_i32 s54, s82, s57
	global_load_lds_dwordx4 v[160:161], off
	v_lshl_add_u64 v[160:161], s[52:53], 0, v[164:165]
	s_mov_b32 m0, s54
	s_nop 0
	global_load_lds_dwordx4 v[160:161], off
	v_lshl_add_u64 v[160:161], s[52:53], 0, v[168:169]
	s_add_i32 m0, s54, 0x2000
	s_nop 0
	global_load_lds_dwordx4 v[160:161], off
	v_lshl_add_u64 v[160:161], v[238:239], 0, s[20:21]
	s_mov_b32 m0, s65
	s_nop 0
	global_load_lds_dwordx4 v[160:161], off
	v_lshl_add_u64 v[160:161], v[240:241], 0, s[20:21]
	s_mov_b32 m0, s66
	s_nop 0
	global_load_lds_dwordx4 v[160:161], off
	ds_read_b128 v[204:207], v195 offset:49152
	ds_read_b128 v[210:213], v195 offset:50176
	ds_read_b128 v[214:217], v195 offset:51200
	ds_read_b128 v[218:221], v195 offset:52224
	ds_read_b128 v[222:225], v195 offset:53248
	ds_read_b128 v[226:229], v195 offset:54272
	ds_read_b128 v[230:233], v195 offset:55296
	ds_read_b128 v[234:237], v195 offset:56320
	s_waitcnt vmcnt(8)
	s_waitcnt lgkmcnt(0)
	s_barrier
	v_mfma_f32_16x16x32_bf16 v[54:57], v[132:135], v[204:207], v[54:57]
	v_mfma_f32_16x16x32_bf16 v[50:53], v[140:143], v[204:207], v[50:53]
	v_mfma_f32_16x16x32_bf16 v[38:41], v[132:135], v[214:217], v[38:41]
	v_mfma_f32_16x16x32_bf16 v[34:37], v[140:143], v[214:217], v[34:37]
	v_mfma_f32_16x16x32_bf16 v[22:25], v[132:135], v[222:225], v[22:25]
	v_mfma_f32_16x16x32_bf16 v[18:21], v[140:143], v[222:225], v[18:21]
	v_mfma_f32_16x16x32_bf16 v[6:9], v[132:135], v[230:233], v[6:9]
	v_mfma_f32_16x16x32_bf16 v[2:5], v[140:143], v[230:233], v[2:5]
	v_mfma_f32_16x16x32_bf16 v[54:57], v[136:139], v[210:213], v[54:57]
	v_mfma_f32_16x16x32_bf16 v[50:53], v[144:147], v[210:213], v[50:53]
	v_mfma_f32_16x16x32_bf16 v[38:41], v[136:139], v[218:221], v[38:41]
	v_mfma_f32_16x16x32_bf16 v[34:37], v[144:147], v[218:221], v[34:37]
	v_mfma_f32_16x16x32_bf16 v[22:25], v[136:139], v[226:229], v[22:25]
	v_mfma_f32_16x16x32_bf16 v[18:21], v[144:147], v[226:229], v[18:21]
	v_mfma_f32_16x16x32_bf16 v[6:9], v[136:139], v[234:237], v[6:9]
	v_mfma_f32_16x16x32_bf16 v[2:5], v[144:147], v[234:237], v[2:5]
	v_mfma_f32_16x16x32_bf16 v[58:61], v[148:151], v[204:207], v[58:61]
	v_mfma_f32_16x16x32_bf16 v[62:65], v[156:159], v[204:207], v[62:65]
	v_mfma_f32_16x16x32_bf16 v[42:45], v[148:151], v[214:217], v[42:45]
	v_mfma_f32_16x16x32_bf16 v[46:49], v[156:159], v[214:217], v[46:49]
	v_mfma_f32_16x16x32_bf16 v[26:29], v[148:151], v[222:225], v[26:29]
	v_mfma_f32_16x16x32_bf16 v[30:33], v[156:159], v[222:225], v[30:33]
	v_mfma_f32_16x16x32_bf16 v[10:13], v[148:151], v[230:233], v[10:13]
	v_mfma_f32_16x16x32_bf16 v[14:17], v[156:159], v[230:233], v[14:17]
	v_mfma_f32_16x16x32_bf16 v[58:61], v[152:155], v[210:213], v[58:61]
	v_mfma_f32_16x16x32_bf16 v[62:65], v[196:199], v[210:213], v[62:65]
	v_mfma_f32_16x16x32_bf16 v[42:45], v[152:155], v[218:221], v[42:45]
	v_mfma_f32_16x16x32_bf16 v[46:49], v[196:199], v[218:221], v[46:49]
	v_mfma_f32_16x16x32_bf16 v[26:29], v[152:155], v[226:229], v[26:29]
	v_mfma_f32_16x16x32_bf16 v[30:33], v[196:199], v[226:229], v[30:33]
	v_mfma_f32_16x16x32_bf16 v[10:13], v[152:155], v[234:237], v[10:13]
	v_mfma_f32_16x16x32_bf16 v[14:17], v[196:199], v[234:237], v[14:17]
	s_barrier
	s_add_i32 s80, s80, 2
	s_add_u32 s50, s50, 0x100
	s_addc_u32 s51, s51, 0
	s_add_u32 s78, s78, 0x100
	s_addc_u32 s79, s79, 0
	s_cmp_gt_u32 s80, 29
	s_cbranch_scc0 .LBB0_247
	s_and_b64 vcc, exec, s[22:23]
	s_cbranch_vccz .LBB0_250
	s_barrier

; #define PG8_STAGE(bufoff, gbase, voff) do { _Pragma("unroll") for (int _i = 0; _i < 2; ++_i) \
;         __builtin_amdgcn_global_load_lds((const unsigned*)((const char*)(gbase) + (voff)[_i]), (PG8_LAS unsigned*)(lds + (bufoff) + ldsw + _i * 8192), 16, 0, 0); } while (0)
; #define PG8_LDA(dst, b, h) do { _Pragma("unroll") for (int m = 0; m < 4; ++m) _Pragma("unroll") for (int k = 0; k < 2; ++k) dst[m][k] = *(const PG8_LAS bf16x8*)(lds + PG8_SA(b, h) + aoff + m * 2048 + k * 1024); } while (0)
; #define PG8_LDB(dst, b, h) do { _Pragma("unroll") for (int n = 0; n < 2; ++n) _Pragma("unroll") for (int k = 0; k < 2; ++k) dst[n][k] = *(const PG8_LAS bf16x8*)(lds + PG8_SB(b, h) + boff + n * 2048 + k * 1024); } while (0)
; #define PG8_MMA(ai, bj, At, Bt) do { __builtin_amdgcn_s_setprio(1); _Pragma("unroll") for (int m = 0; m < 4; ++m) _Pragma("unroll") for (int n = 0; n < 2; ++n) _Pragma("unroll") for (int k = 0; k < 2; ++k) \
;         acc[ai][bj][m][n] = __builtin_amdgcn_mfma_f32_16x16x32_bf16(Bt[n][k], At[m][k], acc[ai][bj][m][n], 0, 0, 0); __builtin_amdgcn_s_setprio(0); } while (0)
; #define PG8_BAR __builtin_amdgcn_s_barrier()
; template <class Epi, class Sched, bool ALIGN_EPI = false>
; __device__ __forceinline__ void gemm_phase(PG8_LAS unsigned char* lds, const Gemm g, const Sched& S, const Epi& E) {
;     ...
;             const bool last = (t == nt - 2);
;             const char* a1 = cA + (size_t)(t + 1) * kstep;
;             const char* a2 = last ? nA : cA + (size_t)(t + 2) * kstep; const char* b2 = last ? nB : cB + (size_t)(t + 2) * kstep;
;             const char* a3 = a2 + kstep; const char* b3 = b2 + kstep;
;             unsigned w0[2], w1[2];
; #pragma unroll
;             for (int i = 0; i < 2; ++i) { w0[i] = (Sched::GATHER && last) ? vn0[i] : vc0[i]; w1[i] = (Sched::GATHER && last) ? vn1[i] : vc1[i]; }
;             if (last && has_next) S.a_ready(nxt);
;             PG8_LDB(B0, 0, 0); PG8_LDB(B1, 0, 1); PG8_SCHED; PG8_LDA(At, 0, 0); PG8_STAGE(PG8_SA(1, 1), a1 + hstepA, vc1);
;             PG8_WAIT_V(8); PG8_WAIT_L(0); PG8_BAR; PG8_MMA(0, 0, At, B0); PG8_MMA(0, 1, At, B1); PG8_BAR; PG8_SCHED;
;             PG8_LDA(At, 0, 1); PG8_STAGE(PG8_SB(0, 0), b2, voffB); PG8_STAGE(PG8_SB(0, 1), b2 + hstep, voffB); PG8_STAGE(PG8_SA(0, 0), a2, w0);
;             PG8_WAIT_V(8); PG8_WAIT_L(0); PG8_BAR; PG8_MMA(1, 0, At, B0); PG8_MMA(1, 1, At, B1); PG8_BAR; PG8_SCHED;
.LBB0_504:
	s_add_u32 s54, s50, s52
	s_addc_u32 s55, s51, s53
	s_waitcnt lgkmcnt(0)
	s_add_u32 s54, s54, 0x100
	s_addc_u32 s55, s55, 0
	s_add_u32 s82, s79, s52
	s_addc_u32 s83, s80, s53
	s_cmpk_eq_i32 s52, 0xf00
	s_cselect_b32 s57, s47, s55
	s_cselect_b32 s56, s49, s54
	s_cselect_b32 s55, s45, s83
	s_cselect_b32 s54, s78, s82
	v_lshl_add_u64 v[142:143], v[132:133], 0, s[52:53]
	s_add_i32 m0, s62, 0xc000
	s_nop 0
	global_load_lds_dwordx4 v[142:143], off
	v_lshl_add_u64 v[142:143], v[134:135], 0, s[52:53]
	s_add_i32 m0, s62, 0xe000
	s_nop 0
	global_load_lds_dwordx4 v[142:143], off
	v_add_u32_e32 v3, s74, v178
	ds_read_b128 v[138:141], v3
	ds_read_b128 v[162:165], v3 offset:1024
	ds_read_b128 v[166:169], v3 offset:2048
	ds_read_b128 v[170:173], v3 offset:3072
	v_add_u32_e32 v3, s75, v178
	ds_read_b128 v[186:189], v3
	ds_read_b128 v[190:193], v3 offset:1024
	ds_read_b128 v[194:197], v3 offset:2048
	ds_read_b128 v[198:201], v3 offset:3072
	ds_read_b128 v[202:205], v184
	ds_read_b128 v[206:209], v184 offset:1024
	ds_read_b128 v[210:213], v184 offset:2048
	ds_read_b128 v[214:217], v184 offset:3072
	ds_read_b128 v[218:221], v184 offset:4096
	ds_read_b128 v[222:225], v184 offset:5120
	ds_read_b128 v[226:229], v184 offset:6144
	ds_read_b128 v[230:233], v184 offset:7168
	s_waitcnt vmcnt(8)
	s_waitcnt lgkmcnt(0)
	s_barrier
	v_mfma_f32_16x16x32_bf16 v[128:131], v[138:141], v[202:205], v[128:131]
	v_mfma_f32_16x16x32_bf16 v[124:127], v[166:169], v[202:205], v[124:127]
	v_mfma_f32_16x16x32_bf16 v[120:123], v[138:141], v[210:213], v[120:123]
	v_mfma_f32_16x16x32_bf16 v[112:115], v[166:169], v[210:213], v[112:115]
	v_mfma_f32_16x16x32_bf16 v[96:99], v[138:141], v[218:221], v[96:99]
	v_mfma_f32_16x16x32_bf16 v[92:95], v[166:169], v[218:221], v[92:95]
	v_mfma_f32_16x16x32_bf16 v[80:83], v[138:141], v[226:229], v[80:83]
	v_mfma_f32_16x16x32_bf16 v[76:79], v[166:169], v[226:229], v[76:79]
	v_mfma_f32_16x16x32_bf16 v[128:131], v[162:165], v[206:209], v[128:131]
	v_mfma_f32_16x16x32_bf16 v[124:127], v[170:173], v[206:209], v[124:127]
	v_mfma_f32_16x16x32_bf16 v[120:123], v[162:165], v[214:217], v[120:123]
	v_mfma_f32_16x16x32_bf16 v[112:115], v[170:173], v[214:217], v[112:115]
	v_mfma_f32_16x16x32_bf16 v[96:99], v[162:165], v[222:225], v[96:99]
	v_mfma_f32_16x16x32_bf16 v[92:95], v[170:173], v[222:225], v[92:95]
	v_mfma_f32_16x16x32_bf16 v[80:83], v[162:165], v[230:233], v[80:83]
	v_mfma_f32_16x16x32_bf16 v[76:79], v[170:173], v[230:233], v[76:79]
	v_mfma_f32_16x16x32_bf16 v[116:119], v[186:189], v[202:205], v[116:119]
	v_mfma_f32_16x16x32_bf16 v[108:111], v[194:197], v[202:205], v[108:111]
	v_mfma_f32_16x16x32_bf16 v[104:107], v[186:189], v[210:213], v[104:107]
	v_mfma_f32_16x16x32_bf16 v[100:103], v[194:197], v[210:213], v[100:103]
	v_mfma_f32_16x16x32_bf16 v[88:91], v[186:189], v[218:221], v[88:91]
	v_mfma_f32_16x16x32_bf16 v[84:87], v[194:197], v[218:221], v[84:87]
	v_mfma_f32_16x16x32_bf16 v[72:75], v[186:189], v[226:229], v[72:75]
	v_mfma_f32_16x16x32_bf16 v[68:71], v[194:197], v[226:229], v[68:71]
	v_mfma_f32_16x16x32_bf16 v[116:119], v[190:193], v[206:209], v[116:119]
	v_mfma_f32_16x16x32_bf16 v[108:111], v[198:201], v[206:209], v[108:111]
	v_mfma_f32_16x16x32_bf16 v[104:107], v[190:193], v[214:217], v[104:107]
	v_mfma_f32_16x16x32_bf16 v[100:103], v[198:201], v[214:217], v[100:103]
	v_mfma_f32_16x16x32_bf16 v[88:91], v[190:193], v[222:225], v[88:91]
	v_mfma_f32_16x16x32_bf16 v[84:87], v[198:201], v[222:225], v[84:87]
	v_mfma_f32_16x16x32_bf16 v[72:75], v[190:193], v[230:233], v[72:75]
	v_mfma_f32_16x16x32_bf16 v[68:71], v[198:201], v[230:233], v[68:71]
	s_barrier
	s_add_i32 s82, s74, s61
	v_lshl_add_u64 v[142:143], s[54:55], 0, v[146:147]
	s_mov_b32 m0, s82
	s_nop 0
	global_load_lds_dwordx4 v[142:143], off
	s_add_i32 m0, s82, 0x2000
	s_add_u32 s82, s54, 0x80000
	v_lshl_add_u64 v[174:175], s[54:55], 0, v[150:151]
	s_addc_u32 s83, s55, 0
	s_add_i32 s84, s75, s61
	global_load_lds_dwordx4 v[174:175], off
	v_lshl_add_u64 v[234:235], s[82:83], 0, v[146:147]
	s_mov_b32 m0, s84
	v_lshl_add_u64 v[236:237], s[56:57], 0, v[148:149]
	global_load_lds_dwordx4 v[234:235], off
	v_lshl_add_u64 v[234:235], s[82:83], 0, v[150:151]
	s_add_i32 m0, s84, 0x2000
	s_nop 0
	global_load_lds_dwordx4 v[234:235], off
	v_lshl_add_u64 v[234:235], s[56:57], 0, v[144:145]
	s_mov_b32 m0, s62
	s_nop 0
	global_load_lds_dwordx4 v[234:235], off
	s_mov_b32 m0, s63
	s_nop 0
	global_load_lds_dwordx4 v[236:237], off
	ds_read_b128 v[202:205], v184 offset:16384
	ds_read_b128 v[206:209], v184 offset:17408
	ds_read_b128 v[210:213], v184 offset:18432
	ds_read_b128 v[214:217], v184 offset:19456
	ds_read_b128 v[218:221], v184 offset:20480
	ds_read_b128 v[222:225], v184 offset:21504
	ds_read_b128 v[226:229], v184 offset:22528
	ds_read_b128 v[230:233], v184 offset:23552
	s_waitcnt vmcnt(8)
	s_waitcnt lgkmcnt(0)
	s_barrier
; #define PG8_STAGE(bufoff, gbase, voff) do { _Pragma("unroll") for (int _i = 0; _i < 2; ++_i) \
;         __builtin_amdgcn_global_load_lds((const unsigned*)((const char*)(gbase) + (voff)[_i]), (PG8_LAS unsigned*)(lds + (bufoff) + ldsw + _i * 8192), 16, 0, 0); } while (0)
; #define PG8_LDA(dst, b, h) do { _Pragma("unroll") for (int m = 0; m < 4; ++m) _Pragma("unroll") for (int k = 0; k < 2; ++k) dst[m][k] = *(const PG8_LAS bf16x8*)(lds + PG8_SA(b, h) + aoff + m * 2048 + k * 1024); } while (0)
; #define PG8_LDB(dst, b, h) do { _Pragma("unroll") for (int n = 0; n < 2; ++n) _Pragma("unroll") for (int k = 0; k < 2; ++k) dst[n][k] = *(const PG8_LAS bf16x8*)(lds + PG8_SB(b, h) + boff + n * 2048 + k * 1024); } while (0)
; #define PG8_MMA(ai, bj, At, Bt) do { __builtin_amdgcn_s_setprio(1); _Pragma("unroll") for (int m = 0; m < 4; ++m) _Pragma("unroll") for (int n = 0; n < 2; ++n) _Pragma("unroll") for (int k = 0; k < 2; ++k) \
;         acc[ai][bj][m][n] = __builtin_amdgcn_mfma_f32_16x16x32_bf16(Bt[n][k], At[m][k], acc[ai][bj][m][n], 0, 0, 0); __builtin_amdgcn_s_setprio(0); } while (0)
; #define PG8_WAIT_V(n) asm volatile("s_waitcnt vmcnt(" #n ")" ::: "memory")
; #define PG8_WAIT_L(n) asm volatile("s_waitcnt lgkmcnt(" #n ")" ::: "memory")
; #define PG8_BAR __builtin_amdgcn_s_barrier()
; #define PG8_SCHED __builtin_amdgcn_sched_barrier(0)
; template <class Epi, class Sched, bool ALIGN_EPI = false>
; __device__ __forceinline__ void gemm_phase(PG8_LAS unsigned char* lds, const Gemm g, const Sched& S, const Epi& E) {
;     ...
;             PG8_WAIT_V(8); PG8_WAIT_L(0); PG8_BAR; PG8_MMA(1, 0, At, B0); PG8_MMA(1, 1, At, B1); PG8_BAR; PG8_SCHED;
;             PG8_LDB(B0, 1, 0); PG8_LDB(B1, 1, 1); PG8_SCHED; PG8_LDA(At, 1, 0); PG8_STAGE(PG8_SA(0, 1), a2 + hstepA, w1);
;             PG8_WAIT_V(8); PG8_WAIT_L(0); PG8_BAR; PG8_MMA(0, 0, At, B0); PG8_MMA(0, 1, At, B1); PG8_BAR; PG8_SCHED;
	v_mfma_f32_16x16x32_bf16 v[64:67], v[138:141], v[202:205], v[64:67]
	v_mfma_f32_16x16x32_bf16 v[60:63], v[166:169], v[202:205], v[60:63]
	v_mfma_f32_16x16x32_bf16 v[48:51], v[138:141], v[210:213], v[48:51]
	v_mfma_f32_16x16x32_bf16 v[44:47], v[166:169], v[210:213], v[44:47]
	v_mfma_f32_16x16x32_bf16 v[32:35], v[138:141], v[218:221], v[32:35]
	v_mfma_f32_16x16x32_bf16 v[28:31], v[166:169], v[218:221], v[28:31]
	v_mfma_f32_16x16x32_bf16 v[16:19], v[138:141], v[226:229], v[16:19]
	v_mfma_f32_16x16x32_bf16 v[12:15], v[166:169], v[226:229], v[12:15]
	v_mfma_f32_16x16x32_bf16 v[64:67], v[162:165], v[206:209], v[64:67]
	v_mfma_f32_16x16x32_bf16 v[60:63], v[170:173], v[206:209], v[60:63]
	v_mfma_f32_16x16x32_bf16 v[48:51], v[162:165], v[214:217], v[48:51]
	v_mfma_f32_16x16x32_bf16 v[44:47], v[170:173], v[214:217], v[44:47]
	v_mfma_f32_16x16x32_bf16 v[32:35], v[162:165], v[222:225], v[32:35]
	v_mfma_f32_16x16x32_bf16 v[28:31], v[170:173], v[222:225], v[28:31]
	v_mfma_f32_16x16x32_bf16 v[16:19], v[162:165], v[230:233], v[16:19]
	v_mfma_f32_16x16x32_bf16 v[12:15], v[170:173], v[230:233], v[12:15]
	v_mfma_f32_16x16x32_bf16 v[56:59], v[186:189], v[202:205], v[56:59]
	v_mfma_f32_16x16x32_bf16 v[52:55], v[194:197], v[202:205], v[52:55]
	v_mfma_f32_16x16x32_bf16 v[40:43], v[186:189], v[210:213], v[40:43]
	v_mfma_f32_16x16x32_bf16 v[36:39], v[194:197], v[210:213], v[36:39]
	v_mfma_f32_16x16x32_bf16 v[24:27], v[186:189], v[218:221], v[24:27]
	v_mfma_f32_16x16x32_bf16 v[20:23], v[194:197], v[218:221], v[20:23]
	v_mfma_f32_16x16x32_bf16 v[8:11], v[186:189], v[226:229], v[8:11]
	v_mfma_f32_16x16x32_bf16 v[4:7], v[194:197], v[226:229], v[4:7]
	v_mfma_f32_16x16x32_bf16 v[56:59], v[190:193], v[206:209], v[56:59]
	v_mfma_f32_16x16x32_bf16 v[52:55], v[198:201], v[206:209], v[52:55]
	v_mfma_f32_16x16x32_bf16 v[40:43], v[190:193], v[214:217], v[40:43]
	v_mfma_f32_16x16x32_bf16 v[36:39], v[198:201], v[214:217], v[36:39]
	v_mfma_f32_16x16x32_bf16 v[24:27], v[190:193], v[222:225], v[24:27]
	v_mfma_f32_16x16x32_bf16 v[20:23], v[198:201], v[222:225], v[20:23]
	v_mfma_f32_16x16x32_bf16 v[8:11], v[190:193], v[230:233], v[8:11]
	v_mfma_f32_16x16x32_bf16 v[4:7], v[198:201], v[230:233], v[4:7]
	s_barrier
	s_add_i32 s82, 0, 0x18000
	s_add_i32 s83, 0, 0x1c000
	s_add_u32 s56, s56, 0x80000
	s_addc_u32 s57, s57, 0
	s_mov_b32 m0, s64
	v_lshl_add_u64 v[238:239], s[56:57], 0, v[144:145]
	global_load_lds_dwordx4 v[238:239], off
	v_lshl_add_u64 v[238:239], s[56:57], 0, v[148:149]
	s_mov_b32 m0, s65
	s_nop 0
	global_load_lds_dwordx4 v[238:239], off
	v_add_u32_e32 v3, s82, v178
	ds_read_b128 v[138:141], v3
	ds_read_b128 v[162:165], v3 offset:1024
	ds_read_b128 v[166:169], v3 offset:2048
	ds_read_b128 v[170:173], v3 offset:3072
	v_add_u32_e32 v3, s83, v178
	ds_read_b128 v[186:189], v3
	ds_read_b128 v[190:193], v3 offset:1024
	ds_read_b128 v[194:197], v3 offset:2048
	ds_read_b128 v[198:201], v3 offset:3072
	ds_read_b128 v[202:205], v184 offset:32768
	ds_read_b128 v[206:209], v184 offset:33792
	ds_read_b128 v[210:213], v184 offset:34816
	ds_read_b128 v[214:217], v184 offset:35840
	ds_read_b128 v[218:221], v184 offset:36864
	ds_read_b128 v[222:225], v184 offset:37888
	ds_read_b128 v[226:229], v184 offset:38912
	ds_read_b128 v[230:233], v184 offset:39936
	s_waitcnt vmcnt(8)
	s_waitcnt lgkmcnt(0)
	s_barrier
	v_mfma_f32_16x16x32_bf16 v[128:131], v[138:141], v[202:205], v[128:131]
	v_mfma_f32_16x16x32_bf16 v[124:127], v[166:169], v[202:205], v[124:127]
	v_mfma_f32_16x16x32_bf16 v[120:123], v[138:141], v[210:213], v[120:123]
	v_mfma_f32_16x16x32_bf16 v[112:115], v[166:169], v[210:213], v[112:115]
	v_mfma_f32_16x16x32_bf16 v[96:99], v[138:141], v[218:221], v[96:99]
	v_mfma_f32_16x16x32_bf16 v[92:95], v[166:169], v[218:221], v[92:95]
	v_mfma_f32_16x16x32_bf16 v[80:83], v[138:141], v[226:229], v[80:83]
	v_mfma_f32_16x16x32_bf16 v[76:79], v[166:169], v[226:229], v[76:79]
	v_mfma_f32_16x16x32_bf16 v[128:131], v[162:165], v[206:209], v[128:131]
	v_mfma_f32_16x16x32_bf16 v[124:127], v[170:173], v[206:209], v[124:127]
	v_mfma_f32_16x16x32_bf16 v[120:123], v[162:165], v[214:217], v[120:123]
	v_mfma_f32_16x16x32_bf16 v[112:115], v[170:173], v[214:217], v[112:115]
	v_mfma_f32_16x16x32_bf16 v[96:99], v[162:165], v[222:225], v[96:99]
	v_mfma_f32_16x16x32_bf16 v[92:95], v[170:173], v[222:225], v[92:95]
	v_mfma_f32_16x16x32_bf16 v[80:83], v[162:165], v[230:233], v[80:83]
	v_mfma_f32_16x16x32_bf16 v[76:79], v[170:173], v[230:233], v[76:79]
	v_mfma_f32_16x16x32_bf16 v[116:119], v[186:189], v[202:205], v[116:119]
	v_mfma_f32_16x16x32_bf16 v[108:111], v[194:197], v[202:205], v[108:111]
	v_mfma_f32_16x16x32_bf16 v[104:107], v[186:189], v[210:213], v[104:107]
	v_mfma_f32_16x16x32_bf16 v[100:103], v[194:197], v[210:213], v[100:103]
	v_mfma_f32_16x16x32_bf16 v[88:91], v[186:189], v[218:221], v[88:91]
	v_mfma_f32_16x16x32_bf16 v[84:87], v[194:197], v[218:221], v[84:87]
	v_mfma_f32_16x16x32_bf16 v[72:75], v[186:189], v[226:229], v[72:75]
	v_mfma_f32_16x16x32_bf16 v[68:71], v[194:197], v[226:229], v[68:71]
	v_mfma_f32_16x16x32_bf16 v[116:119], v[190:193], v[206:209], v[116:119]
	v_mfma_f32_16x16x32_bf16 v[108:111], v[198:201], v[206:209], v[108:111]
	v_mfma_f32_16x16x32_bf16 v[104:107], v[190:193], v[214:217], v[104:107]
	v_mfma_f32_16x16x32_bf16 v[100:103], v[198:201], v[214:217], v[100:103]
	v_mfma_f32_16x16x32_bf16 v[88:91], v[190:193], v[222:225], v[88:91]
	v_mfma_f32_16x16x32_bf16 v[84:87], v[198:201], v[222:225], v[84:87]
	v_mfma_f32_16x16x32_bf16 v[72:75], v[190:193], v[230:233], v[72:75]
	v_mfma_f32_16x16x32_bf16 v[68:71], v[198:201], v[230:233], v[68:71]
	s_barrier
; #define PG8_STAGE(bufoff, gbase, voff) do { _Pragma("unroll") for (int _i = 0; _i < 2; ++_i) \
;         __builtin_amdgcn_global_load_lds((const unsigned*)((const char*)(gbase) + (voff)[_i]), (PG8_LAS unsigned*)(lds + (bufoff) + ldsw + _i * 8192), 16, 0, 0); } while (0)
; #define PG8_LDA(dst, b, h) do { _Pragma("unroll") for (int m = 0; m < 4; ++m) _Pragma("unroll") for (int k = 0; k < 2; ++k) dst[m][k] = *(const PG8_LAS bf16x8*)(lds + PG8_SA(b, h) + aoff + m * 2048 + k * 1024); } while (0)
; #define PG8_MMA(ai, bj, At, Bt) do { __builtin_amdgcn_s_setprio(1); _Pragma("unroll") for (int m = 0; m < 4; ++m) _Pragma("unroll") for (int n = 0; n < 2; ++n) _Pragma("unroll") for (int k = 0; k < 2; ++k) \
;         acc[ai][bj][m][n] = __builtin_amdgcn_mfma_f32_16x16x32_bf16(Bt[n][k], At[m][k], acc[ai][bj][m][n], 0, 0, 0); __builtin_amdgcn_s_setprio(0); } while (0)
; #define PG8_WAIT_V(n) asm volatile("s_waitcnt vmcnt(" #n ")" ::: "memory")
; #define PG8_WAIT_L(n) asm volatile("s_waitcnt lgkmcnt(" #n ")" ::: "memory")
; #define PG8_BAR __builtin_amdgcn_s_barrier()
; #define PG8_SCHED __builtin_amdgcn_sched_barrier(0)
; template <class Epi, class Sched, bool ALIGN_EPI = false>
; __device__ __forceinline__ void gemm_phase(PG8_LAS unsigned char* lds, const Gemm g, const Sched& S, const Epi& E) {
;     ...
;             PG8_LDA(At, 1, 1); PG8_STAGE(PG8_SB(1, 0), b3, voffB); PG8_STAGE(PG8_SB(1, 1), b3 + hstep, voffB); PG8_STAGE(PG8_SA(1, 0), a3, w0);
;             PG8_WAIT_V(8); PG8_WAIT_L(0); PG8_BAR; PG8_MMA(1, 0, At, B0); PG8_MMA(1, 1, At, B1); PG8_BAR; PG8_SCHED;
;             if constexpr (Epi::KSCALE) { if (((t + 2) & 7) == 0 && t + 2 < nt) { E.kscale(acc, pf, ((t + 2) >> 3) - 1, wr, fr); PG8_SCHED; } }
	s_add_i32 s56, s82, s61
	v_lshl_add_u64 v[142:143], v[142:143], 0, s[18:19]
	s_mov_b32 m0, s56
	s_nop 0
	global_load_lds_dwordx4 v[142:143], off
	s_add_i32 m0, s56, 0x2000
	s_add_u32 s54, s54, 0x80080
	v_lshl_add_u64 v[142:143], v[174:175], 0, s[18:19]
	s_addc_u32 s55, s55, 0
	s_add_i32 s56, s83, s61
	global_load_lds_dwordx4 v[142:143], off
	v_lshl_add_u64 v[142:143], s[54:55], 0, v[146:147]
	s_mov_b32 m0, s56
	s_nop 0
	global_load_lds_dwordx4 v[142:143], off
	v_lshl_add_u64 v[142:143], s[54:55], 0, v[150:151]
	s_add_i32 m0, s56, 0x2000
	s_nop 0
	global_load_lds_dwordx4 v[142:143], off
	v_lshl_add_u64 v[142:143], v[234:235], 0, s[18:19]
	s_mov_b32 m0, s68
	s_nop 0
	global_load_lds_dwordx4 v[142:143], off
	v_lshl_add_u64 v[142:143], v[236:237], 0, s[18:19]
	s_mov_b32 m0, s69
	s_nop 0
	global_load_lds_dwordx4 v[142:143], off
	ds_read_b128 v[202:205], v184 offset:49152
	ds_read_b128 v[206:209], v184 offset:50176
	ds_read_b128 v[210:213], v184 offset:51200
	ds_read_b128 v[214:217], v184 offset:52224
	ds_read_b128 v[218:221], v184 offset:53248
	ds_read_b128 v[222:225], v184 offset:54272
	ds_read_b128 v[226:229], v184 offset:55296
	ds_read_b128 v[230:233], v184 offset:56320
	s_waitcnt vmcnt(8)
	s_waitcnt lgkmcnt(0)
	s_barrier
	v_mfma_f32_16x16x32_bf16 v[64:67], v[138:141], v[202:205], v[64:67]
	v_mfma_f32_16x16x32_bf16 v[60:63], v[166:169], v[202:205], v[60:63]
	v_mfma_f32_16x16x32_bf16 v[48:51], v[138:141], v[210:213], v[48:51]
	v_mfma_f32_16x16x32_bf16 v[44:47], v[166:169], v[210:213], v[44:47]
	v_mfma_f32_16x16x32_bf16 v[32:35], v[138:141], v[218:221], v[32:35]
	v_mfma_f32_16x16x32_bf16 v[28:31], v[166:169], v[218:221], v[28:31]
	v_mfma_f32_16x16x32_bf16 v[16:19], v[138:141], v[226:229], v[16:19]
	v_mfma_f32_16x16x32_bf16 v[12:15], v[166:169], v[226:229], v[12:15]
	v_mfma_f32_16x16x32_bf16 v[64:67], v[162:165], v[206:209], v[64:67]
	v_mfma_f32_16x16x32_bf16 v[60:63], v[170:173], v[206:209], v[60:63]
	v_mfma_f32_16x16x32_bf16 v[48:51], v[162:165], v[214:217], v[48:51]
	v_mfma_f32_16x16x32_bf16 v[44:47], v[170:173], v[214:217], v[44:47]
	v_mfma_f32_16x16x32_bf16 v[32:35], v[162:165], v[222:225], v[32:35]
	v_mfma_f32_16x16x32_bf16 v[28:31], v[170:173], v[222:225], v[28:31]
	v_mfma_f32_16x16x32_bf16 v[16:19], v[162:165], v[230:233], v[16:19]
	v_mfma_f32_16x16x32_bf16 v[12:15], v[170:173], v[230:233], v[12:15]
	v_mfma_f32_16x16x32_bf16 v[56:59], v[186:189], v[202:205], v[56:59]
	v_mfma_f32_16x16x32_bf16 v[52:55], v[194:197], v[202:205], v[52:55]
	v_mfma_f32_16x16x32_bf16 v[40:43], v[186:189], v[210:213], v[40:43]
	v_mfma_f32_16x16x32_bf16 v[36:39], v[194:197], v[210:213], v[36:39]
	v_mfma_f32_16x16x32_bf16 v[24:27], v[186:189], v[218:221], v[24:27]
	v_mfma_f32_16x16x32_bf16 v[20:23], v[194:197], v[218:221], v[20:23]
	v_mfma_f32_16x16x32_bf16 v[8:11], v[186:189], v[226:229], v[8:11]
	v_mfma_f32_16x16x32_bf16 v[4:7], v[194:197], v[226:229], v[4:7]
	v_mfma_f32_16x16x32_bf16 v[56:59], v[190:193], v[206:209], v[56:59]
	v_mfma_f32_16x16x32_bf16 v[52:55], v[198:201], v[206:209], v[52:55]
	v_mfma_f32_16x16x32_bf16 v[40:43], v[190:193], v[214:217], v[40:43]
	v_mfma_f32_16x16x32_bf16 v[36:39], v[198:201], v[214:217], v[36:39]
	v_mfma_f32_16x16x32_bf16 v[24:27], v[190:193], v[222:225], v[24:27]
	v_mfma_f32_16x16x32_bf16 v[20:23], v[198:201], v[222:225], v[20:23]
	v_mfma_f32_16x16x32_bf16 v[8:11], v[190:193], v[230:233], v[8:11]
	v_mfma_f32_16x16x32_bf16 v[4:7], v[198:201], v[230:233], v[4:7]
	s_barrier
	s_mov_b32 s82, s81
	s_add_i32 s81, s81, 2
	s_and_b32 s54, s81, 6
	s_cmp_eq_u32 s54, 0
	s_cselect_b64 s[56:57], -1, 0
	s_cmp_gt_u32 s82, 29
	s_cselect_b64 s[54:55], -1, 0
	s_cmp_lt_u32 s82, 30
	s_cselect_b64 s[82:83], -1, 0
	s_and_b64 s[56:57], s[56:57], s[82:83]
	s_andn2_b64 vcc, exec, s[56:57]
	s_cbranch_vccnz .LBB0_503
; #define PG8_SCHED __builtin_amdgcn_sched_barrier(0)
;     __device__ __forceinline__ void kscale(f32x4 (&acc)[2][2][4][2], const Pre& pf, int b, int wr, int fr) const {
; #pragma unroll
;         for (int ai = 0; ai < 2; ++ai)
; #pragma unroll
;             for (int m = 0; m < 4; ++m) { const float f = pf.tab[(ai * HALF + wr * 64 + m * 16 + fr) * 4 + b];
; #pragma unroll
;                 for (int bj = 0; bj < 2; ++bj)
; #pragma unroll
;                     for (int n = 0; n < 2; ++n) acc[ai][bj][m][n] = acc[ai][bj][m][n] * f; }
;     }
; template <class Epi, class Sched, bool ALIGN_EPI = false>
; __device__ __forceinline__ void gemm_phase(PG8_LAS unsigned char* lds, const Gemm g, const Sched& S, const Epi& E) {
;     ...
;             if constexpr (Epi::KSCALE) { if (((t + 2) & 7) == 0 && t + 2 < nt) { E.kscale(acc, pf, ((t + 2) >> 3) - 1, wr, fr); PG8_SCHED; } }
	s_lshr_b32 s56, s81, 1
	v_add_u32_e32 v3, s56, v137
	v_add_u32_e32 v136, -4, v3
	ds_read_b32 v136, v136
	ds_read_b32 v138, v3 offset:2812
	ds_read2_b32 v[140:141], v3 offset0:63 offset1:127
	v_add_u32_e32 v3, 0xfc, v3
	s_waitcnt lgkmcnt(0)
	v_pk_mul_f32 v[130:131], v[130:131], v[136:137] op_sel_hi:[1,0]
	v_pk_mul_f32 v[128:129], v[128:129], v[136:137] op_sel_hi:[1,0]
	v_pk_mul_f32 v[126:127], v[126:127], v[136:137] op_sel_hi:[1,0]
	v_pk_mul_f32 v[124:125], v[124:125], v[136:137] op_sel_hi:[1,0]
	v_pk_mul_f32 v[118:119], v[118:119], v[136:137] op_sel_hi:[1,0]
	v_pk_mul_f32 v[116:117], v[116:117], v[136:137] op_sel_hi:[1,0]
	v_pk_mul_f32 v[110:111], v[110:111], v[136:137] op_sel_hi:[1,0]
	v_pk_mul_f32 v[108:109], v[108:109], v[136:137] op_sel_hi:[1,0]
	v_pk_mul_f32 v[122:123], v[122:123], v[140:141] op_sel_hi:[1,0]
	v_pk_mul_f32 v[120:121], v[120:121], v[140:141] op_sel_hi:[1,0]
	v_pk_mul_f32 v[114:115], v[114:115], v[140:141] op_sel_hi:[1,0]
	v_pk_mul_f32 v[112:113], v[112:113], v[140:141] op_sel_hi:[1,0]
	v_pk_mul_f32 v[106:107], v[106:107], v[140:141] op_sel_hi:[1,0]
	v_pk_mul_f32 v[104:105], v[104:105], v[140:141] op_sel_hi:[1,0]
	v_pk_mul_f32 v[102:103], v[102:103], v[140:141] op_sel_hi:[1,0]
	v_pk_mul_f32 v[100:101], v[100:101], v[140:141] op_sel_hi:[1,0]
	v_mov_b32_e32 v136, v141
	ds_read2st64_b32 v[140:141], v3 offset0:2 offset1:7
	v_pk_mul_f32 v[98:99], v[98:99], v[136:137] op_sel_hi:[1,0]
	v_pk_mul_f32 v[96:97], v[96:97], v[136:137] op_sel_hi:[1,0]
	v_pk_mul_f32 v[94:95], v[94:95], v[136:137] op_sel_hi:[1,0]
	v_pk_mul_f32 v[92:93], v[92:93], v[136:137] op_sel_hi:[1,0]
	v_pk_mul_f32 v[90:91], v[90:91], v[136:137] op_sel_hi:[1,0]
	v_pk_mul_f32 v[88:89], v[88:89], v[136:137] op_sel_hi:[1,0]
	v_pk_mul_f32 v[86:87], v[86:87], v[136:137] op_sel_hi:[1,0]
	v_pk_mul_f32 v[84:85], v[84:85], v[136:137] op_sel_hi:[1,0]
	s_waitcnt lgkmcnt(0)
	v_pk_mul_f32 v[82:83], v[82:83], v[140:141] op_sel_hi:[1,0]
	v_pk_mul_f32 v[80:81], v[80:81], v[140:141] op_sel_hi:[1,0]
	v_pk_mul_f32 v[78:79], v[78:79], v[140:141] op_sel_hi:[1,0]
	v_pk_mul_f32 v[76:77], v[76:77], v[140:141] op_sel_hi:[1,0]
	v_pk_mul_f32 v[74:75], v[74:75], v[140:141] op_sel_hi:[1,0]
	v_pk_mul_f32 v[72:73], v[72:73], v[140:141] op_sel_hi:[1,0]
	v_pk_mul_f32 v[70:71], v[70:71], v[140:141] op_sel_hi:[1,0]
	v_pk_mul_f32 v[68:69], v[68:69], v[140:141] op_sel_hi:[1,0]
	v_mov_b32_e32 v136, v141
	ds_read2st64_b32 v[140:141], v3 offset0:8 offset1:9
	v_pk_mul_f32 v[66:67], v[66:67], v[136:137] op_sel_hi:[1,0]
	v_pk_mul_f32 v[64:65], v[64:65], v[136:137] op_sel_hi:[1,0]
	v_pk_mul_f32 v[62:63], v[62:63], v[136:137] op_sel_hi:[1,0]
	v_pk_mul_f32 v[60:61], v[60:61], v[136:137] op_sel_hi:[1,0]
	v_pk_mul_f32 v[58:59], v[58:59], v[136:137] op_sel_hi:[1,0]
	v_pk_mul_f32 v[56:57], v[56:57], v[136:137] op_sel_hi:[1,0]
	v_pk_mul_f32 v[54:55], v[54:55], v[136:137] op_sel_hi:[1,0]
	v_pk_mul_f32 v[52:53], v[52:53], v[136:137] op_sel_hi:[1,0]
	s_waitcnt lgkmcnt(0)
	v_mov_b32_e32 v136, v141
	v_pk_mul_f32 v[50:51], v[50:51], v[140:141] op_sel_hi:[1,0]
	v_pk_mul_f32 v[48:49], v[48:49], v[140:141] op_sel_hi:[1,0]
	v_pk_mul_f32 v[46:47], v[46:47], v[140:141] op_sel_hi:[1,0]
	v_pk_mul_f32 v[44:45], v[44:45], v[140:141] op_sel_hi:[1,0]
	v_pk_mul_f32 v[42:43], v[42:43], v[140:141] op_sel_hi:[1,0]
	v_pk_mul_f32 v[40:41], v[40:41], v[140:141] op_sel_hi:[1,0]
	v_pk_mul_f32 v[38:39], v[38:39], v[140:141] op_sel_hi:[1,0]
	v_pk_mul_f32 v[36:37], v[36:37], v[140:141] op_sel_hi:[1,0]
	v_pk_mul_f32 v[34:35], v[34:35], v[136:137] op_sel_hi:[1,0]
	v_pk_mul_f32 v[32:33], v[32:33], v[136:137] op_sel_hi:[1,0]
	v_pk_mul_f32 v[30:31], v[30:31], v[136:137] op_sel_hi:[1,0]
	v_pk_mul_f32 v[28:29], v[28:29], v[136:137] op_sel_hi:[1,0]
	v_pk_mul_f32 v[26:27], v[26:27], v[136:137] op_sel_hi:[1,0]
	v_pk_mul_f32 v[24:25], v[24:25], v[136:137] op_sel_hi:[1,0]
	v_pk_mul_f32 v[22:23], v[22:23], v[136:137] op_sel_hi:[1,0]
	v_pk_mul_f32 v[20:21], v[20:21], v[136:137] op_sel_hi:[1,0]
	v_pk_mul_f32 v[18:19], v[18:19], v[138:139] op_sel_hi:[1,0]
	v_pk_mul_f32 v[16:17], v[16:17], v[138:139] op_sel_hi:[1,0]
	v_pk_mul_f32 v[14:15], v[14:15], v[138:139] op_sel_hi:[1,0]
	v_pk_mul_f32 v[12:13], v[12:13], v[138:139] op_sel_hi:[1,0]
	v_pk_mul_f32 v[10:11], v[10:11], v[138:139] op_sel_hi:[1,0]
	v_pk_mul_f32 v[8:9], v[8:9], v[138:139] op_sel_hi:[1,0]
	v_pk_mul_f32 v[6:7], v[6:7], v[138:139] op_sel_hi:[1,0]
	v_pk_mul_f32 v[4:5], v[4:5], v[138:139] op_sel_hi:[1,0]
	s_branch .LBB0_503

; #define PG8_STAGE(bufoff, gbase, voff) do { _Pragma("unroll") for (int _i = 0; _i < 2; ++_i) \
;         __builtin_amdgcn_global_load_lds((const unsigned*)((const char*)(gbase) + (voff)[_i]), (PG8_LAS unsigned*)(lds + (bufoff) + ldsw + _i * 8192), 16, 0, 0); } while (0)
; #define PG8_LDA(dst, b, h) do { _Pragma("unroll") for (int m = 0; m < 4; ++m) _Pragma("unroll") for (int k = 0; k < 2; ++k) dst[m][k] = *(const PG8_LAS bf16x8*)(lds + PG8_SA(b, h) + aoff + m * 2048 + k * 1024); } while (0)
; #define PG8_LDB(dst, b, h) do { _Pragma("unroll") for (int n = 0; n < 2; ++n) _Pragma("unroll") for (int k = 0; k < 2; ++k) dst[n][k] = *(const PG8_LAS bf16x8*)(lds + PG8_SB(b, h) + boff + n * 2048 + k * 1024); } while (0)
; #define PG8_MMA(ai, bj, At, Bt) do { __builtin_amdgcn_s_setprio(1); _Pragma("unroll") for (int m = 0; m < 4; ++m) _Pragma("unroll") for (int n = 0; n < 2; ++n) _Pragma("unroll") for (int k = 0; k < 2; ++k) \
;         acc[ai][bj][m][n] = __builtin_amdgcn_mfma_f32_16x16x32_bf16(Bt[n][k], At[m][k], acc[ai][bj][m][n], 0, 0, 0); __builtin_amdgcn_s_setprio(0); } while (0)
; #define PG8_BAR __builtin_amdgcn_s_barrier()
; template <class Epi, class Sched, bool ALIGN_EPI = false>
; __device__ __forceinline__ void gemm_phase(PG8_LAS unsigned char* lds, const Gemm g, const Sched& S, const Epi& E) {
;     ...
;             const bool last = (t == nt - 2);
;             const char* a1 = cA + (size_t)(t + 1) * kstep;
;             const char* a2 = last ? nA : cA + (size_t)(t + 2) * kstep; const char* b2 = last ? nB : cB + (size_t)(t + 2) * kstep;
;             const char* a3 = a2 + kstep; const char* b3 = b2 + kstep;
;             unsigned w0[2], w1[2];
; #pragma unroll
;             for (int i = 0; i < 2; ++i) { w0[i] = (Sched::GATHER && last) ? vn0[i] : vc0[i]; w1[i] = (Sched::GATHER && last) ? vn1[i] : vc1[i]; }
;             if (last && has_next) S.a_ready(nxt);
;             PG8_LDB(B0, 0, 0); PG8_LDB(B1, 0, 1); PG8_SCHED; PG8_LDA(At, 0, 0); PG8_STAGE(PG8_SA(1, 1), a1 + hstepA, vc1);
;             PG8_WAIT_V(8); PG8_WAIT_L(0); PG8_BAR; PG8_MMA(0, 0, At, B0); PG8_MMA(0, 1, At, B1); PG8_BAR; PG8_SCHED;
;             PG8_LDA(At, 0, 1); PG8_STAGE(PG8_SB(0, 0), b2, voffB); PG8_STAGE(PG8_SB(0, 1), b2 + hstep, voffB); PG8_STAGE(PG8_SA(0, 0), a2, w0);
;             PG8_WAIT_V(8); PG8_WAIT_L(0); PG8_BAR; PG8_MMA(1, 0, At, B0); PG8_MMA(1, 1, At, B1); PG8_BAR; PG8_SCHED;
.LBB0_721:
	s_add_u32 s58, s36, s56
	v_add_u32_e32 v155, s82, v143
	s_addc_u32 s59, s37, s57
	ds_read_b128 v[164:167], v155
	ds_read_b128 v[168:171], v155 offset:1024
	ds_read_b128 v[172:175], v155 offset:2048
	ds_read_b128 v[176:179], v155 offset:3072
	v_add_u32_e32 v155, s83, v143
	s_add_u32 s60, s58, 0x3c800100
	ds_read_b128 v[180:183], v155
	ds_read_b128 v[184:187], v155 offset:1024
	ds_read_b128 v[188:191], v155 offset:2048
	ds_read_b128 v[192:195], v155 offset:3072
	s_addc_u32 s61, s59, 0
	s_add_u32 s91, s49, s56
	s_addc_u32 s92, s89, s57
	s_cmpk_eq_i32 s56, 0xf00
	s_cselect_b64 vcc, -1, 0
	s_and_b64 s[58:59], vcc, exec
	v_cndmask_b32_e32 v134, v151, v149, vcc
	s_cselect_b32 s61, s21, s61
	s_cselect_b32 s60, s20, s60
	v_cndmask_b32_e32 v153, v152, v157, vcc
	v_cndmask_b32_e32 v228, v150, v162, vcc
	v_cndmask_b32_e32 v155, v154, v163, vcc
	s_cselect_b32 s59, s53, s92
	s_cselect_b32 s58, s52, s91
	v_lshl_add_u64 v[230:231], v[160:161], 0, s[56:57]
	s_add_i32 m0, s55, 0xc000
	ds_read_b128 v[196:199], v147
	ds_read_b128 v[200:203], v147 offset:1024
	ds_read_b128 v[204:207], v147 offset:2048
	ds_read_b128 v[208:211], v147 offset:3072
	ds_read_b128 v[212:215], v147 offset:4096
	ds_read_b128 v[216:219], v147 offset:5120
	ds_read_b128 v[220:223], v147 offset:6144
	ds_read_b128 v[224:227], v147 offset:7168
	global_load_lds_dwordx4 v[230:231], off
	v_lshl_add_u64 v[230:231], v[158:159], 0, s[56:57]
	s_add_i32 m0, s55, 0xe000
	s_nop 0
	global_load_lds_dwordx4 v[230:231], off
	s_waitcnt vmcnt(8)
	s_waitcnt lgkmcnt(0)
	s_barrier
	v_mfma_f32_16x16x32_bf16 v[126:129], v[164:167], v[196:199], v[126:129]
	v_mfma_f32_16x16x32_bf16 v[122:125], v[172:175], v[196:199], v[122:125]
	v_mfma_f32_16x16x32_bf16 v[110:113], v[164:167], v[204:207], v[110:113]
	v_mfma_f32_16x16x32_bf16 v[106:109], v[172:175], v[204:207], v[106:109]
	v_mfma_f32_16x16x32_bf16 v[94:97], v[164:167], v[212:215], v[94:97]
	v_mfma_f32_16x16x32_bf16 v[90:93], v[172:175], v[212:215], v[90:93]
	v_mfma_f32_16x16x32_bf16 v[78:81], v[164:167], v[220:223], v[78:81]
	v_mfma_f32_16x16x32_bf16 v[74:77], v[172:175], v[220:223], v[74:77]
	v_mfma_f32_16x16x32_bf16 v[126:129], v[168:171], v[200:203], v[126:129]
	v_mfma_f32_16x16x32_bf16 v[122:125], v[176:179], v[200:203], v[122:125]
	v_mfma_f32_16x16x32_bf16 v[110:113], v[168:171], v[208:211], v[110:113]
	v_mfma_f32_16x16x32_bf16 v[106:109], v[176:179], v[208:211], v[106:109]
	v_mfma_f32_16x16x32_bf16 v[94:97], v[168:171], v[216:219], v[94:97]
	v_mfma_f32_16x16x32_bf16 v[90:93], v[176:179], v[216:219], v[90:93]
	v_mfma_f32_16x16x32_bf16 v[78:81], v[168:171], v[224:227], v[78:81]
	v_mfma_f32_16x16x32_bf16 v[74:77], v[176:179], v[224:227], v[74:77]
	v_mfma_f32_16x16x32_bf16 v[118:121], v[180:183], v[196:199], v[118:121]
	v_mfma_f32_16x16x32_bf16 v[114:117], v[188:191], v[196:199], v[114:117]
	v_mfma_f32_16x16x32_bf16 v[102:105], v[180:183], v[204:207], v[102:105]
	v_mfma_f32_16x16x32_bf16 v[98:101], v[188:191], v[204:207], v[98:101]
	v_mfma_f32_16x16x32_bf16 v[86:89], v[180:183], v[212:215], v[86:89]
	v_mfma_f32_16x16x32_bf16 v[82:85], v[188:191], v[212:215], v[82:85]
	v_mfma_f32_16x16x32_bf16 v[70:73], v[180:183], v[220:223], v[70:73]
	v_mfma_f32_16x16x32_bf16 v[66:69], v[188:191], v[220:223], v[66:69]
	v_mfma_f32_16x16x32_bf16 v[118:121], v[184:187], v[200:203], v[118:121]
	v_mfma_f32_16x16x32_bf16 v[114:117], v[192:195], v[200:203], v[114:117]
	v_mfma_f32_16x16x32_bf16 v[102:105], v[184:187], v[208:211], v[102:105]
	v_mfma_f32_16x16x32_bf16 v[98:101], v[192:195], v[208:211], v[98:101]
	v_mfma_f32_16x16x32_bf16 v[86:89], v[184:187], v[216:219], v[86:89]
	v_mfma_f32_16x16x32_bf16 v[82:85], v[192:195], v[216:219], v[82:85]
	v_mfma_f32_16x16x32_bf16 v[70:73], v[184:187], v[224:227], v[70:73]
	v_mfma_f32_16x16x32_bf16 v[66:69], v[192:195], v[224:227], v[66:69]
	s_barrier
	s_add_i32 s91, s82, s74
	v_lshl_add_u64 v[230:231], s[58:59], 0, v[130:131]
	s_mov_b32 m0, s91
	s_nop 0
	global_load_lds_dwordx4 v[230:231], off
	s_add_i32 m0, s91, 0x2000
	s_add_u32 s92, s58, 0x80000
	v_lshl_add_u64 v[232:233], s[58:59], 0, v[132:133]
	s_addc_u32 s93, s59, 0
	s_add_i32 s91, s83, s74
	global_load_lds_dwordx4 v[232:233], off
	v_lshl_add_u64 v[234:235], s[92:93], 0, v[130:131]
	s_mov_b32 m0, s91
	v_mov_b32_e32 v229, v135
	global_load_lds_dwordx4 v[234:235], off
	v_lshl_add_u64 v[234:235], s[92:93], 0, v[132:133]
	s_add_i32 m0, s91, 0x2000
	s_nop 0
	global_load_lds_dwordx4 v[234:235], off
	s_mov_b32 m0, s55
	v_lshl_add_u64 v[234:235], s[60:61], 0, v[134:135]
	global_load_lds_dwordx4 v134, s[60:61]
	s_mov_b32 m0, s75
	s_nop 0
	global_load_lds_dwordx4 v228, s[60:61]
	ds_read_b128 v[196:199], v147 offset:16384
	ds_read_b128 v[200:203], v147 offset:17408
	ds_read_b128 v[204:207], v147 offset:18432
	ds_read_b128 v[208:211], v147 offset:19456
	ds_read_b128 v[212:215], v147 offset:20480
	ds_read_b128 v[216:219], v147 offset:21504
	ds_read_b128 v[220:223], v147 offset:22528
	ds_read_b128 v[224:227], v147 offset:23552
	s_waitcnt vmcnt(8)
	s_waitcnt lgkmcnt(0)
	v_lshl_add_u64 v[228:229], s[60:61], 0, v[228:229]
	s_barrier
; #define PG8_STAGE(bufoff, gbase, voff) do { _Pragma("unroll") for (int _i = 0; _i < 2; ++_i) \
;         __builtin_amdgcn_global_load_lds((const unsigned*)((const char*)(gbase) + (voff)[_i]), (PG8_LAS unsigned*)(lds + (bufoff) + ldsw + _i * 8192), 16, 0, 0); } while (0)
; #define PG8_LDA(dst, b, h) do { _Pragma("unroll") for (int m = 0; m < 4; ++m) _Pragma("unroll") for (int k = 0; k < 2; ++k) dst[m][k] = *(const PG8_LAS bf16x8*)(lds + PG8_SA(b, h) + aoff + m * 2048 + k * 1024); } while (0)
; #define PG8_LDB(dst, b, h) do { _Pragma("unroll") for (int n = 0; n < 2; ++n) _Pragma("unroll") for (int k = 0; k < 2; ++k) dst[n][k] = *(const PG8_LAS bf16x8*)(lds + PG8_SB(b, h) + boff + n * 2048 + k * 1024); } while (0)
; #define PG8_MMA(ai, bj, At, Bt) do { __builtin_amdgcn_s_setprio(1); _Pragma("unroll") for (int m = 0; m < 4; ++m) _Pragma("unroll") for (int n = 0; n < 2; ++n) _Pragma("unroll") for (int k = 0; k < 2; ++k) \
;         acc[ai][bj][m][n] = __builtin_amdgcn_mfma_f32_16x16x32_bf16(Bt[n][k], At[m][k], acc[ai][bj][m][n], 0, 0, 0); __builtin_amdgcn_s_setprio(0); } while (0)
; #define PG8_WAIT_V(n) asm volatile("s_waitcnt vmcnt(" #n ")" ::: "memory")
; #define PG8_WAIT_L(n) asm volatile("s_waitcnt lgkmcnt(" #n ")" ::: "memory")
; #define PG8_BAR __builtin_amdgcn_s_barrier()
; #define PG8_SCHED __builtin_amdgcn_sched_barrier(0)
; template <class Epi, class Sched, bool ALIGN_EPI = false>
; __device__ __forceinline__ void gemm_phase(PG8_LAS unsigned char* lds, const Gemm g, const Sched& S, const Epi& E) {
;     ...
;             PG8_WAIT_V(8); PG8_WAIT_L(0); PG8_BAR; PG8_MMA(1, 0, At, B0); PG8_MMA(1, 1, At, B1); PG8_BAR; PG8_SCHED;
;             PG8_LDB(B0, 1, 0); PG8_LDB(B1, 1, 1); PG8_SCHED; PG8_LDA(At, 1, 0); PG8_STAGE(PG8_SA(0, 1), a2 + hstepA, w1);
;             PG8_WAIT_V(8); PG8_WAIT_L(0); PG8_BAR; PG8_MMA(0, 0, At, B0); PG8_MMA(0, 1, At, B1); PG8_BAR; PG8_SCHED;
	v_mfma_f32_16x16x32_bf16 v[62:65], v[164:167], v[196:199], v[62:65]
	v_mfma_f32_16x16x32_bf16 v[58:61], v[172:175], v[196:199], v[58:61]
	v_mfma_f32_16x16x32_bf16 v[50:53], v[164:167], v[204:207], v[50:53]
	v_mfma_f32_16x16x32_bf16 v[42:45], v[172:175], v[204:207], v[42:45]
	v_mfma_f32_16x16x32_bf16 v[34:37], v[164:167], v[212:215], v[34:37]
	v_mfma_f32_16x16x32_bf16 v[30:33], v[172:175], v[212:215], v[30:33]
	v_mfma_f32_16x16x32_bf16 v[14:17], v[164:167], v[220:223], v[14:17]
	v_mfma_f32_16x16x32_bf16 v[2:5], v[172:175], v[220:223], v[2:5]
	v_mfma_f32_16x16x32_bf16 v[62:65], v[168:171], v[200:203], v[62:65]
	v_mfma_f32_16x16x32_bf16 v[58:61], v[176:179], v[200:203], v[58:61]
	v_mfma_f32_16x16x32_bf16 v[50:53], v[168:171], v[208:211], v[50:53]
	v_mfma_f32_16x16x32_bf16 v[42:45], v[176:179], v[208:211], v[42:45]
	v_mfma_f32_16x16x32_bf16 v[34:37], v[168:171], v[216:219], v[34:37]
	v_mfma_f32_16x16x32_bf16 v[30:33], v[176:179], v[216:219], v[30:33]
	v_mfma_f32_16x16x32_bf16 v[14:17], v[168:171], v[224:227], v[14:17]
	v_mfma_f32_16x16x32_bf16 v[2:5], v[176:179], v[224:227], v[2:5]
	v_mfma_f32_16x16x32_bf16 v[54:57], v[180:183], v[196:199], v[54:57]
	v_mfma_f32_16x16x32_bf16 v[46:49], v[188:191], v[196:199], v[46:49]
	v_mfma_f32_16x16x32_bf16 v[38:41], v[180:183], v[204:207], v[38:41]
	v_mfma_f32_16x16x32_bf16 v[26:29], v[188:191], v[204:207], v[26:29]
	v_mfma_f32_16x16x32_bf16 v[22:25], v[180:183], v[212:215], v[22:25]
	v_mfma_f32_16x16x32_bf16 v[18:21], v[188:191], v[212:215], v[18:21]
	v_mfma_f32_16x16x32_bf16 v[10:13], v[180:183], v[220:223], v[10:13]
	v_mfma_f32_16x16x32_bf16 v[6:9], v[188:191], v[220:223], v[6:9]
	v_mfma_f32_16x16x32_bf16 v[54:57], v[184:187], v[200:203], v[54:57]
	v_mfma_f32_16x16x32_bf16 v[46:49], v[192:195], v[200:203], v[46:49]
	v_mfma_f32_16x16x32_bf16 v[38:41], v[184:187], v[208:211], v[38:41]
	v_mfma_f32_16x16x32_bf16 v[26:29], v[192:195], v[208:211], v[26:29]
	v_mfma_f32_16x16x32_bf16 v[22:25], v[184:187], v[216:219], v[22:25]
	v_mfma_f32_16x16x32_bf16 v[18:21], v[192:195], v[216:219], v[18:21]
	v_mfma_f32_16x16x32_bf16 v[10:13], v[184:187], v[224:227], v[10:13]
	v_mfma_f32_16x16x32_bf16 v[6:9], v[192:195], v[224:227], v[6:9]
	s_barrier
	s_add_i32 s91, 0, 0x18000
	s_add_i32 s92, 0, 0x1c000
	s_mov_b32 m0, s76
	s_nop 0
	global_load_lds_dwordx4 v153, s[60:61]
	s_mov_b32 m0, s77
	s_nop 0
	global_load_lds_dwordx4 v155, s[60:61]
	v_add_u32_e32 v134, s91, v143
	ds_read_b128 v[164:167], v134
	ds_read_b128 v[168:171], v134 offset:1024
	ds_read_b128 v[172:175], v134 offset:2048
	ds_read_b128 v[176:179], v134 offset:3072
	v_add_u32_e32 v134, s92, v143
	ds_read_b128 v[180:183], v134
	ds_read_b128 v[184:187], v134 offset:1024
	ds_read_b128 v[188:191], v134 offset:2048
	ds_read_b128 v[192:195], v134 offset:3072
	ds_read_b128 v[196:199], v147 offset:32768
	ds_read_b128 v[200:203], v147 offset:33792
	ds_read_b128 v[204:207], v147 offset:34816
	ds_read_b128 v[208:211], v147 offset:35840
	ds_read_b128 v[212:215], v147 offset:36864
	ds_read_b128 v[216:219], v147 offset:37888
	ds_read_b128 v[220:223], v147 offset:38912
	ds_read_b128 v[224:227], v147 offset:39936
	s_waitcnt vmcnt(8)
	s_waitcnt lgkmcnt(0)
	s_barrier
	v_mfma_f32_16x16x32_bf16 v[126:129], v[164:167], v[196:199], v[126:129]
	v_mfma_f32_16x16x32_bf16 v[122:125], v[172:175], v[196:199], v[122:125]
	v_mfma_f32_16x16x32_bf16 v[110:113], v[164:167], v[204:207], v[110:113]
	v_mfma_f32_16x16x32_bf16 v[106:109], v[172:175], v[204:207], v[106:109]
	v_mfma_f32_16x16x32_bf16 v[94:97], v[164:167], v[212:215], v[94:97]
	v_mfma_f32_16x16x32_bf16 v[90:93], v[172:175], v[212:215], v[90:93]
	v_mfma_f32_16x16x32_bf16 v[78:81], v[164:167], v[220:223], v[78:81]
	v_mfma_f32_16x16x32_bf16 v[74:77], v[172:175], v[220:223], v[74:77]
	v_mfma_f32_16x16x32_bf16 v[126:129], v[168:171], v[200:203], v[126:129]
	v_mfma_f32_16x16x32_bf16 v[122:125], v[176:179], v[200:203], v[122:125]
	v_mfma_f32_16x16x32_bf16 v[110:113], v[168:171], v[208:211], v[110:113]
	v_mfma_f32_16x16x32_bf16 v[106:109], v[176:179], v[208:211], v[106:109]
	v_mfma_f32_16x16x32_bf16 v[94:97], v[168:171], v[216:219], v[94:97]
	v_mfma_f32_16x16x32_bf16 v[90:93], v[176:179], v[216:219], v[90:93]
	v_mfma_f32_16x16x32_bf16 v[78:81], v[168:171], v[224:227], v[78:81]
	v_mfma_f32_16x16x32_bf16 v[74:77], v[176:179], v[224:227], v[74:77]
	v_mfma_f32_16x16x32_bf16 v[118:121], v[180:183], v[196:199], v[118:121]
	v_mfma_f32_16x16x32_bf16 v[114:117], v[188:191], v[196:199], v[114:117]
	v_mfma_f32_16x16x32_bf16 v[102:105], v[180:183], v[204:207], v[102:105]
	v_mfma_f32_16x16x32_bf16 v[98:101], v[188:191], v[204:207], v[98:101]
	v_mfma_f32_16x16x32_bf16 v[86:89], v[180:183], v[212:215], v[86:89]
	v_mfma_f32_16x16x32_bf16 v[82:85], v[188:191], v[212:215], v[82:85]
	v_mfma_f32_16x16x32_bf16 v[70:73], v[180:183], v[220:223], v[70:73]
	v_mfma_f32_16x16x32_bf16 v[66:69], v[188:191], v[220:223], v[66:69]
	v_mfma_f32_16x16x32_bf16 v[118:121], v[184:187], v[200:203], v[118:121]
	v_mfma_f32_16x16x32_bf16 v[114:117], v[192:195], v[200:203], v[114:117]
	v_mfma_f32_16x16x32_bf16 v[102:105], v[184:187], v[208:211], v[102:105]
	v_mfma_f32_16x16x32_bf16 v[98:101], v[192:195], v[208:211], v[98:101]
	v_mfma_f32_16x16x32_bf16 v[86:89], v[184:187], v[216:219], v[86:89]
	v_mfma_f32_16x16x32_bf16 v[82:85], v[192:195], v[216:219], v[82:85]
	v_mfma_f32_16x16x32_bf16 v[70:73], v[184:187], v[224:227], v[70:73]
	v_mfma_f32_16x16x32_bf16 v[66:69], v[192:195], v[224:227], v[66:69]
	s_barrier
; #define PG8_STAGE(bufoff, gbase, voff) do { _Pragma("unroll") for (int _i = 0; _i < 2; ++_i) \
;         __builtin_amdgcn_global_load_lds((const unsigned*)((const char*)(gbase) + (voff)[_i]), (PG8_LAS unsigned*)(lds + (bufoff) + ldsw + _i * 8192), 16, 0, 0); } while (0)
; #define PG8_LDA(dst, b, h) do { _Pragma("unroll") for (int m = 0; m < 4; ++m) _Pragma("unroll") for (int k = 0; k < 2; ++k) dst[m][k] = *(const PG8_LAS bf16x8*)(lds + PG8_SA(b, h) + aoff + m * 2048 + k * 1024); } while (0)
; #define PG8_MMA(ai, bj, At, Bt) do { __builtin_amdgcn_s_setprio(1); _Pragma("unroll") for (int m = 0; m < 4; ++m) _Pragma("unroll") for (int n = 0; n < 2; ++n) _Pragma("unroll") for (int k = 0; k < 2; ++k) \
;         acc[ai][bj][m][n] = __builtin_amdgcn_mfma_f32_16x16x32_bf16(Bt[n][k], At[m][k], acc[ai][bj][m][n], 0, 0, 0); __builtin_amdgcn_s_setprio(0); } while (0)
; #define PG8_WAIT_V(n) asm volatile("s_waitcnt vmcnt(" #n ")" ::: "memory")
; #define PG8_WAIT_L(n) asm volatile("s_waitcnt lgkmcnt(" #n ")" ::: "memory")
; #define PG8_BAR __builtin_amdgcn_s_barrier()
; #define PG8_SCHED __builtin_amdgcn_sched_barrier(0)
; template <class Epi, class Sched, bool ALIGN_EPI = false>
; __device__ __forceinline__ void gemm_phase(PG8_LAS unsigned char* lds, const Gemm g, const Sched& S, const Epi& E) {
;     ...
;             PG8_LDA(At, 1, 1); PG8_STAGE(PG8_SB(1, 0), b3, voffB); PG8_STAGE(PG8_SB(1, 1), b3 + hstep, voffB); PG8_STAGE(PG8_SA(1, 0), a3, w0);
;             PG8_WAIT_V(8); PG8_WAIT_L(0); PG8_BAR; PG8_MMA(1, 0, At, B0); PG8_MMA(1, 1, At, B1); PG8_BAR; PG8_SCHED;
;             if constexpr (Epi::KSCALE) { if (((t + 2) & 7) == 0 && t + 2 < nt) { E.kscale(acc, pf, ((t + 2) >> 3) - 1, wr, fr); PG8_SCHED; } }
;         }
	s_add_i32 s60, s91, s74
	v_lshl_add_u64 v[230:231], v[230:231], 0, s[44:45]
	s_mov_b32 m0, s60
	s_nop 0
	global_load_lds_dwordx4 v[230:231], off
	s_add_i32 m0, s60, 0x2000
	s_add_u32 s58, s58, 0x80080
	v_lshl_add_u64 v[230:231], v[232:233], 0, s[44:45]
	s_addc_u32 s59, s59, 0
	s_add_i32 s60, s92, s74
	global_load_lds_dwordx4 v[230:231], off
	v_lshl_add_u64 v[230:231], s[58:59], 0, v[130:131]
	s_mov_b32 m0, s60
	v_lshl_add_u64 v[228:229], v[228:229], 0, s[44:45]
	global_load_lds_dwordx4 v[230:231], off
	v_lshl_add_u64 v[230:231], s[58:59], 0, v[132:133]
	s_add_i32 m0, s60, 0x2000
	s_nop 0
	global_load_lds_dwordx4 v[230:231], off
	v_lshl_add_u64 v[230:231], v[234:235], 0, s[44:45]
	s_mov_b32 m0, s80
	s_nop 0
	global_load_lds_dwordx4 v[230:231], off
	s_mov_b32 m0, s81
	s_nop 0
	global_load_lds_dwordx4 v[228:229], off
	ds_read_b128 v[196:199], v147 offset:49152
	ds_read_b128 v[200:203], v147 offset:50176
	ds_read_b128 v[204:207], v147 offset:51200
	ds_read_b128 v[208:211], v147 offset:52224
	ds_read_b128 v[212:215], v147 offset:53248
	ds_read_b128 v[216:219], v147 offset:54272
	ds_read_b128 v[220:223], v147 offset:55296
	ds_read_b128 v[224:227], v147 offset:56320
	s_waitcnt vmcnt(8)
	s_waitcnt lgkmcnt(0)
	s_barrier
	v_mfma_f32_16x16x32_bf16 v[62:65], v[164:167], v[196:199], v[62:65]
	v_mfma_f32_16x16x32_bf16 v[58:61], v[172:175], v[196:199], v[58:61]
	v_mfma_f32_16x16x32_bf16 v[50:53], v[164:167], v[204:207], v[50:53]
	v_mfma_f32_16x16x32_bf16 v[42:45], v[172:175], v[204:207], v[42:45]
	v_mfma_f32_16x16x32_bf16 v[34:37], v[164:167], v[212:215], v[34:37]
	v_mfma_f32_16x16x32_bf16 v[30:33], v[172:175], v[212:215], v[30:33]
	v_mfma_f32_16x16x32_bf16 v[14:17], v[164:167], v[220:223], v[14:17]
	v_mfma_f32_16x16x32_bf16 v[2:5], v[172:175], v[220:223], v[2:5]
	v_mfma_f32_16x16x32_bf16 v[62:65], v[168:171], v[200:203], v[62:65]
	v_mfma_f32_16x16x32_bf16 v[58:61], v[176:179], v[200:203], v[58:61]
	v_mfma_f32_16x16x32_bf16 v[50:53], v[168:171], v[208:211], v[50:53]
	v_mfma_f32_16x16x32_bf16 v[42:45], v[176:179], v[208:211], v[42:45]
	v_mfma_f32_16x16x32_bf16 v[34:37], v[168:171], v[216:219], v[34:37]
	v_mfma_f32_16x16x32_bf16 v[30:33], v[176:179], v[216:219], v[30:33]
	v_mfma_f32_16x16x32_bf16 v[14:17], v[168:171], v[224:227], v[14:17]
	v_mfma_f32_16x16x32_bf16 v[2:5], v[176:179], v[224:227], v[2:5]
	v_mfma_f32_16x16x32_bf16 v[54:57], v[180:183], v[196:199], v[54:57]
	v_mfma_f32_16x16x32_bf16 v[46:49], v[188:191], v[196:199], v[46:49]
	v_mfma_f32_16x16x32_bf16 v[38:41], v[180:183], v[204:207], v[38:41]
	v_mfma_f32_16x16x32_bf16 v[26:29], v[188:191], v[204:207], v[26:29]
	v_mfma_f32_16x16x32_bf16 v[22:25], v[180:183], v[212:215], v[22:25]
	v_mfma_f32_16x16x32_bf16 v[18:21], v[188:191], v[212:215], v[18:21]
	v_mfma_f32_16x16x32_bf16 v[10:13], v[180:183], v[220:223], v[10:13]
	v_mfma_f32_16x16x32_bf16 v[6:9], v[188:191], v[220:223], v[6:9]
	v_mfma_f32_16x16x32_bf16 v[54:57], v[184:187], v[200:203], v[54:57]
	v_mfma_f32_16x16x32_bf16 v[46:49], v[192:195], v[200:203], v[46:49]
	v_mfma_f32_16x16x32_bf16 v[38:41], v[184:187], v[208:211], v[38:41]
	v_mfma_f32_16x16x32_bf16 v[26:29], v[192:195], v[208:211], v[26:29]
	v_mfma_f32_16x16x32_bf16 v[22:25], v[184:187], v[216:219], v[22:25]
	v_mfma_f32_16x16x32_bf16 v[18:21], v[192:195], v[216:219], v[18:21]
	v_mfma_f32_16x16x32_bf16 v[10:13], v[184:187], v[224:227], v[10:13]
	v_mfma_f32_16x16x32_bf16 v[6:9], v[192:195], v[224:227], v[6:9]
	s_barrier
	s_add_i32 s90, s90, 2
	s_add_u32 s56, s56, 0x100
	s_addc_u32 s57, s57, 0
	s_cmp_gt_u32 s90, 29
	s_cbranch_scc0 .LBB0_721
	s_and_b64 vcc, exec, s[46:47]
	s_cbranch_vccz .LBB0_724
	s_barrier

; #define PG8_STAGE(bufoff, gbase, voff) do { _Pragma("unroll") for (int _i = 0; _i < 2; ++_i) \
;         __builtin_amdgcn_global_load_lds((const unsigned*)((const char*)(gbase) + (voff)[_i]), (PG8_LAS unsigned*)(lds + (bufoff) + ldsw + _i * 8192), 16, 0, 0); } while (0)
; #define PG8_LDA(dst, b, h) do { _Pragma("unroll") for (int m = 0; m < 4; ++m) _Pragma("unroll") for (int k = 0; k < 2; ++k) dst[m][k] = *(const PG8_LAS bf16x8*)(lds + PG8_SA(b, h) + aoff + m * 2048 + k * 1024); } while (0)
; #define PG8_LDB(dst, b, h) do { _Pragma("unroll") for (int n = 0; n < 2; ++n) _Pragma("unroll") for (int k = 0; k < 2; ++k) dst[n][k] = *(const PG8_LAS bf16x8*)(lds + PG8_SB(b, h) + boff + n * 2048 + k * 1024); } while (0)
; #define PG8_MMA(ai, bj, At, Bt) do { __builtin_amdgcn_s_setprio(1); _Pragma("unroll") for (int m = 0; m < 4; ++m) _Pragma("unroll") for (int n = 0; n < 2; ++n) _Pragma("unroll") for (int k = 0; k < 2; ++k) \
;         acc[ai][bj][m][n] = __builtin_amdgcn_mfma_f32_16x16x32_bf16(Bt[n][k], At[m][k], acc[ai][bj][m][n], 0, 0, 0); __builtin_amdgcn_s_setprio(0); } while (0)
; #define PG8_BAR __builtin_amdgcn_s_barrier()
; template <class Epi, class Sched, bool ALIGN_EPI = false>
; __device__ __forceinline__ void gemm_phase(PG8_LAS unsigned char* lds, const Gemm g, const Sched& S, const Epi& E) {
;     ...
;             const bool last = (t == nt - 2);
;             const char* a1 = cA + (size_t)(t + 1) * kstep;
;             const char* a2 = last ? nA : cA + (size_t)(t + 2) * kstep; const char* b2 = last ? nB : cB + (size_t)(t + 2) * kstep;
;             const char* a3 = a2 + kstep; const char* b3 = b2 + kstep;
;             unsigned w0[2], w1[2];
; #pragma unroll
;             for (int i = 0; i < 2; ++i) { w0[i] = (Sched::GATHER && last) ? vn0[i] : vc0[i]; w1[i] = (Sched::GATHER && last) ? vn1[i] : vc1[i]; }
;             if (last && has_next) S.a_ready(nxt);
;             PG8_LDB(B0, 0, 0); PG8_LDB(B1, 0, 1); PG8_SCHED; PG8_LDA(At, 0, 0); PG8_STAGE(PG8_SA(1, 1), a1 + hstepA, vc1);
;             PG8_WAIT_V(8); PG8_WAIT_L(0); PG8_BAR; PG8_MMA(0, 0, At, B0); PG8_MMA(0, 1, At, B1); PG8_BAR; PG8_SCHED;
;             PG8_LDA(At, 0, 1); PG8_STAGE(PG8_SB(0, 0), b2, voffB); PG8_STAGE(PG8_SB(0, 1), b2 + hstep, voffB); PG8_STAGE(PG8_SA(0, 0), a2, w0);
;             PG8_WAIT_V(8); PG8_WAIT_L(0); PG8_BAR; PG8_MMA(1, 0, At, B0); PG8_MMA(1, 1, At, B1); PG8_BAR; PG8_SCHED;
.LBB0_787:
	s_add_u32 s18, s16, 0x3c800100
	s_addc_u32 s19, s17, 0
	s_add_u32 s58, s16, s45
	s_addc_u32 s59, s17, s46
	s_cmp_eq_u32 s47, 28
	s_cselect_b32 s23, s21, s19
	s_cselect_b32 s22, s20, s18
	s_cselect_b32 s19, s13, s59
	s_cselect_b32 s18, s12, s58
	s_mov_b32 m0, s48
	v_lshl_add_u64 v[236:237], s[16:17], 0, v[160:161]
	global_load_lds_dwordx4 v[236:237], off
	v_lshl_add_u64 v[236:237], s[16:17], 0, v[158:159]
	s_mov_b32 m0, s49
	s_nop 0
	global_load_lds_dwordx4 v[236:237], off
	ds_read_b128 v[172:175], v167
	ds_read_b128 v[176:179], v167 offset:1024
	ds_read_b128 v[180:183], v167 offset:2048
	ds_read_b128 v[184:187], v167 offset:3072
	ds_read_b128 v[188:191], v168
	ds_read_b128 v[192:195], v168 offset:1024
	ds_read_b128 v[196:199], v168 offset:2048
	ds_read_b128 v[200:203], v168 offset:3072
	ds_read_b128 v[204:207], v169
	ds_read_b128 v[208:211], v169 offset:1024
	ds_read_b128 v[212:215], v169 offset:2048
	ds_read_b128 v[216:219], v169 offset:3072
	ds_read_b128 v[220:223], v169 offset:4096
	ds_read_b128 v[224:227], v169 offset:5120
	ds_read_b128 v[228:231], v169 offset:6144
	ds_read_b128 v[232:235], v169 offset:7168
	s_waitcnt vmcnt(8)
	s_waitcnt lgkmcnt(0)
	s_barrier
	v_mfma_f32_16x16x32_bf16 v[126:129], v[172:175], v[204:207], v[126:129]
	v_mfma_f32_16x16x32_bf16 v[122:125], v[180:183], v[204:207], v[122:125]
	v_mfma_f32_16x16x32_bf16 v[110:113], v[172:175], v[212:215], v[110:113]
	v_mfma_f32_16x16x32_bf16 v[106:109], v[180:183], v[212:215], v[106:109]
	v_mfma_f32_16x16x32_bf16 v[94:97], v[172:175], v[220:223], v[94:97]
	v_mfma_f32_16x16x32_bf16 v[90:93], v[180:183], v[220:223], v[90:93]
	v_mfma_f32_16x16x32_bf16 v[78:81], v[172:175], v[228:231], v[78:81]
	v_mfma_f32_16x16x32_bf16 v[74:77], v[180:183], v[228:231], v[74:77]
	v_mfma_f32_16x16x32_bf16 v[126:129], v[176:179], v[208:211], v[126:129]
	v_mfma_f32_16x16x32_bf16 v[122:125], v[184:187], v[208:211], v[122:125]
	v_mfma_f32_16x16x32_bf16 v[110:113], v[176:179], v[216:219], v[110:113]
	v_mfma_f32_16x16x32_bf16 v[106:109], v[184:187], v[216:219], v[106:109]
	v_mfma_f32_16x16x32_bf16 v[94:97], v[176:179], v[224:227], v[94:97]
	v_mfma_f32_16x16x32_bf16 v[90:93], v[184:187], v[224:227], v[90:93]
	v_mfma_f32_16x16x32_bf16 v[78:81], v[176:179], v[232:235], v[78:81]
	v_mfma_f32_16x16x32_bf16 v[74:77], v[184:187], v[232:235], v[74:77]
	v_mfma_f32_16x16x32_bf16 v[118:121], v[188:191], v[204:207], v[118:121]
	v_mfma_f32_16x16x32_bf16 v[114:117], v[196:199], v[204:207], v[114:117]
	v_mfma_f32_16x16x32_bf16 v[102:105], v[188:191], v[212:215], v[102:105]
	v_mfma_f32_16x16x32_bf16 v[98:101], v[196:199], v[212:215], v[98:101]
	v_mfma_f32_16x16x32_bf16 v[86:89], v[188:191], v[220:223], v[86:89]
	v_mfma_f32_16x16x32_bf16 v[82:85], v[196:199], v[220:223], v[82:85]
	v_mfma_f32_16x16x32_bf16 v[70:73], v[188:191], v[228:231], v[70:73]
	v_mfma_f32_16x16x32_bf16 v[66:69], v[196:199], v[228:231], v[66:69]
	v_mfma_f32_16x16x32_bf16 v[118:121], v[192:195], v[208:211], v[118:121]
	v_mfma_f32_16x16x32_bf16 v[114:117], v[200:203], v[208:211], v[114:117]
	v_mfma_f32_16x16x32_bf16 v[102:105], v[192:195], v[216:219], v[102:105]
	v_mfma_f32_16x16x32_bf16 v[98:101], v[200:203], v[216:219], v[98:101]
	v_mfma_f32_16x16x32_bf16 v[86:89], v[192:195], v[224:227], v[86:89]
	v_mfma_f32_16x16x32_bf16 v[82:85], v[200:203], v[224:227], v[82:85]
	v_mfma_f32_16x16x32_bf16 v[70:73], v[192:195], v[232:235], v[70:73]
	v_mfma_f32_16x16x32_bf16 v[66:69], v[200:203], v[232:235], v[66:69]
	s_barrier
	s_mov_b32 m0, s50
	v_lshl_add_u64 v[236:237], s[18:19], 0, v[146:147]
	s_add_u32 s58, s18, 0x80000
	global_load_lds_dwordx4 v[236:237], off
	v_lshl_add_u64 v[238:239], s[18:19], 0, v[144:145]
	s_mov_b32 m0, s51
	s_addc_u32 s59, s19, 0
	global_load_lds_dwordx4 v[238:239], off
	v_lshl_add_u64 v[240:241], s[58:59], 0, v[146:147]
	s_mov_b32 m0, s52
	v_lshl_add_u64 v[242:243], s[22:23], 0, v[150:151]
	global_load_lds_dwordx4 v[240:241], off
	v_lshl_add_u64 v[240:241], s[58:59], 0, v[144:145]
	s_mov_b32 m0, s53
	s_nop 0
	global_load_lds_dwordx4 v[240:241], off
	v_lshl_add_u64 v[240:241], s[22:23], 0, v[148:149]
	s_mov_b32 m0, s27
	s_nop 0
	global_load_lds_dwordx4 v[240:241], off
	s_mov_b32 m0, s35
	s_nop 0
	global_load_lds_dwordx4 v[242:243], off
	ds_read_b128 v[204:207], v169 offset:16384
	ds_read_b128 v[208:211], v169 offset:17408
	ds_read_b128 v[212:215], v169 offset:18432
	ds_read_b128 v[216:219], v169 offset:19456
	ds_read_b128 v[220:223], v169 offset:20480
	ds_read_b128 v[224:227], v169 offset:21504
	ds_read_b128 v[228:231], v169 offset:22528
	ds_read_b128 v[232:235], v169 offset:23552
	s_waitcnt vmcnt(8)
	s_waitcnt lgkmcnt(0)
	s_barrier
; #define PG8_STAGE(bufoff, gbase, voff) do { _Pragma("unroll") for (int _i = 0; _i < 2; ++_i) \
;         __builtin_amdgcn_global_load_lds((const unsigned*)((const char*)(gbase) + (voff)[_i]), (PG8_LAS unsigned*)(lds + (bufoff) + ldsw + _i * 8192), 16, 0, 0); } while (0)
; #define PG8_LDA(dst, b, h) do { _Pragma("unroll") for (int m = 0; m < 4; ++m) _Pragma("unroll") for (int k = 0; k < 2; ++k) dst[m][k] = *(const PG8_LAS bf16x8*)(lds + PG8_SA(b, h) + aoff + m * 2048 + k * 1024); } while (0)
; #define PG8_LDB(dst, b, h) do { _Pragma("unroll") for (int n = 0; n < 2; ++n) _Pragma("unroll") for (int k = 0; k < 2; ++k) dst[n][k] = *(const PG8_LAS bf16x8*)(lds + PG8_SB(b, h) + boff + n * 2048 + k * 1024); } while (0)
; #define PG8_MMA(ai, bj, At, Bt) do { __builtin_amdgcn_s_setprio(1); _Pragma("unroll") for (int m = 0; m < 4; ++m) _Pragma("unroll") for (int n = 0; n < 2; ++n) _Pragma("unroll") for (int k = 0; k < 2; ++k) \
;         acc[ai][bj][m][n] = __builtin_amdgcn_mfma_f32_16x16x32_bf16(Bt[n][k], At[m][k], acc[ai][bj][m][n], 0, 0, 0); __builtin_amdgcn_s_setprio(0); } while (0)
; #define PG8_WAIT_V(n) asm volatile("s_waitcnt vmcnt(" #n ")" ::: "memory")
; #define PG8_WAIT_L(n) asm volatile("s_waitcnt lgkmcnt(" #n ")" ::: "memory")
; #define PG8_BAR __builtin_amdgcn_s_barrier()
; #define PG8_SCHED __builtin_amdgcn_sched_barrier(0)
; template <class Epi, class Sched, bool ALIGN_EPI = false>
; __device__ __forceinline__ void gemm_phase(PG8_LAS unsigned char* lds, const Gemm g, const Sched& S, const Epi& E) {
;     ...
;             PG8_WAIT_V(8); PG8_WAIT_L(0); PG8_BAR; PG8_MMA(1, 0, At, B0); PG8_MMA(1, 1, At, B1); PG8_BAR; PG8_SCHED;
;             PG8_LDB(B0, 1, 0); PG8_LDB(B1, 1, 1); PG8_SCHED; PG8_LDA(At, 1, 0); PG8_STAGE(PG8_SA(0, 1), a2 + hstepA, w1);
;             PG8_WAIT_V(8); PG8_WAIT_L(0); PG8_BAR; PG8_MMA(0, 0, At, B0); PG8_MMA(0, 1, At, B1); PG8_BAR; PG8_SCHED;
	v_mfma_f32_16x16x32_bf16 v[62:65], v[172:175], v[204:207], v[62:65]
	v_mfma_f32_16x16x32_bf16 v[58:61], v[180:183], v[204:207], v[58:61]
	v_mfma_f32_16x16x32_bf16 v[50:53], v[172:175], v[212:215], v[50:53]
	v_mfma_f32_16x16x32_bf16 v[42:45], v[180:183], v[212:215], v[42:45]
	v_mfma_f32_16x16x32_bf16 v[34:37], v[172:175], v[220:223], v[34:37]
	v_mfma_f32_16x16x32_bf16 v[26:29], v[180:183], v[220:223], v[26:29]
	v_mfma_f32_16x16x32_bf16 v[14:17], v[172:175], v[228:231], v[14:17]
	v_mfma_f32_16x16x32_bf16 v[2:5], v[180:183], v[228:231], v[2:5]
	v_mfma_f32_16x16x32_bf16 v[62:65], v[176:179], v[208:211], v[62:65]
	v_mfma_f32_16x16x32_bf16 v[58:61], v[184:187], v[208:211], v[58:61]
	v_mfma_f32_16x16x32_bf16 v[50:53], v[176:179], v[216:219], v[50:53]
	v_mfma_f32_16x16x32_bf16 v[42:45], v[184:187], v[216:219], v[42:45]
	v_mfma_f32_16x16x32_bf16 v[34:37], v[176:179], v[224:227], v[34:37]
	v_mfma_f32_16x16x32_bf16 v[26:29], v[184:187], v[224:227], v[26:29]
	v_mfma_f32_16x16x32_bf16 v[14:17], v[176:179], v[232:235], v[14:17]
	v_mfma_f32_16x16x32_bf16 v[2:5], v[184:187], v[232:235], v[2:5]
	v_mfma_f32_16x16x32_bf16 v[54:57], v[188:191], v[204:207], v[54:57]
	v_mfma_f32_16x16x32_bf16 v[46:49], v[196:199], v[204:207], v[46:49]
	v_mfma_f32_16x16x32_bf16 v[38:41], v[188:191], v[212:215], v[38:41]
	v_mfma_f32_16x16x32_bf16 v[30:33], v[196:199], v[212:215], v[30:33]
	v_mfma_f32_16x16x32_bf16 v[22:25], v[188:191], v[220:223], v[22:25]
	v_mfma_f32_16x16x32_bf16 v[18:21], v[196:199], v[220:223], v[18:21]
	v_mfma_f32_16x16x32_bf16 v[10:13], v[188:191], v[228:231], v[10:13]
	v_mfma_f32_16x16x32_bf16 v[6:9], v[196:199], v[228:231], v[6:9]
	v_mfma_f32_16x16x32_bf16 v[54:57], v[192:195], v[208:211], v[54:57]
	v_mfma_f32_16x16x32_bf16 v[46:49], v[200:203], v[208:211], v[46:49]
	v_mfma_f32_16x16x32_bf16 v[38:41], v[192:195], v[216:219], v[38:41]
	v_mfma_f32_16x16x32_bf16 v[30:33], v[200:203], v[216:219], v[30:33]
	v_mfma_f32_16x16x32_bf16 v[22:25], v[192:195], v[224:227], v[22:25]
	v_mfma_f32_16x16x32_bf16 v[18:21], v[200:203], v[224:227], v[18:21]
	v_mfma_f32_16x16x32_bf16 v[10:13], v[192:195], v[232:235], v[10:13]
	v_mfma_f32_16x16x32_bf16 v[6:9], v[200:203], v[232:235], v[6:9]
	s_barrier
	s_mov_b32 m0, s40
	v_lshl_add_u64 v[244:245], s[22:23], 0, v[152:153]
	global_load_lds_dwordx4 v[244:245], off
	v_lshl_add_u64 v[244:245], s[22:23], 0, v[154:155]
	s_mov_b32 m0, s41
	s_nop 0
	global_load_lds_dwordx4 v[244:245], off
	ds_read_b128 v[172:175], v170
	ds_read_b128 v[176:179], v170 offset:1024
	ds_read_b128 v[180:183], v170 offset:2048
	ds_read_b128 v[184:187], v170 offset:3072
	ds_read_b128 v[188:191], v171
	ds_read_b128 v[192:195], v171 offset:1024
	ds_read_b128 v[196:199], v171 offset:2048
	ds_read_b128 v[200:203], v171 offset:3072
	ds_read_b128 v[204:207], v169 offset:32768
	ds_read_b128 v[208:211], v169 offset:33792
	ds_read_b128 v[212:215], v169 offset:34816
	ds_read_b128 v[216:219], v169 offset:35840
	ds_read_b128 v[220:223], v169 offset:36864
	ds_read_b128 v[224:227], v169 offset:37888
	ds_read_b128 v[228:231], v169 offset:38912
	ds_read_b128 v[232:235], v169 offset:39936
	s_waitcnt vmcnt(8)
	s_waitcnt lgkmcnt(0)
	s_barrier
	v_mfma_f32_16x16x32_bf16 v[126:129], v[172:175], v[204:207], v[126:129]
	v_mfma_f32_16x16x32_bf16 v[122:125], v[180:183], v[204:207], v[122:125]
	v_mfma_f32_16x16x32_bf16 v[110:113], v[172:175], v[212:215], v[110:113]
	v_mfma_f32_16x16x32_bf16 v[106:109], v[180:183], v[212:215], v[106:109]
	v_mfma_f32_16x16x32_bf16 v[94:97], v[172:175], v[220:223], v[94:97]
	v_mfma_f32_16x16x32_bf16 v[90:93], v[180:183], v[220:223], v[90:93]
	v_mfma_f32_16x16x32_bf16 v[78:81], v[172:175], v[228:231], v[78:81]
	v_mfma_f32_16x16x32_bf16 v[74:77], v[180:183], v[228:231], v[74:77]
	v_mfma_f32_16x16x32_bf16 v[126:129], v[176:179], v[208:211], v[126:129]
	v_mfma_f32_16x16x32_bf16 v[122:125], v[184:187], v[208:211], v[122:125]
	v_mfma_f32_16x16x32_bf16 v[110:113], v[176:179], v[216:219], v[110:113]
	v_mfma_f32_16x16x32_bf16 v[106:109], v[184:187], v[216:219], v[106:109]
	v_mfma_f32_16x16x32_bf16 v[94:97], v[176:179], v[224:227], v[94:97]
	v_mfma_f32_16x16x32_bf16 v[90:93], v[184:187], v[224:227], v[90:93]
	v_mfma_f32_16x16x32_bf16 v[78:81], v[176:179], v[232:235], v[78:81]
	v_mfma_f32_16x16x32_bf16 v[74:77], v[184:187], v[232:235], v[74:77]
	v_mfma_f32_16x16x32_bf16 v[118:121], v[188:191], v[204:207], v[118:121]
	v_mfma_f32_16x16x32_bf16 v[114:117], v[196:199], v[204:207], v[114:117]
	v_mfma_f32_16x16x32_bf16 v[102:105], v[188:191], v[212:215], v[102:105]
	v_mfma_f32_16x16x32_bf16 v[98:101], v[196:199], v[212:215], v[98:101]
	v_mfma_f32_16x16x32_bf16 v[86:89], v[188:191], v[220:223], v[86:89]
	v_mfma_f32_16x16x32_bf16 v[82:85], v[196:199], v[220:223], v[82:85]
	v_mfma_f32_16x16x32_bf16 v[70:73], v[188:191], v[228:231], v[70:73]
	v_mfma_f32_16x16x32_bf16 v[66:69], v[196:199], v[228:231], v[66:69]
	v_mfma_f32_16x16x32_bf16 v[118:121], v[192:195], v[208:211], v[118:121]
	v_mfma_f32_16x16x32_bf16 v[114:117], v[200:203], v[208:211], v[114:117]
	v_mfma_f32_16x16x32_bf16 v[102:105], v[192:195], v[216:219], v[102:105]
	v_mfma_f32_16x16x32_bf16 v[98:101], v[200:203], v[216:219], v[98:101]
	v_mfma_f32_16x16x32_bf16 v[86:89], v[192:195], v[224:227], v[86:89]
	v_mfma_f32_16x16x32_bf16 v[82:85], v[200:203], v[224:227], v[82:85]
	v_mfma_f32_16x16x32_bf16 v[70:73], v[192:195], v[232:235], v[70:73]
	v_mfma_f32_16x16x32_bf16 v[66:69], v[200:203], v[232:235], v[66:69]
	s_barrier
; #define PG8_STAGE(bufoff, gbase, voff) do { _Pragma("unroll") for (int _i = 0; _i < 2; ++_i) \
;         __builtin_amdgcn_global_load_lds((const unsigned*)((const char*)(gbase) + (voff)[_i]), (PG8_LAS unsigned*)(lds + (bufoff) + ldsw + _i * 8192), 16, 0, 0); } while (0)
; #define PG8_LDA(dst, b, h) do { _Pragma("unroll") for (int m = 0; m < 4; ++m) _Pragma("unroll") for (int k = 0; k < 2; ++k) dst[m][k] = *(const PG8_LAS bf16x8*)(lds + PG8_SA(b, h) + aoff + m * 2048 + k * 1024); } while (0)
; #define PG8_MMA(ai, bj, At, Bt) do { __builtin_amdgcn_s_setprio(1); _Pragma("unroll") for (int m = 0; m < 4; ++m) _Pragma("unroll") for (int n = 0; n < 2; ++n) _Pragma("unroll") for (int k = 0; k < 2; ++k) \
;         acc[ai][bj][m][n] = __builtin_amdgcn_mfma_f32_16x16x32_bf16(Bt[n][k], At[m][k], acc[ai][bj][m][n], 0, 0, 0); __builtin_amdgcn_s_setprio(0); } while (0)
; #define PG8_WAIT_V(n) asm volatile("s_waitcnt vmcnt(" #n ")" ::: "memory")
; #define PG8_WAIT_L(n) asm volatile("s_waitcnt lgkmcnt(" #n ")" ::: "memory")
; #define PG8_BAR __builtin_amdgcn_s_barrier()
; #define PG8_SCHED __builtin_amdgcn_sched_barrier(0)
; template <class Epi, class Sched, bool ALIGN_EPI = false>
; __device__ __forceinline__ void gemm_phase(PG8_LAS unsigned char* lds, const Gemm g, const Sched& S, const Epi& E) {
;     ...
;             PG8_LDA(At, 1, 1); PG8_STAGE(PG8_SB(1, 0), b3, voffB); PG8_STAGE(PG8_SB(1, 1), b3 + hstep, voffB); PG8_STAGE(PG8_SA(1, 0), a3, w0);
;             PG8_WAIT_V(8); PG8_WAIT_L(0); PG8_BAR; PG8_MMA(1, 0, At, B0); PG8_MMA(1, 1, At, B1); PG8_BAR; PG8_SCHED;
;             if constexpr (Epi::KSCALE) { if (((t + 2) & 7) == 0 && t + 2 < nt) { E.kscale(acc, pf, ((t + 2) >> 3) - 1, wr, fr); PG8_SCHED; } }
;         }
;         if constexpr (ALIGN_EPI) { if (wr == 0) PG8_BAR; }
	s_mov_b32 m0, s54
	v_lshl_add_u64 v[236:237], v[236:237], 0, s[14:15]
	s_add_u32 s18, s18, 0x80080
	global_load_lds_dwordx4 v[236:237], off
	v_lshl_add_u64 v[236:237], v[238:239], 0, s[14:15]
	s_mov_b32 m0, s55
	s_addc_u32 s19, s19, 0
	global_load_lds_dwordx4 v[236:237], off
	v_lshl_add_u64 v[236:237], s[18:19], 0, v[146:147]
	s_mov_b32 m0, s56
	s_nop 0
	global_load_lds_dwordx4 v[236:237], off
	v_lshl_add_u64 v[236:237], s[18:19], 0, v[144:145]
	s_mov_b32 m0, s57
	s_nop 0
	global_load_lds_dwordx4 v[236:237], off
	v_lshl_add_u64 v[236:237], v[240:241], 0, s[14:15]
	s_mov_b32 m0, s43
	s_nop 0
	global_load_lds_dwordx4 v[236:237], off
	v_lshl_add_u64 v[236:237], v[242:243], 0, s[14:15]
	s_mov_b32 m0, s44
	s_nop 0
	global_load_lds_dwordx4 v[236:237], off
	ds_read_b128 v[204:207], v169 offset:49152
	ds_read_b128 v[208:211], v169 offset:50176
	ds_read_b128 v[212:215], v169 offset:51200
	ds_read_b128 v[216:219], v169 offset:52224
	ds_read_b128 v[220:223], v169 offset:53248
	ds_read_b128 v[224:227], v169 offset:54272
	ds_read_b128 v[228:231], v169 offset:55296
	ds_read_b128 v[232:235], v169 offset:56320
	s_waitcnt vmcnt(8)
	s_waitcnt lgkmcnt(0)
	s_barrier
	v_mfma_f32_16x16x32_bf16 v[62:65], v[172:175], v[204:207], v[62:65]
	v_mfma_f32_16x16x32_bf16 v[58:61], v[180:183], v[204:207], v[58:61]
	v_mfma_f32_16x16x32_bf16 v[50:53], v[172:175], v[212:215], v[50:53]
	v_mfma_f32_16x16x32_bf16 v[42:45], v[180:183], v[212:215], v[42:45]
	v_mfma_f32_16x16x32_bf16 v[34:37], v[172:175], v[220:223], v[34:37]
	v_mfma_f32_16x16x32_bf16 v[26:29], v[180:183], v[220:223], v[26:29]
	v_mfma_f32_16x16x32_bf16 v[14:17], v[172:175], v[228:231], v[14:17]
	v_mfma_f32_16x16x32_bf16 v[2:5], v[180:183], v[228:231], v[2:5]
	v_mfma_f32_16x16x32_bf16 v[62:65], v[176:179], v[208:211], v[62:65]
	v_mfma_f32_16x16x32_bf16 v[58:61], v[184:187], v[208:211], v[58:61]
	v_mfma_f32_16x16x32_bf16 v[50:53], v[176:179], v[216:219], v[50:53]
	v_mfma_f32_16x16x32_bf16 v[42:45], v[184:187], v[216:219], v[42:45]
	v_mfma_f32_16x16x32_bf16 v[34:37], v[176:179], v[224:227], v[34:37]
	v_mfma_f32_16x16x32_bf16 v[26:29], v[184:187], v[224:227], v[26:29]
	v_mfma_f32_16x16x32_bf16 v[14:17], v[176:179], v[232:235], v[14:17]
	v_mfma_f32_16x16x32_bf16 v[2:5], v[184:187], v[232:235], v[2:5]
	v_mfma_f32_16x16x32_bf16 v[54:57], v[188:191], v[204:207], v[54:57]
	v_mfma_f32_16x16x32_bf16 v[46:49], v[196:199], v[204:207], v[46:49]
	v_mfma_f32_16x16x32_bf16 v[38:41], v[188:191], v[212:215], v[38:41]
	v_mfma_f32_16x16x32_bf16 v[30:33], v[196:199], v[212:215], v[30:33]
	v_mfma_f32_16x16x32_bf16 v[22:25], v[188:191], v[220:223], v[22:25]
	v_mfma_f32_16x16x32_bf16 v[18:21], v[196:199], v[220:223], v[18:21]
	v_mfma_f32_16x16x32_bf16 v[10:13], v[188:191], v[228:231], v[10:13]
	v_mfma_f32_16x16x32_bf16 v[6:9], v[196:199], v[228:231], v[6:9]
	v_mfma_f32_16x16x32_bf16 v[54:57], v[192:195], v[208:211], v[54:57]
	v_mfma_f32_16x16x32_bf16 v[46:49], v[200:203], v[208:211], v[46:49]
	v_mfma_f32_16x16x32_bf16 v[38:41], v[192:195], v[216:219], v[38:41]
	v_mfma_f32_16x16x32_bf16 v[30:33], v[200:203], v[216:219], v[30:33]
	v_mfma_f32_16x16x32_bf16 v[22:25], v[192:195], v[224:227], v[22:25]
	v_mfma_f32_16x16x32_bf16 v[18:21], v[200:203], v[224:227], v[18:21]
	v_mfma_f32_16x16x32_bf16 v[10:13], v[192:195], v[232:235], v[10:13]
	v_mfma_f32_16x16x32_bf16 v[6:9], v[200:203], v[232:235], v[6:9]
	s_barrier
	s_add_i32 s47, s47, 2
	s_add_u32 s16, s16, 0x100
	s_addc_u32 s17, s17, 0
	s_cmp_gt_u32 s47, 29
	s_cbranch_scc0 .LBB0_787
	s_cmpk_lt_u32 s24, 0x100
	s_cbranch_scc0 .LBB0_790
	s_barrier

; #define PG8_STAGE(bufoff, gbase, voff) do { _Pragma("unroll") for (int _i = 0; _i < 2; ++_i) \
;         __builtin_amdgcn_global_load_lds((const unsigned*)((const char*)(gbase) + (voff)[_i]), (PG8_LAS unsigned*)(lds + (bufoff) + ldsw + _i * 8192), 16, 0, 0); } while (0)
; #define PG8_LDA(dst, b, h) do { _Pragma("unroll") for (int m = 0; m < 4; ++m) _Pragma("unroll") for (int k = 0; k < 2; ++k) dst[m][k] = *(const PG8_LAS bf16x8*)(lds + PG8_SA(b, h) + aoff + m * 2048 + k * 1024); } while (0)
; #define PG8_LDB(dst, b, h) do { _Pragma("unroll") for (int n = 0; n < 2; ++n) _Pragma("unroll") for (int k = 0; k < 2; ++k) dst[n][k] = *(const PG8_LAS bf16x8*)(lds + PG8_SB(b, h) + boff + n * 2048 + k * 1024); } while (0)
; #define PG8_MMA(ai, bj, At, Bt) do { __builtin_amdgcn_s_setprio(1); _Pragma("unroll") for (int m = 0; m < 4; ++m) _Pragma("unroll") for (int n = 0; n < 2; ++n) _Pragma("unroll") for (int k = 0; k < 2; ++k) \
;         acc[ai][bj][m][n] = __builtin_amdgcn_mfma_f32_16x16x32_bf16(Bt[n][k], At[m][k], acc[ai][bj][m][n], 0, 0, 0); __builtin_amdgcn_s_setprio(0); } while (0)
; #define PG8_BAR __builtin_amdgcn_s_barrier()
; template <class Epi, class Sched, bool ALIGN_EPI = false>
; __device__ __forceinline__ void gemm_phase(PG8_LAS unsigned char* lds, const Gemm g, const Sched& S, const Epi& E) {
;     ...
;             const bool last = (t == nt - 2);
;             const char* a1 = cA + (size_t)(t + 1) * kstep;
;             const char* a2 = last ? nA : cA + (size_t)(t + 2) * kstep; const char* b2 = last ? nB : cB + (size_t)(t + 2) * kstep;
;             const char* a3 = a2 + kstep; const char* b3 = b2 + kstep;
;             unsigned w0[2], w1[2];
; #pragma unroll
;             for (int i = 0; i < 2; ++i) { w0[i] = (Sched::GATHER && last) ? vn0[i] : vc0[i]; w1[i] = (Sched::GATHER && last) ? vn1[i] : vc1[i]; }
;             if (last && has_next) S.a_ready(nxt);
;             PG8_LDB(B0, 0, 0); PG8_LDB(B1, 0, 1); PG8_SCHED; PG8_LDA(At, 0, 0); PG8_STAGE(PG8_SA(1, 1), a1 + hstepA, vc1);
;             PG8_WAIT_V(8); PG8_WAIT_L(0); PG8_BAR; PG8_MMA(0, 0, At, B0); PG8_MMA(0, 1, At, B1); PG8_BAR; PG8_SCHED;
;             PG8_LDA(At, 0, 1); PG8_STAGE(PG8_SB(0, 0), b2, voffB); PG8_STAGE(PG8_SB(0, 1), b2 + hstep, voffB); PG8_STAGE(PG8_SA(0, 0), a2, w0);
;             PG8_WAIT_V(8); PG8_WAIT_L(0); PG8_BAR; PG8_MMA(1, 0, At, B0); PG8_MMA(1, 1, At, B1); PG8_BAR; PG8_SCHED;
.LBB0_805:
	s_add_u32 s62, s60, 0xfffe0080
	s_addc_u32 s63, s61, -1
	s_cmp_eq_u32 s92, 4
	s_cselect_b32 s65, s45, s63
	s_cselect_b32 s64, s57, s62
	s_cselect_b32 s63, s47, s91
	s_cselect_b32 s62, s89, s90
	v_lshl_add_u64 v[218:219], s[60:61], 0, v[140:141]
	s_add_i32 m0, s59, 0xc000
	s_nop 0
	global_load_lds_dwordx4 v[218:219], off
	v_lshl_add_u64 v[218:219], s[60:61], 0, v[138:139]
	s_add_i32 m0, s59, 0xe000
	s_nop 0
	global_load_lds_dwordx4 v[218:219], off
	ds_read_b128 v[142:145], v1
	ds_read_b128 v[158:161], v1 offset:1024
	ds_read_b128 v[162:165], v1 offset:2048
	ds_read_b128 v[166:169], v1 offset:3072
	ds_read_b128 v[170:173], v156
	ds_read_b128 v[174:177], v156 offset:1024
	ds_read_b128 v[178:181], v156 offset:2048
	ds_read_b128 v[182:185], v156 offset:3072
	ds_read_b128 v[186:189], v157
	ds_read_b128 v[190:193], v157 offset:1024
	ds_read_b128 v[194:197], v157 offset:2048
	ds_read_b128 v[198:201], v157 offset:3072
	ds_read_b128 v[202:205], v157 offset:4096
	ds_read_b128 v[206:209], v157 offset:5120
	ds_read_b128 v[210:213], v157 offset:6144
	ds_read_b128 v[214:217], v157 offset:7168
	s_waitcnt vmcnt(8)
	s_waitcnt lgkmcnt(0)
	s_barrier
	v_mfma_f32_16x16x32_bf16 v[126:129], v[142:145], v[186:189], v[126:129]
	v_mfma_f32_16x16x32_bf16 v[122:125], v[162:165], v[186:189], v[122:125]
	v_mfma_f32_16x16x32_bf16 v[114:117], v[142:145], v[194:197], v[114:117]
	v_mfma_f32_16x16x32_bf16 v[106:109], v[162:165], v[194:197], v[106:109]
	v_mfma_f32_16x16x32_bf16 v[98:101], v[142:145], v[202:205], v[98:101]
	v_mfma_f32_16x16x32_bf16 v[90:93], v[162:165], v[202:205], v[90:93]
	v_mfma_f32_16x16x32_bf16 v[82:85], v[142:145], v[210:213], v[82:85]
	v_mfma_f32_16x16x32_bf16 v[74:77], v[162:165], v[210:213], v[74:77]
	v_mfma_f32_16x16x32_bf16 v[126:129], v[158:161], v[190:193], v[126:129]
	v_mfma_f32_16x16x32_bf16 v[122:125], v[166:169], v[190:193], v[122:125]
	v_mfma_f32_16x16x32_bf16 v[114:117], v[158:161], v[198:201], v[114:117]
	v_mfma_f32_16x16x32_bf16 v[106:109], v[166:169], v[198:201], v[106:109]
	v_mfma_f32_16x16x32_bf16 v[98:101], v[158:161], v[206:209], v[98:101]
	v_mfma_f32_16x16x32_bf16 v[90:93], v[166:169], v[206:209], v[90:93]
	v_mfma_f32_16x16x32_bf16 v[82:85], v[158:161], v[214:217], v[82:85]
	v_mfma_f32_16x16x32_bf16 v[74:77], v[166:169], v[214:217], v[74:77]
	v_mfma_f32_16x16x32_bf16 v[118:121], v[170:173], v[186:189], v[118:121]
	v_mfma_f32_16x16x32_bf16 v[110:113], v[178:181], v[186:189], v[110:113]
	v_mfma_f32_16x16x32_bf16 v[102:105], v[170:173], v[194:197], v[102:105]
	v_mfma_f32_16x16x32_bf16 v[94:97], v[178:181], v[194:197], v[94:97]
	v_mfma_f32_16x16x32_bf16 v[86:89], v[170:173], v[202:205], v[86:89]
	v_mfma_f32_16x16x32_bf16 v[78:81], v[178:181], v[202:205], v[78:81]
	v_mfma_f32_16x16x32_bf16 v[62:65], v[170:173], v[210:213], v[62:65]
	v_mfma_f32_16x16x32_bf16 v[58:61], v[178:181], v[210:213], v[58:61]
	v_mfma_f32_16x16x32_bf16 v[118:121], v[174:177], v[190:193], v[118:121]
	v_mfma_f32_16x16x32_bf16 v[110:113], v[182:185], v[190:193], v[110:113]
	v_mfma_f32_16x16x32_bf16 v[102:105], v[174:177], v[198:201], v[102:105]
	v_mfma_f32_16x16x32_bf16 v[94:97], v[182:185], v[198:201], v[94:97]
	v_mfma_f32_16x16x32_bf16 v[86:89], v[174:177], v[206:209], v[86:89]
	v_mfma_f32_16x16x32_bf16 v[78:81], v[182:185], v[206:209], v[78:81]
	v_mfma_f32_16x16x32_bf16 v[62:65], v[174:177], v[214:217], v[62:65]
	v_mfma_f32_16x16x32_bf16 v[58:61], v[182:185], v[214:217], v[58:61]
	s_barrier
	s_add_i32 s93, s79, s66
	v_lshl_add_u64 v[218:219], s[62:63], 0, v[132:133]
	s_mov_b32 m0, s93
	s_nop 0
	global_load_lds_dwordx4 v[218:219], off
	s_add_i32 m0, s93, 0x2000
	s_add_u32 s94, s62, 0x20000
	v_lshl_add_u64 v[220:221], s[62:63], 0, v[136:137]
	s_addc_u32 s95, s63, 0
	s_add_i32 s93, s80, s66
	global_load_lds_dwordx4 v[220:221], off
	v_lshl_add_u64 v[222:223], s[94:95], 0, v[132:133]
	s_mov_b32 m0, s93
	v_lshl_add_u64 v[224:225], s[64:65], 0, v[134:135]
	global_load_lds_dwordx4 v[222:223], off
	v_lshl_add_u64 v[222:223], s[94:95], 0, v[136:137]
	s_add_i32 m0, s93, 0x2000
	s_nop 0
	global_load_lds_dwordx4 v[222:223], off
	v_lshl_add_u64 v[222:223], s[64:65], 0, v[130:131]
	s_mov_b32 m0, s59
	s_nop 0
	global_load_lds_dwordx4 v[222:223], off
	s_mov_b32 m0, s67
	s_nop 0
	global_load_lds_dwordx4 v[224:225], off
	ds_read_b128 v[186:189], v157 offset:16384
	ds_read_b128 v[190:193], v157 offset:17408
	ds_read_b128 v[194:197], v157 offset:18432
	ds_read_b128 v[198:201], v157 offset:19456
	ds_read_b128 v[202:205], v157 offset:20480
	ds_read_b128 v[206:209], v157 offset:21504
	ds_read_b128 v[210:213], v157 offset:22528
	ds_read_b128 v[214:217], v157 offset:23552
	s_waitcnt vmcnt(8)
	s_waitcnt lgkmcnt(0)
	s_barrier
; #define PG8_STAGE(bufoff, gbase, voff) do { _Pragma("unroll") for (int _i = 0; _i < 2; ++_i) \
;         __builtin_amdgcn_global_load_lds((const unsigned*)((const char*)(gbase) + (voff)[_i]), (PG8_LAS unsigned*)(lds + (bufoff) + ldsw + _i * 8192), 16, 0, 0); } while (0)
; #define PG8_LDA(dst, b, h) do { _Pragma("unroll") for (int m = 0; m < 4; ++m) _Pragma("unroll") for (int k = 0; k < 2; ++k) dst[m][k] = *(const PG8_LAS bf16x8*)(lds + PG8_SA(b, h) + aoff + m * 2048 + k * 1024); } while (0)
; #define PG8_LDB(dst, b, h) do { _Pragma("unroll") for (int n = 0; n < 2; ++n) _Pragma("unroll") for (int k = 0; k < 2; ++k) dst[n][k] = *(const PG8_LAS bf16x8*)(lds + PG8_SB(b, h) + boff + n * 2048 + k * 1024); } while (0)
; #define PG8_MMA(ai, bj, At, Bt) do { __builtin_amdgcn_s_setprio(1); _Pragma("unroll") for (int m = 0; m < 4; ++m) _Pragma("unroll") for (int n = 0; n < 2; ++n) _Pragma("unroll") for (int k = 0; k < 2; ++k) \
;         acc[ai][bj][m][n] = __builtin_amdgcn_mfma_f32_16x16x32_bf16(Bt[n][k], At[m][k], acc[ai][bj][m][n], 0, 0, 0); __builtin_amdgcn_s_setprio(0); } while (0)
; #define PG8_WAIT_V(n) asm volatile("s_waitcnt vmcnt(" #n ")" ::: "memory")
; #define PG8_WAIT_L(n) asm volatile("s_waitcnt lgkmcnt(" #n ")" ::: "memory")
; #define PG8_BAR __builtin_amdgcn_s_barrier()
; #define PG8_SCHED __builtin_amdgcn_sched_barrier(0)
; template <class Epi, class Sched, bool ALIGN_EPI = false>
; __device__ __forceinline__ void gemm_phase(PG8_LAS unsigned char* lds, const Gemm g, const Sched& S, const Epi& E) {
;     ...
;             PG8_WAIT_V(8); PG8_WAIT_L(0); PG8_BAR; PG8_MMA(1, 0, At, B0); PG8_MMA(1, 1, At, B1); PG8_BAR; PG8_SCHED;
;             PG8_LDB(B0, 1, 0); PG8_LDB(B1, 1, 1); PG8_SCHED; PG8_LDA(At, 1, 0); PG8_STAGE(PG8_SA(0, 1), a2 + hstepA, w1);
;             PG8_WAIT_V(8); PG8_WAIT_L(0); PG8_BAR; PG8_MMA(0, 0, At, B0); PG8_MMA(0, 1, At, B1); PG8_BAR; PG8_SCHED;
	v_mfma_f32_16x16x32_bf16 v[54:57], v[142:145], v[186:189], v[54:57]
	v_mfma_f32_16x16x32_bf16 v[42:45], v[162:165], v[186:189], v[42:45]
	v_mfma_f32_16x16x32_bf16 v[30:33], v[142:145], v[194:197], v[30:33]
	v_mfma_f32_16x16x32_bf16 v[26:29], v[162:165], v[194:197], v[26:29]
	v_mfma_f32_16x16x32_bf16 v[14:17], v[142:145], v[202:205], v[14:17]
	v_mfma_f32_16x16x32_bf16 v[10:13], v[162:165], v[202:205], v[10:13]
	v_mfma_f32_16x16x32_bf16 v[6:9], v[142:145], v[210:213], v[6:9]
	v_mfma_f32_16x16x32_bf16 v[2:5], v[162:165], v[210:213], v[2:5]
	v_mfma_f32_16x16x32_bf16 v[54:57], v[158:161], v[190:193], v[54:57]
	v_mfma_f32_16x16x32_bf16 v[42:45], v[166:169], v[190:193], v[42:45]
	v_mfma_f32_16x16x32_bf16 v[30:33], v[158:161], v[198:201], v[30:33]
	v_mfma_f32_16x16x32_bf16 v[26:29], v[166:169], v[198:201], v[26:29]
	v_mfma_f32_16x16x32_bf16 v[14:17], v[158:161], v[206:209], v[14:17]
	v_mfma_f32_16x16x32_bf16 v[10:13], v[166:169], v[206:209], v[10:13]
	v_mfma_f32_16x16x32_bf16 v[6:9], v[158:161], v[214:217], v[6:9]
	v_mfma_f32_16x16x32_bf16 v[2:5], v[166:169], v[214:217], v[2:5]
	v_mfma_f32_16x16x32_bf16 v[70:73], v[170:173], v[186:189], v[70:73]
	v_mfma_f32_16x16x32_bf16 v[66:69], v[178:181], v[186:189], v[66:69]
	v_mfma_f32_16x16x32_bf16 v[50:53], v[170:173], v[194:197], v[50:53]
	v_mfma_f32_16x16x32_bf16 v[46:49], v[178:181], v[194:197], v[46:49]
	v_mfma_f32_16x16x32_bf16 v[38:41], v[170:173], v[202:205], v[38:41]
	v_mfma_f32_16x16x32_bf16 v[34:37], v[178:181], v[202:205], v[34:37]
	v_mfma_f32_16x16x32_bf16 v[22:25], v[170:173], v[210:213], v[22:25]
	v_mfma_f32_16x16x32_bf16 v[18:21], v[178:181], v[210:213], v[18:21]
	v_mfma_f32_16x16x32_bf16 v[70:73], v[174:177], v[190:193], v[70:73]
	v_mfma_f32_16x16x32_bf16 v[66:69], v[182:185], v[190:193], v[66:69]
	v_mfma_f32_16x16x32_bf16 v[50:53], v[174:177], v[198:201], v[50:53]
	v_mfma_f32_16x16x32_bf16 v[46:49], v[182:185], v[198:201], v[46:49]
	v_mfma_f32_16x16x32_bf16 v[38:41], v[174:177], v[206:209], v[38:41]
	v_mfma_f32_16x16x32_bf16 v[34:37], v[182:185], v[206:209], v[34:37]
	v_mfma_f32_16x16x32_bf16 v[22:25], v[174:177], v[214:217], v[22:25]
	v_mfma_f32_16x16x32_bf16 v[18:21], v[182:185], v[214:217], v[18:21]
	s_barrier
	s_add_i32 s93, 0, 0x18000
	s_add_i32 s94, 0, 0x1c000
	s_add_u32 s64, s64, 0x20000
	s_addc_u32 s65, s65, 0
	s_mov_b32 m0, s68
	v_lshl_add_u64 v[226:227], s[64:65], 0, v[130:131]
	global_load_lds_dwordx4 v[226:227], off
	v_lshl_add_u64 v[226:227], s[64:65], 0, v[134:135]
	s_mov_b32 m0, s69
	s_nop 0
	global_load_lds_dwordx4 v[226:227], off
	v_add_u32_e32 v166, s93, v147
	v_add_u32_e32 v182, s94, v147
	ds_read_b128 v[142:145], v166
	ds_read_b128 v[158:161], v166 offset:1024
	ds_read_b128 v[162:165], v166 offset:2048
	ds_read_b128 v[166:169], v166 offset:3072
	ds_read_b128 v[170:173], v182
	ds_read_b128 v[174:177], v182 offset:1024
	ds_read_b128 v[178:181], v182 offset:2048
	ds_read_b128 v[182:185], v182 offset:3072
	ds_read_b128 v[186:189], v157 offset:32768
	ds_read_b128 v[190:193], v157 offset:33792
	ds_read_b128 v[194:197], v157 offset:34816
	ds_read_b128 v[198:201], v157 offset:35840
	ds_read_b128 v[202:205], v157 offset:36864
	ds_read_b128 v[206:209], v157 offset:37888
	ds_read_b128 v[210:213], v157 offset:38912
	ds_read_b128 v[214:217], v157 offset:39936
	s_waitcnt vmcnt(8)
	s_waitcnt lgkmcnt(0)
	s_barrier
	v_mfma_f32_16x16x32_bf16 v[126:129], v[142:145], v[186:189], v[126:129]
	v_mfma_f32_16x16x32_bf16 v[122:125], v[162:165], v[186:189], v[122:125]
	v_mfma_f32_16x16x32_bf16 v[114:117], v[142:145], v[194:197], v[114:117]
	v_mfma_f32_16x16x32_bf16 v[106:109], v[162:165], v[194:197], v[106:109]
	v_mfma_f32_16x16x32_bf16 v[98:101], v[142:145], v[202:205], v[98:101]
	v_mfma_f32_16x16x32_bf16 v[90:93], v[162:165], v[202:205], v[90:93]
	v_mfma_f32_16x16x32_bf16 v[82:85], v[142:145], v[210:213], v[82:85]
	v_mfma_f32_16x16x32_bf16 v[74:77], v[162:165], v[210:213], v[74:77]
	v_mfma_f32_16x16x32_bf16 v[126:129], v[158:161], v[190:193], v[126:129]
	v_mfma_f32_16x16x32_bf16 v[122:125], v[166:169], v[190:193], v[122:125]
	v_mfma_f32_16x16x32_bf16 v[114:117], v[158:161], v[198:201], v[114:117]
	v_mfma_f32_16x16x32_bf16 v[106:109], v[166:169], v[198:201], v[106:109]
	v_mfma_f32_16x16x32_bf16 v[98:101], v[158:161], v[206:209], v[98:101]
	v_mfma_f32_16x16x32_bf16 v[90:93], v[166:169], v[206:209], v[90:93]
	v_mfma_f32_16x16x32_bf16 v[82:85], v[158:161], v[214:217], v[82:85]
	v_mfma_f32_16x16x32_bf16 v[74:77], v[166:169], v[214:217], v[74:77]
	v_mfma_f32_16x16x32_bf16 v[118:121], v[170:173], v[186:189], v[118:121]
	v_mfma_f32_16x16x32_bf16 v[110:113], v[178:181], v[186:189], v[110:113]
	v_mfma_f32_16x16x32_bf16 v[102:105], v[170:173], v[194:197], v[102:105]
	v_mfma_f32_16x16x32_bf16 v[94:97], v[178:181], v[194:197], v[94:97]
	v_mfma_f32_16x16x32_bf16 v[86:89], v[170:173], v[202:205], v[86:89]
	v_mfma_f32_16x16x32_bf16 v[78:81], v[178:181], v[202:205], v[78:81]
	v_mfma_f32_16x16x32_bf16 v[62:65], v[170:173], v[210:213], v[62:65]
	v_mfma_f32_16x16x32_bf16 v[58:61], v[178:181], v[210:213], v[58:61]
	v_mfma_f32_16x16x32_bf16 v[118:121], v[174:177], v[190:193], v[118:121]
	v_mfma_f32_16x16x32_bf16 v[110:113], v[182:185], v[190:193], v[110:113]
	v_mfma_f32_16x16x32_bf16 v[102:105], v[174:177], v[198:201], v[102:105]
	v_mfma_f32_16x16x32_bf16 v[94:97], v[182:185], v[198:201], v[94:97]
	v_mfma_f32_16x16x32_bf16 v[86:89], v[174:177], v[206:209], v[86:89]
	v_mfma_f32_16x16x32_bf16 v[78:81], v[182:185], v[206:209], v[78:81]
	v_mfma_f32_16x16x32_bf16 v[62:65], v[174:177], v[214:217], v[62:65]
	v_mfma_f32_16x16x32_bf16 v[58:61], v[182:185], v[214:217], v[58:61]
	s_barrier
; #define PG8_STAGE(bufoff, gbase, voff) do { _Pragma("unroll") for (int _i = 0; _i < 2; ++_i) \
;         __builtin_amdgcn_global_load_lds((const unsigned*)((const char*)(gbase) + (voff)[_i]), (PG8_LAS unsigned*)(lds + (bufoff) + ldsw + _i * 8192), 16, 0, 0); } while (0)
; #define PG8_LDA(dst, b, h) do { _Pragma("unroll") for (int m = 0; m < 4; ++m) _Pragma("unroll") for (int k = 0; k < 2; ++k) dst[m][k] = *(const PG8_LAS bf16x8*)(lds + PG8_SA(b, h) + aoff + m * 2048 + k * 1024); } while (0)
; #define PG8_MMA(ai, bj, At, Bt) do { __builtin_amdgcn_s_setprio(1); _Pragma("unroll") for (int m = 0; m < 4; ++m) _Pragma("unroll") for (int n = 0; n < 2; ++n) _Pragma("unroll") for (int k = 0; k < 2; ++k) \
;         acc[ai][bj][m][n] = __builtin_amdgcn_mfma_f32_16x16x32_bf16(Bt[n][k], At[m][k], acc[ai][bj][m][n], 0, 0, 0); __builtin_amdgcn_s_setprio(0); } while (0)
; #define PG8_WAIT_V(n) asm volatile("s_waitcnt vmcnt(" #n ")" ::: "memory")
; #define PG8_WAIT_L(n) asm volatile("s_waitcnt lgkmcnt(" #n ")" ::: "memory")
; #define PG8_BAR __builtin_amdgcn_s_barrier()
; #define PG8_SCHED __builtin_amdgcn_sched_barrier(0)
; template <class Epi, class Sched, bool ALIGN_EPI = false>
; __device__ __forceinline__ void gemm_phase(PG8_LAS unsigned char* lds, const Gemm g, const Sched& S, const Epi& E) {
;     ...
;             PG8_LDA(At, 1, 1); PG8_STAGE(PG8_SB(1, 0), b3, voffB); PG8_STAGE(PG8_SB(1, 1), b3 + hstep, voffB); PG8_STAGE(PG8_SA(1, 0), a3, w0);
;             PG8_WAIT_V(8); PG8_WAIT_L(0); PG8_BAR; PG8_MMA(1, 0, At, B0); PG8_MMA(1, 1, At, B1); PG8_BAR; PG8_SCHED;
;             if constexpr (Epi::KSCALE) { if (((t + 2) & 7) == 0 && t + 2 < nt) { E.kscale(acc, pf, ((t + 2) >> 3) - 1, wr, fr); PG8_SCHED; } }
;         }
	s_add_i32 s64, s93, s66
	v_lshl_add_u64 v[218:219], v[218:219], 0, s[18:19]
	s_mov_b32 m0, s64
	s_nop 0
	global_load_lds_dwordx4 v[218:219], off
	s_add_i32 m0, s64, 0x2000
	s_add_u32 s62, s62, 0x20080
	v_lshl_add_u64 v[218:219], v[220:221], 0, s[18:19]
	s_addc_u32 s63, s63, 0
	s_add_i32 s64, s94, s66
	global_load_lds_dwordx4 v[218:219], off
	v_lshl_add_u64 v[218:219], s[62:63], 0, v[132:133]
	s_mov_b32 m0, s64
	s_nop 0
	global_load_lds_dwordx4 v[218:219], off
	v_lshl_add_u64 v[218:219], s[62:63], 0, v[136:137]
	s_add_i32 m0, s64, 0x2000
	s_nop 0
	global_load_lds_dwordx4 v[218:219], off
	v_lshl_add_u64 v[218:219], v[222:223], 0, s[18:19]
	s_mov_b32 m0, s73
	s_nop 0
	global_load_lds_dwordx4 v[218:219], off
	v_lshl_add_u64 v[218:219], v[224:225], 0, s[18:19]
	s_mov_b32 m0, s74
	s_nop 0
	global_load_lds_dwordx4 v[218:219], off
	ds_read_b128 v[186:189], v157 offset:49152
	ds_read_b128 v[190:193], v157 offset:50176
	ds_read_b128 v[194:197], v157 offset:51200
	ds_read_b128 v[198:201], v157 offset:52224
	ds_read_b128 v[202:205], v157 offset:53248
	ds_read_b128 v[206:209], v157 offset:54272
	ds_read_b128 v[210:213], v157 offset:55296
	ds_read_b128 v[214:217], v157 offset:56320
	s_waitcnt vmcnt(8)
	s_waitcnt lgkmcnt(0)
	s_barrier
	v_mfma_f32_16x16x32_bf16 v[54:57], v[142:145], v[186:189], v[54:57]
	v_mfma_f32_16x16x32_bf16 v[42:45], v[162:165], v[186:189], v[42:45]
	v_mfma_f32_16x16x32_bf16 v[30:33], v[142:145], v[194:197], v[30:33]
	v_mfma_f32_16x16x32_bf16 v[26:29], v[162:165], v[194:197], v[26:29]
	v_mfma_f32_16x16x32_bf16 v[14:17], v[142:145], v[202:205], v[14:17]
	v_mfma_f32_16x16x32_bf16 v[10:13], v[162:165], v[202:205], v[10:13]
	v_mfma_f32_16x16x32_bf16 v[6:9], v[142:145], v[210:213], v[6:9]
	v_mfma_f32_16x16x32_bf16 v[2:5], v[162:165], v[210:213], v[2:5]
	v_mfma_f32_16x16x32_bf16 v[54:57], v[158:161], v[190:193], v[54:57]
	v_mfma_f32_16x16x32_bf16 v[42:45], v[166:169], v[190:193], v[42:45]
	v_mfma_f32_16x16x32_bf16 v[30:33], v[158:161], v[198:201], v[30:33]
	v_mfma_f32_16x16x32_bf16 v[26:29], v[166:169], v[198:201], v[26:29]
	v_mfma_f32_16x16x32_bf16 v[14:17], v[158:161], v[206:209], v[14:17]
	v_mfma_f32_16x16x32_bf16 v[10:13], v[166:169], v[206:209], v[10:13]
	v_mfma_f32_16x16x32_bf16 v[6:9], v[158:161], v[214:217], v[6:9]
	v_mfma_f32_16x16x32_bf16 v[2:5], v[166:169], v[214:217], v[2:5]
	v_mfma_f32_16x16x32_bf16 v[70:73], v[170:173], v[186:189], v[70:73]
	v_mfma_f32_16x16x32_bf16 v[66:69], v[178:181], v[186:189], v[66:69]
	v_mfma_f32_16x16x32_bf16 v[50:53], v[170:173], v[194:197], v[50:53]
	v_mfma_f32_16x16x32_bf16 v[46:49], v[178:181], v[194:197], v[46:49]
	v_mfma_f32_16x16x32_bf16 v[38:41], v[170:173], v[202:205], v[38:41]
	v_mfma_f32_16x16x32_bf16 v[34:37], v[178:181], v[202:205], v[34:37]
	v_mfma_f32_16x16x32_bf16 v[22:25], v[170:173], v[210:213], v[22:25]
	v_mfma_f32_16x16x32_bf16 v[18:21], v[178:181], v[210:213], v[18:21]
	v_mfma_f32_16x16x32_bf16 v[70:73], v[174:177], v[190:193], v[70:73]
	v_mfma_f32_16x16x32_bf16 v[66:69], v[182:185], v[190:193], v[66:69]
	v_mfma_f32_16x16x32_bf16 v[50:53], v[174:177], v[198:201], v[50:53]
	v_mfma_f32_16x16x32_bf16 v[46:49], v[182:185], v[198:201], v[46:49]
	v_mfma_f32_16x16x32_bf16 v[38:41], v[174:177], v[206:209], v[38:41]
	v_mfma_f32_16x16x32_bf16 v[34:37], v[182:185], v[206:209], v[34:37]
	v_mfma_f32_16x16x32_bf16 v[22:25], v[174:177], v[214:217], v[22:25]
	v_mfma_f32_16x16x32_bf16 v[18:21], v[182:185], v[214:217], v[18:21]
	s_barrier
	s_add_i32 s92, s92, 2
	s_add_u32 s90, s90, 0x100
	s_addc_u32 s91, s91, 0
	s_add_u32 s60, s60, 0x100
	s_addc_u32 s61, s61, 0
	s_cmp_gt_u32 s92, 5
	s_cbranch_scc0 .LBB0_805
	s_and_b64 vcc, exec, s[22:23]
	s_cbranch_vccz .LBB0_808
	s_barrier

; #define PG8_STAGE(bufoff, gbase, voff) do { _Pragma("unroll") for (int _i = 0; _i < 2; ++_i) \
;         __builtin_amdgcn_global_load_lds((const unsigned*)((const char*)(gbase) + (voff)[_i]), (PG8_LAS unsigned*)(lds + (bufoff) + ldsw + _i * 8192), 16, 0, 0); } while (0)
; #define PG8_LDA(dst, b, h) do { _Pragma("unroll") for (int m = 0; m < 4; ++m) _Pragma("unroll") for (int k = 0; k < 2; ++k) dst[m][k] = *(const PG8_LAS bf16x8*)(lds + PG8_SA(b, h) + aoff + m * 2048 + k * 1024); } while (0)
; #define PG8_LDB(dst, b, h) do { _Pragma("unroll") for (int n = 0; n < 2; ++n) _Pragma("unroll") for (int k = 0; k < 2; ++k) dst[n][k] = *(const PG8_LAS bf16x8*)(lds + PG8_SB(b, h) + boff + n * 2048 + k * 1024); } while (0)
; #define PG8_MMA(ai, bj, At, Bt) do { __builtin_amdgcn_s_setprio(1); _Pragma("unroll") for (int m = 0; m < 4; ++m) _Pragma("unroll") for (int n = 0; n < 2; ++n) _Pragma("unroll") for (int k = 0; k < 2; ++k) \
;         acc[ai][bj][m][n] = __builtin_amdgcn_mfma_f32_16x16x32_bf16(Bt[n][k], At[m][k], acc[ai][bj][m][n], 0, 0, 0); __builtin_amdgcn_s_setprio(0); } while (0)
; #define PG8_BAR __builtin_amdgcn_s_barrier()
; template <class Epi, class Sched, bool ALIGN_EPI = false>
; __device__ __forceinline__ void gemm_phase(PG8_LAS unsigned char* lds, const Gemm g, const Sched& S, const Epi& E) {
;     ...
;             const bool last = (t == nt - 2);
;             const char* a1 = cA + (size_t)(t + 1) * kstep;
;             const char* a2 = last ? nA : cA + (size_t)(t + 2) * kstep; const char* b2 = last ? nB : cB + (size_t)(t + 2) * kstep;
;             const char* a3 = a2 + kstep; const char* b3 = b2 + kstep;
;             unsigned w0[2], w1[2];
; #pragma unroll
;             for (int i = 0; i < 2; ++i) { w0[i] = (Sched::GATHER && last) ? vn0[i] : vc0[i]; w1[i] = (Sched::GATHER && last) ? vn1[i] : vc1[i]; }
;             if (last && has_next) S.a_ready(nxt);
;             PG8_LDB(B0, 0, 0); PG8_LDB(B1, 0, 1); PG8_SCHED; PG8_LDA(At, 0, 0); PG8_STAGE(PG8_SA(1, 1), a1 + hstepA, vc1);
;             PG8_WAIT_V(8); PG8_WAIT_L(0); PG8_BAR; PG8_MMA(0, 0, At, B0); PG8_MMA(0, 1, At, B1); PG8_BAR; PG8_SCHED;
;             PG8_LDA(At, 0, 1); PG8_STAGE(PG8_SB(0, 0), b2, voffB); PG8_STAGE(PG8_SB(0, 1), b2 + hstep, voffB); PG8_STAGE(PG8_SA(0, 0), a2, w0);
;             PG8_WAIT_V(8); PG8_WAIT_L(0); PG8_BAR; PG8_MMA(1, 0, At, B0); PG8_MMA(1, 1, At, B1); PG8_BAR; PG8_SCHED;
.LBB0_908:
	s_add_u32 s58, s56, 0xfffe0080
	s_addc_u32 s59, s57, -1
	s_cmp_eq_u32 s92, 4
	s_cselect_b32 s61, s41, s59
	s_cselect_b32 s60, s47, s58
	s_cselect_b32 s59, s43, s91
	s_cselect_b32 s58, s89, s90
	v_lshl_add_u64 v[220:221], s[56:57], 0, v[142:143]
	s_add_i32 m0, s49, 0xc000
	s_nop 0
	global_load_lds_dwordx4 v[220:221], off
	v_lshl_add_u64 v[220:221], s[56:57], 0, v[140:141]
	s_add_i32 m0, s49, 0xe000
	s_nop 0
	global_load_lds_dwordx4 v[220:221], off
	ds_read_b128 v[144:147], v157
	ds_read_b128 v[160:163], v157 offset:1024
	ds_read_b128 v[164:167], v157 offset:2048
	ds_read_b128 v[168:171], v157 offset:3072
	ds_read_b128 v[172:175], v158
	ds_read_b128 v[176:179], v158 offset:1024
	ds_read_b128 v[180:183], v158 offset:2048
	ds_read_b128 v[184:187], v158 offset:3072
	ds_read_b128 v[188:191], v159
	ds_read_b128 v[192:195], v159 offset:1024
	ds_read_b128 v[196:199], v159 offset:2048
	ds_read_b128 v[200:203], v159 offset:3072
	ds_read_b128 v[204:207], v159 offset:4096
	ds_read_b128 v[208:211], v159 offset:5120
	ds_read_b128 v[212:215], v159 offset:6144
	ds_read_b128 v[216:219], v159 offset:7168
	s_waitcnt vmcnt(8)
	s_waitcnt lgkmcnt(0)
	s_barrier
	v_mfma_f32_16x16x32_bf16 v[126:129], v[144:147], v[188:191], v[126:129]
	v_mfma_f32_16x16x32_bf16 v[122:125], v[164:167], v[188:191], v[122:125]
	v_mfma_f32_16x16x32_bf16 v[114:117], v[144:147], v[196:199], v[114:117]
	v_mfma_f32_16x16x32_bf16 v[106:109], v[164:167], v[196:199], v[106:109]
	v_mfma_f32_16x16x32_bf16 v[98:101], v[144:147], v[204:207], v[98:101]
	v_mfma_f32_16x16x32_bf16 v[90:93], v[164:167], v[204:207], v[90:93]
	v_mfma_f32_16x16x32_bf16 v[82:85], v[144:147], v[212:215], v[82:85]
	v_mfma_f32_16x16x32_bf16 v[74:77], v[164:167], v[212:215], v[74:77]
	v_mfma_f32_16x16x32_bf16 v[126:129], v[160:163], v[192:195], v[126:129]
	v_mfma_f32_16x16x32_bf16 v[122:125], v[168:171], v[192:195], v[122:125]
	v_mfma_f32_16x16x32_bf16 v[114:117], v[160:163], v[200:203], v[114:117]
	v_mfma_f32_16x16x32_bf16 v[106:109], v[168:171], v[200:203], v[106:109]
	v_mfma_f32_16x16x32_bf16 v[98:101], v[160:163], v[208:211], v[98:101]
	v_mfma_f32_16x16x32_bf16 v[90:93], v[168:171], v[208:211], v[90:93]
	v_mfma_f32_16x16x32_bf16 v[82:85], v[160:163], v[216:219], v[82:85]
	v_mfma_f32_16x16x32_bf16 v[74:77], v[168:171], v[216:219], v[74:77]
	v_mfma_f32_16x16x32_bf16 v[118:121], v[172:175], v[188:191], v[118:121]
	v_mfma_f32_16x16x32_bf16 v[110:113], v[180:183], v[188:191], v[110:113]
	v_mfma_f32_16x16x32_bf16 v[102:105], v[172:175], v[196:199], v[102:105]
	v_mfma_f32_16x16x32_bf16 v[94:97], v[180:183], v[196:199], v[94:97]
	v_mfma_f32_16x16x32_bf16 v[86:89], v[172:175], v[204:207], v[86:89]
	v_mfma_f32_16x16x32_bf16 v[78:81], v[180:183], v[204:207], v[78:81]
	v_mfma_f32_16x16x32_bf16 v[62:65], v[172:175], v[212:215], v[62:65]
	v_mfma_f32_16x16x32_bf16 v[58:61], v[180:183], v[212:215], v[58:61]
	v_mfma_f32_16x16x32_bf16 v[118:121], v[176:179], v[192:195], v[118:121]
	v_mfma_f32_16x16x32_bf16 v[110:113], v[184:187], v[192:195], v[110:113]
	v_mfma_f32_16x16x32_bf16 v[102:105], v[176:179], v[200:203], v[102:105]
	v_mfma_f32_16x16x32_bf16 v[94:97], v[184:187], v[200:203], v[94:97]
	v_mfma_f32_16x16x32_bf16 v[86:89], v[176:179], v[208:211], v[86:89]
	v_mfma_f32_16x16x32_bf16 v[78:81], v[184:187], v[208:211], v[78:81]
	v_mfma_f32_16x16x32_bf16 v[62:65], v[176:179], v[216:219], v[62:65]
	v_mfma_f32_16x16x32_bf16 v[58:61], v[184:187], v[216:219], v[58:61]
	s_barrier
	s_add_i32 s93, s79, s66
	v_lshl_add_u64 v[220:221], s[58:59], 0, v[134:135]
	s_mov_b32 m0, s93
	s_nop 0
	global_load_lds_dwordx4 v[220:221], off
	s_add_i32 m0, s93, 0x2000
	s_add_u32 s94, s58, 0x20000
	v_lshl_add_u64 v[222:223], s[58:59], 0, v[138:139]
	s_addc_u32 s95, s59, 0
	s_add_i32 s93, s80, s66
	global_load_lds_dwordx4 v[222:223], off
	v_lshl_add_u64 v[224:225], s[94:95], 0, v[134:135]
	s_mov_b32 m0, s93
	v_lshl_add_u64 v[226:227], s[60:61], 0, v[136:137]
	global_load_lds_dwordx4 v[224:225], off
	v_lshl_add_u64 v[224:225], s[94:95], 0, v[138:139]
	s_add_i32 m0, s93, 0x2000
	s_nop 0
	global_load_lds_dwordx4 v[224:225], off
	v_lshl_add_u64 v[224:225], s[60:61], 0, v[132:133]
	s_mov_b32 m0, s49
	s_nop 0
	global_load_lds_dwordx4 v[224:225], off
	s_mov_b32 m0, s67
	s_nop 0
	global_load_lds_dwordx4 v[226:227], off
	ds_read_b128 v[188:191], v159 offset:16384
	ds_read_b128 v[192:195], v159 offset:17408
	ds_read_b128 v[196:199], v159 offset:18432
	ds_read_b128 v[200:203], v159 offset:19456
	ds_read_b128 v[204:207], v159 offset:20480
	ds_read_b128 v[208:211], v159 offset:21504
	ds_read_b128 v[212:215], v159 offset:22528
	ds_read_b128 v[216:219], v159 offset:23552
	s_waitcnt vmcnt(8)
	s_waitcnt lgkmcnt(0)
	s_barrier
; #define PG8_STAGE(bufoff, gbase, voff) do { _Pragma("unroll") for (int _i = 0; _i < 2; ++_i) \
;         __builtin_amdgcn_global_load_lds((const unsigned*)((const char*)(gbase) + (voff)[_i]), (PG8_LAS unsigned*)(lds + (bufoff) + ldsw + _i * 8192), 16, 0, 0); } while (0)
; #define PG8_LDA(dst, b, h) do { _Pragma("unroll") for (int m = 0; m < 4; ++m) _Pragma("unroll") for (int k = 0; k < 2; ++k) dst[m][k] = *(const PG8_LAS bf16x8*)(lds + PG8_SA(b, h) + aoff + m * 2048 + k * 1024); } while (0)
; #define PG8_LDB(dst, b, h) do { _Pragma("unroll") for (int n = 0; n < 2; ++n) _Pragma("unroll") for (int k = 0; k < 2; ++k) dst[n][k] = *(const PG8_LAS bf16x8*)(lds + PG8_SB(b, h) + boff + n * 2048 + k * 1024); } while (0)
; #define PG8_MMA(ai, bj, At, Bt) do { __builtin_amdgcn_s_setprio(1); _Pragma("unroll") for (int m = 0; m < 4; ++m) _Pragma("unroll") for (int n = 0; n < 2; ++n) _Pragma("unroll") for (int k = 0; k < 2; ++k) \
;         acc[ai][bj][m][n] = __builtin_amdgcn_mfma_f32_16x16x32_bf16(Bt[n][k], At[m][k], acc[ai][bj][m][n], 0, 0, 0); __builtin_amdgcn_s_setprio(0); } while (0)
; #define PG8_WAIT_V(n) asm volatile("s_waitcnt vmcnt(" #n ")" ::: "memory")
; #define PG8_WAIT_L(n) asm volatile("s_waitcnt lgkmcnt(" #n ")" ::: "memory")
; #define PG8_BAR __builtin_amdgcn_s_barrier()
; #define PG8_SCHED __builtin_amdgcn_sched_barrier(0)
; template <class Epi, class Sched, bool ALIGN_EPI = false>
; __device__ __forceinline__ void gemm_phase(PG8_LAS unsigned char* lds, const Gemm g, const Sched& S, const Epi& E) {
;     ...
;             PG8_WAIT_V(8); PG8_WAIT_L(0); PG8_BAR; PG8_MMA(1, 0, At, B0); PG8_MMA(1, 1, At, B1); PG8_BAR; PG8_SCHED;
;             PG8_LDB(B0, 1, 0); PG8_LDB(B1, 1, 1); PG8_SCHED; PG8_LDA(At, 1, 0); PG8_STAGE(PG8_SA(0, 1), a2 + hstepA, w1);
;             PG8_WAIT_V(8); PG8_WAIT_L(0); PG8_BAR; PG8_MMA(0, 0, At, B0); PG8_MMA(0, 1, At, B1); PG8_BAR; PG8_SCHED;
	v_mfma_f32_16x16x32_bf16 v[54:57], v[144:147], v[188:191], v[54:57]
	v_mfma_f32_16x16x32_bf16 v[42:45], v[164:167], v[188:191], v[42:45]
	v_mfma_f32_16x16x32_bf16 v[30:33], v[144:147], v[196:199], v[30:33]
	v_mfma_f32_16x16x32_bf16 v[26:29], v[164:167], v[196:199], v[26:29]
	v_mfma_f32_16x16x32_bf16 v[14:17], v[144:147], v[204:207], v[14:17]
	v_mfma_f32_16x16x32_bf16 v[10:13], v[164:167], v[204:207], v[10:13]
	v_mfma_f32_16x16x32_bf16 v[6:9], v[144:147], v[212:215], v[6:9]
	v_mfma_f32_16x16x32_bf16 v[2:5], v[164:167], v[212:215], v[2:5]
	v_mfma_f32_16x16x32_bf16 v[54:57], v[160:163], v[192:195], v[54:57]
	v_mfma_f32_16x16x32_bf16 v[42:45], v[168:171], v[192:195], v[42:45]
	v_mfma_f32_16x16x32_bf16 v[30:33], v[160:163], v[200:203], v[30:33]
	v_mfma_f32_16x16x32_bf16 v[26:29], v[168:171], v[200:203], v[26:29]
	v_mfma_f32_16x16x32_bf16 v[14:17], v[160:163], v[208:211], v[14:17]
	v_mfma_f32_16x16x32_bf16 v[10:13], v[168:171], v[208:211], v[10:13]
	v_mfma_f32_16x16x32_bf16 v[6:9], v[160:163], v[216:219], v[6:9]
	v_mfma_f32_16x16x32_bf16 v[2:5], v[168:171], v[216:219], v[2:5]
	v_mfma_f32_16x16x32_bf16 v[70:73], v[172:175], v[188:191], v[70:73]
	v_mfma_f32_16x16x32_bf16 v[66:69], v[180:183], v[188:191], v[66:69]
	v_mfma_f32_16x16x32_bf16 v[50:53], v[172:175], v[196:199], v[50:53]
	v_mfma_f32_16x16x32_bf16 v[46:49], v[180:183], v[196:199], v[46:49]
	v_mfma_f32_16x16x32_bf16 v[38:41], v[172:175], v[204:207], v[38:41]
	v_mfma_f32_16x16x32_bf16 v[34:37], v[180:183], v[204:207], v[34:37]
	v_mfma_f32_16x16x32_bf16 v[22:25], v[172:175], v[212:215], v[22:25]
	v_mfma_f32_16x16x32_bf16 v[18:21], v[180:183], v[212:215], v[18:21]
	v_mfma_f32_16x16x32_bf16 v[70:73], v[176:179], v[192:195], v[70:73]
	v_mfma_f32_16x16x32_bf16 v[66:69], v[184:187], v[192:195], v[66:69]
	v_mfma_f32_16x16x32_bf16 v[50:53], v[176:179], v[200:203], v[50:53]
	v_mfma_f32_16x16x32_bf16 v[46:49], v[184:187], v[200:203], v[46:49]
	v_mfma_f32_16x16x32_bf16 v[38:41], v[176:179], v[208:211], v[38:41]
	v_mfma_f32_16x16x32_bf16 v[34:37], v[184:187], v[208:211], v[34:37]
	v_mfma_f32_16x16x32_bf16 v[22:25], v[176:179], v[216:219], v[22:25]
	v_mfma_f32_16x16x32_bf16 v[18:21], v[184:187], v[216:219], v[18:21]
	s_barrier
	s_add_i32 s93, 0, 0x18000
	s_add_i32 s94, 0, 0x1c000
	s_add_u32 s60, s60, 0x20000
	s_addc_u32 s61, s61, 0
	s_mov_b32 m0, s68
	v_lshl_add_u64 v[228:229], s[60:61], 0, v[132:133]
	global_load_lds_dwordx4 v[228:229], off
	v_lshl_add_u64 v[228:229], s[60:61], 0, v[136:137]
	s_mov_b32 m0, s69
	s_nop 0
	global_load_lds_dwordx4 v[228:229], off
	v_add_u32_e32 v168, s93, v148
	v_add_u32_e32 v184, s94, v148
	ds_read_b128 v[144:147], v168
	ds_read_b128 v[160:163], v168 offset:1024
	ds_read_b128 v[164:167], v168 offset:2048
	ds_read_b128 v[168:171], v168 offset:3072
	ds_read_b128 v[172:175], v184
	ds_read_b128 v[176:179], v184 offset:1024
	ds_read_b128 v[180:183], v184 offset:2048
	ds_read_b128 v[184:187], v184 offset:3072
	ds_read_b128 v[188:191], v159 offset:32768
	ds_read_b128 v[192:195], v159 offset:33792
	ds_read_b128 v[196:199], v159 offset:34816
	ds_read_b128 v[200:203], v159 offset:35840
	ds_read_b128 v[204:207], v159 offset:36864
	ds_read_b128 v[208:211], v159 offset:37888
	ds_read_b128 v[212:215], v159 offset:38912
	ds_read_b128 v[216:219], v159 offset:39936
	s_waitcnt vmcnt(8)
	s_waitcnt lgkmcnt(0)
	s_barrier
	v_mfma_f32_16x16x32_bf16 v[126:129], v[144:147], v[188:191], v[126:129]
	v_mfma_f32_16x16x32_bf16 v[122:125], v[164:167], v[188:191], v[122:125]
	v_mfma_f32_16x16x32_bf16 v[114:117], v[144:147], v[196:199], v[114:117]
	v_mfma_f32_16x16x32_bf16 v[106:109], v[164:167], v[196:199], v[106:109]
	v_mfma_f32_16x16x32_bf16 v[98:101], v[144:147], v[204:207], v[98:101]
	v_mfma_f32_16x16x32_bf16 v[90:93], v[164:167], v[204:207], v[90:93]
	v_mfma_f32_16x16x32_bf16 v[82:85], v[144:147], v[212:215], v[82:85]
	v_mfma_f32_16x16x32_bf16 v[74:77], v[164:167], v[212:215], v[74:77]
	v_mfma_f32_16x16x32_bf16 v[126:129], v[160:163], v[192:195], v[126:129]
	v_mfma_f32_16x16x32_bf16 v[122:125], v[168:171], v[192:195], v[122:125]
	v_mfma_f32_16x16x32_bf16 v[114:117], v[160:163], v[200:203], v[114:117]
	v_mfma_f32_16x16x32_bf16 v[106:109], v[168:171], v[200:203], v[106:109]
	v_mfma_f32_16x16x32_bf16 v[98:101], v[160:163], v[208:211], v[98:101]
	v_mfma_f32_16x16x32_bf16 v[90:93], v[168:171], v[208:211], v[90:93]
	v_mfma_f32_16x16x32_bf16 v[82:85], v[160:163], v[216:219], v[82:85]
	v_mfma_f32_16x16x32_bf16 v[74:77], v[168:171], v[216:219], v[74:77]
	v_mfma_f32_16x16x32_bf16 v[118:121], v[172:175], v[188:191], v[118:121]
	v_mfma_f32_16x16x32_bf16 v[110:113], v[180:183], v[188:191], v[110:113]
	v_mfma_f32_16x16x32_bf16 v[102:105], v[172:175], v[196:199], v[102:105]
	v_mfma_f32_16x16x32_bf16 v[94:97], v[180:183], v[196:199], v[94:97]
	v_mfma_f32_16x16x32_bf16 v[86:89], v[172:175], v[204:207], v[86:89]
	v_mfma_f32_16x16x32_bf16 v[78:81], v[180:183], v[204:207], v[78:81]
	v_mfma_f32_16x16x32_bf16 v[62:65], v[172:175], v[212:215], v[62:65]
	v_mfma_f32_16x16x32_bf16 v[58:61], v[180:183], v[212:215], v[58:61]
	v_mfma_f32_16x16x32_bf16 v[118:121], v[176:179], v[192:195], v[118:121]
	v_mfma_f32_16x16x32_bf16 v[110:113], v[184:187], v[192:195], v[110:113]
	v_mfma_f32_16x16x32_bf16 v[102:105], v[176:179], v[200:203], v[102:105]
	v_mfma_f32_16x16x32_bf16 v[94:97], v[184:187], v[200:203], v[94:97]
	v_mfma_f32_16x16x32_bf16 v[86:89], v[176:179], v[208:211], v[86:89]
	v_mfma_f32_16x16x32_bf16 v[78:81], v[184:187], v[208:211], v[78:81]
	v_mfma_f32_16x16x32_bf16 v[62:65], v[176:179], v[216:219], v[62:65]
	v_mfma_f32_16x16x32_bf16 v[58:61], v[184:187], v[216:219], v[58:61]
	s_barrier
; #define PG8_STAGE(bufoff, gbase, voff) do { _Pragma("unroll") for (int _i = 0; _i < 2; ++_i) \
;         __builtin_amdgcn_global_load_lds((const unsigned*)((const char*)(gbase) + (voff)[_i]), (PG8_LAS unsigned*)(lds + (bufoff) + ldsw + _i * 8192), 16, 0, 0); } while (0)
; #define PG8_LDA(dst, b, h) do { _Pragma("unroll") for (int m = 0; m < 4; ++m) _Pragma("unroll") for (int k = 0; k < 2; ++k) dst[m][k] = *(const PG8_LAS bf16x8*)(lds + PG8_SA(b, h) + aoff + m * 2048 + k * 1024); } while (0)
; #define PG8_MMA(ai, bj, At, Bt) do { __builtin_amdgcn_s_setprio(1); _Pragma("unroll") for (int m = 0; m < 4; ++m) _Pragma("unroll") for (int n = 0; n < 2; ++n) _Pragma("unroll") for (int k = 0; k < 2; ++k) \
;         acc[ai][bj][m][n] = __builtin_amdgcn_mfma_f32_16x16x32_bf16(Bt[n][k], At[m][k], acc[ai][bj][m][n], 0, 0, 0); __builtin_amdgcn_s_setprio(0); } while (0)
; #define PG8_WAIT_V(n) asm volatile("s_waitcnt vmcnt(" #n ")" ::: "memory")
; #define PG8_WAIT_L(n) asm volatile("s_waitcnt lgkmcnt(" #n ")" ::: "memory")
; #define PG8_BAR __builtin_amdgcn_s_barrier()
; #define PG8_SCHED __builtin_amdgcn_sched_barrier(0)
; template <class Epi, class Sched, bool ALIGN_EPI = false>
; __device__ __forceinline__ void gemm_phase(PG8_LAS unsigned char* lds, const Gemm g, const Sched& S, const Epi& E) {
;     ...
;             PG8_LDA(At, 1, 1); PG8_STAGE(PG8_SB(1, 0), b3, voffB); PG8_STAGE(PG8_SB(1, 1), b3 + hstep, voffB); PG8_STAGE(PG8_SA(1, 0), a3, w0);
;             PG8_WAIT_V(8); PG8_WAIT_L(0); PG8_BAR; PG8_MMA(1, 0, At, B0); PG8_MMA(1, 1, At, B1); PG8_BAR; PG8_SCHED;
;             if constexpr (Epi::KSCALE) { if (((t + 2) & 7) == 0 && t + 2 < nt) { E.kscale(acc, pf, ((t + 2) >> 3) - 1, wr, fr); PG8_SCHED; } }
;         }
	s_add_i32 s60, s93, s66
	v_lshl_add_u64 v[220:221], v[220:221], 0, s[14:15]
	s_mov_b32 m0, s60
	s_nop 0
	global_load_lds_dwordx4 v[220:221], off
	s_add_i32 m0, s60, 0x2000
	s_add_u32 s58, s58, 0x20080
	v_lshl_add_u64 v[220:221], v[222:223], 0, s[14:15]
	s_addc_u32 s59, s59, 0
	s_add_i32 s60, s94, s66
	global_load_lds_dwordx4 v[220:221], off
	v_lshl_add_u64 v[220:221], s[58:59], 0, v[134:135]
	s_mov_b32 m0, s60
	s_nop 0
	global_load_lds_dwordx4 v[220:221], off
	v_lshl_add_u64 v[220:221], s[58:59], 0, v[138:139]
	s_add_i32 m0, s60, 0x2000
	s_nop 0
	global_load_lds_dwordx4 v[220:221], off
	v_lshl_add_u64 v[220:221], v[224:225], 0, s[14:15]
	s_mov_b32 m0, s74
	s_nop 0
	global_load_lds_dwordx4 v[220:221], off
	v_lshl_add_u64 v[220:221], v[226:227], 0, s[14:15]
	s_mov_b32 m0, s75
	s_nop 0
	global_load_lds_dwordx4 v[220:221], off
	ds_read_b128 v[188:191], v159 offset:49152
	ds_read_b128 v[192:195], v159 offset:50176
	ds_read_b128 v[196:199], v159 offset:51200
	ds_read_b128 v[200:203], v159 offset:52224
	ds_read_b128 v[204:207], v159 offset:53248
	ds_read_b128 v[208:211], v159 offset:54272
	ds_read_b128 v[212:215], v159 offset:55296
	ds_read_b128 v[216:219], v159 offset:56320
	s_waitcnt vmcnt(8)
	s_waitcnt lgkmcnt(0)
	s_barrier
	v_mfma_f32_16x16x32_bf16 v[54:57], v[144:147], v[188:191], v[54:57]
	v_mfma_f32_16x16x32_bf16 v[42:45], v[164:167], v[188:191], v[42:45]
	v_mfma_f32_16x16x32_bf16 v[30:33], v[144:147], v[196:199], v[30:33]
	v_mfma_f32_16x16x32_bf16 v[26:29], v[164:167], v[196:199], v[26:29]
	v_mfma_f32_16x16x32_bf16 v[14:17], v[144:147], v[204:207], v[14:17]
	v_mfma_f32_16x16x32_bf16 v[10:13], v[164:167], v[204:207], v[10:13]
	v_mfma_f32_16x16x32_bf16 v[6:9], v[144:147], v[212:215], v[6:9]
	v_mfma_f32_16x16x32_bf16 v[2:5], v[164:167], v[212:215], v[2:5]
	v_mfma_f32_16x16x32_bf16 v[54:57], v[160:163], v[192:195], v[54:57]
	v_mfma_f32_16x16x32_bf16 v[42:45], v[168:171], v[192:195], v[42:45]
	v_mfma_f32_16x16x32_bf16 v[30:33], v[160:163], v[200:203], v[30:33]
	v_mfma_f32_16x16x32_bf16 v[26:29], v[168:171], v[200:203], v[26:29]
	v_mfma_f32_16x16x32_bf16 v[14:17], v[160:163], v[208:211], v[14:17]
	v_mfma_f32_16x16x32_bf16 v[10:13], v[168:171], v[208:211], v[10:13]
	v_mfma_f32_16x16x32_bf16 v[6:9], v[160:163], v[216:219], v[6:9]
	v_mfma_f32_16x16x32_bf16 v[2:5], v[168:171], v[216:219], v[2:5]
	v_mfma_f32_16x16x32_bf16 v[70:73], v[172:175], v[188:191], v[70:73]
	v_mfma_f32_16x16x32_bf16 v[66:69], v[180:183], v[188:191], v[66:69]
	v_mfma_f32_16x16x32_bf16 v[50:53], v[172:175], v[196:199], v[50:53]
	v_mfma_f32_16x16x32_bf16 v[46:49], v[180:183], v[196:199], v[46:49]
	v_mfma_f32_16x16x32_bf16 v[38:41], v[172:175], v[204:207], v[38:41]
	v_mfma_f32_16x16x32_bf16 v[34:37], v[180:183], v[204:207], v[34:37]
	v_mfma_f32_16x16x32_bf16 v[22:25], v[172:175], v[212:215], v[22:25]
	v_mfma_f32_16x16x32_bf16 v[18:21], v[180:183], v[212:215], v[18:21]
	v_mfma_f32_16x16x32_bf16 v[70:73], v[176:179], v[192:195], v[70:73]
	v_mfma_f32_16x16x32_bf16 v[66:69], v[184:187], v[192:195], v[66:69]
	v_mfma_f32_16x16x32_bf16 v[50:53], v[176:179], v[200:203], v[50:53]
	v_mfma_f32_16x16x32_bf16 v[46:49], v[184:187], v[200:203], v[46:49]
	v_mfma_f32_16x16x32_bf16 v[38:41], v[176:179], v[208:211], v[38:41]
	v_mfma_f32_16x16x32_bf16 v[34:37], v[184:187], v[208:211], v[34:37]
	v_mfma_f32_16x16x32_bf16 v[22:25], v[176:179], v[216:219], v[22:25]
	v_mfma_f32_16x16x32_bf16 v[18:21], v[184:187], v[216:219], v[18:21]
	s_barrier
	s_add_i32 s92, s92, 2
	s_add_u32 s90, s90, 0x100
	s_addc_u32 s91, s91, 0
	s_add_u32 s56, s56, 0x100
	s_addc_u32 s57, s57, 0
	s_cmp_gt_u32 s92, 5
	s_cbranch_scc0 .LBB0_908
	s_and_b64 vcc, exec, s[16:17]
	s_cbranch_vccz .LBB0_911
	s_barrier

; #define PG8_STAGE(bufoff, gbase, voff) do { _Pragma("unroll") for (int _i = 0; _i < 2; ++_i) \
;         __builtin_amdgcn_global_load_lds((const unsigned*)((const char*)(gbase) + (voff)[_i]), (PG8_LAS unsigned*)(lds + (bufoff) + ldsw + _i * 8192), 16, 0, 0); } while (0)
; #define PG8_LDA(dst, b, h) do { _Pragma("unroll") for (int m = 0; m < 4; ++m) _Pragma("unroll") for (int k = 0; k < 2; ++k) dst[m][k] = *(const PG8_LAS bf16x8*)(lds + PG8_SA(b, h) + aoff + m * 2048 + k * 1024); } while (0)
; #define PG8_LDB(dst, b, h) do { _Pragma("unroll") for (int n = 0; n < 2; ++n) _Pragma("unroll") for (int k = 0; k < 2; ++k) dst[n][k] = *(const PG8_LAS bf16x8*)(lds + PG8_SB(b, h) + boff + n * 2048 + k * 1024); } while (0)
; #define PG8_MMA(ai, bj, At, Bt) do { __builtin_amdgcn_s_setprio(1); _Pragma("unroll") for (int m = 0; m < 4; ++m) _Pragma("unroll") for (int n = 0; n < 2; ++n) _Pragma("unroll") for (int k = 0; k < 2; ++k) \
;         acc[ai][bj][m][n] = __builtin_amdgcn_mfma_f32_16x16x32_bf16(Bt[n][k], At[m][k], acc[ai][bj][m][n], 0, 0, 0); __builtin_amdgcn_s_setprio(0); } while (0)
; #define PG8_BAR __builtin_amdgcn_s_barrier()
; template <class Epi, class Sched, bool ALIGN_EPI = false>
; __device__ __forceinline__ void gemm_phase(PG8_LAS unsigned char* lds, const Gemm g, const Sched& S, const Epi& E) {
;     ...
;             const bool last = (t == nt - 2);
;             const char* a1 = cA + (size_t)(t + 1) * kstep;
;             const char* a2 = last ? nA : cA + (size_t)(t + 2) * kstep; const char* b2 = last ? nB : cB + (size_t)(t + 2) * kstep;
;             const char* a3 = a2 + kstep; const char* b3 = b2 + kstep;
;             unsigned w0[2], w1[2];
; #pragma unroll
;             for (int i = 0; i < 2; ++i) { w0[i] = (Sched::GATHER && last) ? vn0[i] : vc0[i]; w1[i] = (Sched::GATHER && last) ? vn1[i] : vc1[i]; }
;             if (last && has_next) S.a_ready(nxt);
;             PG8_LDB(B0, 0, 0); PG8_LDB(B1, 0, 1); PG8_SCHED; PG8_LDA(At, 0, 0); PG8_STAGE(PG8_SA(1, 1), a1 + hstepA, vc1);
;             PG8_WAIT_V(8); PG8_WAIT_L(0); PG8_BAR; PG8_MMA(0, 0, At, B0); PG8_MMA(0, 1, At, B1); PG8_BAR; PG8_SCHED;
;             PG8_LDA(At, 0, 1); PG8_STAGE(PG8_SB(0, 0), b2, voffB); PG8_STAGE(PG8_SB(0, 1), b2 + hstep, voffB); PG8_STAGE(PG8_SA(0, 0), a2, w0);
;             PG8_WAIT_V(8); PG8_WAIT_L(0); PG8_BAR; PG8_MMA(1, 0, At, B0); PG8_MMA(1, 1, At, B1); PG8_BAR; PG8_SCHED;
.LBB0_1055:
	s_add_u32 s56, s54, 0xfff80080
	s_addc_u32 s57, s55, -1
	s_cmp_eq_u32 s83, 28
	s_cselect_b32 s59, s15, s57
	s_cselect_b32 s58, s79, s56
	s_cselect_b32 s57, s49, s82
	s_cselect_b32 s56, s80, s81
	v_lshl_add_u64 v[230:231], s[54:55], 0, v[140:141]
	s_add_i32 m0, s63, 0xc000
	s_nop 0
	global_load_lds_dwordx4 v[230:231], off
	v_lshl_add_u64 v[230:231], s[54:55], 0, v[142:143]
	s_add_i32 m0, s63, 0xe000
	s_nop 0
	global_load_lds_dwordx4 v[230:231], off
	ds_read_b128 v[166:169], v155
	ds_read_b128 v[170:173], v155 offset:1024
	ds_read_b128 v[174:177], v155 offset:2048
	ds_read_b128 v[178:181], v155 offset:3072
	ds_read_b128 v[182:185], v157
	ds_read_b128 v[186:189], v157 offset:1024
	ds_read_b128 v[190:193], v157 offset:2048
	ds_read_b128 v[194:197], v157 offset:3072
	ds_read_b128 v[198:201], v159
	ds_read_b128 v[202:205], v159 offset:1024
	ds_read_b128 v[206:209], v159 offset:2048
	ds_read_b128 v[210:213], v159 offset:3072
	ds_read_b128 v[214:217], v159 offset:4096
	ds_read_b128 v[218:221], v159 offset:5120
	ds_read_b128 v[222:225], v159 offset:6144
	ds_read_b128 v[226:229], v159 offset:7168
	s_waitcnt vmcnt(8)
	s_waitcnt lgkmcnt(0)
	s_barrier
	v_mfma_f32_16x16x32_bf16 v[126:129], v[166:169], v[198:201], v[126:129]
	v_mfma_f32_16x16x32_bf16 v[122:125], v[174:177], v[198:201], v[122:125]
	v_mfma_f32_16x16x32_bf16 v[114:117], v[166:169], v[206:209], v[114:117]
	v_mfma_f32_16x16x32_bf16 v[106:109], v[174:177], v[206:209], v[106:109]
	v_mfma_f32_16x16x32_bf16 v[98:101], v[166:169], v[214:217], v[98:101]
	v_mfma_f32_16x16x32_bf16 v[90:93], v[174:177], v[214:217], v[90:93]
	v_mfma_f32_16x16x32_bf16 v[82:85], v[166:169], v[222:225], v[82:85]
	v_mfma_f32_16x16x32_bf16 v[74:77], v[174:177], v[222:225], v[74:77]
	v_mfma_f32_16x16x32_bf16 v[126:129], v[170:173], v[202:205], v[126:129]
	v_mfma_f32_16x16x32_bf16 v[122:125], v[178:181], v[202:205], v[122:125]
	v_mfma_f32_16x16x32_bf16 v[114:117], v[170:173], v[210:213], v[114:117]
	v_mfma_f32_16x16x32_bf16 v[106:109], v[178:181], v[210:213], v[106:109]
	v_mfma_f32_16x16x32_bf16 v[98:101], v[170:173], v[218:221], v[98:101]
	v_mfma_f32_16x16x32_bf16 v[90:93], v[178:181], v[218:221], v[90:93]
	v_mfma_f32_16x16x32_bf16 v[82:85], v[170:173], v[226:229], v[82:85]
	v_mfma_f32_16x16x32_bf16 v[74:77], v[178:181], v[226:229], v[74:77]
	v_mfma_f32_16x16x32_bf16 v[118:121], v[182:185], v[198:201], v[118:121]
	v_mfma_f32_16x16x32_bf16 v[110:113], v[190:193], v[198:201], v[110:113]
	v_mfma_f32_16x16x32_bf16 v[102:105], v[182:185], v[206:209], v[102:105]
	v_mfma_f32_16x16x32_bf16 v[94:97], v[190:193], v[206:209], v[94:97]
	v_mfma_f32_16x16x32_bf16 v[86:89], v[182:185], v[214:217], v[86:89]
	v_mfma_f32_16x16x32_bf16 v[78:81], v[190:193], v[214:217], v[78:81]
	v_mfma_f32_16x16x32_bf16 v[62:65], v[182:185], v[222:225], v[62:65]
	v_mfma_f32_16x16x32_bf16 v[58:61], v[190:193], v[222:225], v[58:61]
	v_mfma_f32_16x16x32_bf16 v[118:121], v[186:189], v[202:205], v[118:121]
	v_mfma_f32_16x16x32_bf16 v[110:113], v[194:197], v[202:205], v[110:113]
	v_mfma_f32_16x16x32_bf16 v[102:105], v[186:189], v[210:213], v[102:105]
	v_mfma_f32_16x16x32_bf16 v[94:97], v[194:197], v[210:213], v[94:97]
	v_mfma_f32_16x16x32_bf16 v[86:89], v[186:189], v[218:221], v[86:89]
	v_mfma_f32_16x16x32_bf16 v[78:81], v[194:197], v[218:221], v[78:81]
	v_mfma_f32_16x16x32_bf16 v[62:65], v[186:189], v[226:229], v[62:65]
	v_mfma_f32_16x16x32_bf16 v[58:61], v[194:197], v[226:229], v[58:61]
	s_barrier
	s_add_i32 s84, s73, s61
	v_lshl_add_u64 v[230:231], s[56:57], 0, v[132:133]
	s_mov_b32 m0, s84
	s_nop 0
	global_load_lds_dwordx4 v[230:231], off
	s_add_i32 m0, s84, 0x2000
	s_add_u32 s84, s56, 0x80000
	v_lshl_add_u64 v[232:233], s[56:57], 0, v[136:137]
	s_addc_u32 s85, s57, 0
	s_add_i32 s86, s74, s61
	global_load_lds_dwordx4 v[232:233], off
	v_lshl_add_u64 v[234:235], s[84:85], 0, v[132:133]
	s_mov_b32 m0, s86
	v_lshl_add_u64 v[236:237], s[58:59], 0, v[134:135]
	global_load_lds_dwordx4 v[234:235], off
	v_lshl_add_u64 v[234:235], s[84:85], 0, v[136:137]
	s_add_i32 m0, s86, 0x2000
	s_nop 0
	global_load_lds_dwordx4 v[234:235], off
	v_lshl_add_u64 v[234:235], s[58:59], 0, v[130:131]
	s_mov_b32 m0, s63
	s_nop 0
	global_load_lds_dwordx4 v[234:235], off
	s_mov_b32 m0, s64
	s_nop 0
	global_load_lds_dwordx4 v[236:237], off
	ds_read_b128 v[198:201], v159 offset:16384
	ds_read_b128 v[202:205], v159 offset:17408
	ds_read_b128 v[206:209], v159 offset:18432
	ds_read_b128 v[210:213], v159 offset:19456
	ds_read_b128 v[214:217], v159 offset:20480
	ds_read_b128 v[218:221], v159 offset:21504
	ds_read_b128 v[222:225], v159 offset:22528
	ds_read_b128 v[226:229], v159 offset:23552
	s_waitcnt vmcnt(8)
	s_waitcnt lgkmcnt(0)
	s_barrier
; #define PG8_STAGE(bufoff, gbase, voff) do { _Pragma("unroll") for (int _i = 0; _i < 2; ++_i) \
;         __builtin_amdgcn_global_load_lds((const unsigned*)((const char*)(gbase) + (voff)[_i]), (PG8_LAS unsigned*)(lds + (bufoff) + ldsw + _i * 8192), 16, 0, 0); } while (0)
; #define PG8_LDA(dst, b, h) do { _Pragma("unroll") for (int m = 0; m < 4; ++m) _Pragma("unroll") for (int k = 0; k < 2; ++k) dst[m][k] = *(const PG8_LAS bf16x8*)(lds + PG8_SA(b, h) + aoff + m * 2048 + k * 1024); } while (0)
; #define PG8_LDB(dst, b, h) do { _Pragma("unroll") for (int n = 0; n < 2; ++n) _Pragma("unroll") for (int k = 0; k < 2; ++k) dst[n][k] = *(const PG8_LAS bf16x8*)(lds + PG8_SB(b, h) + boff + n * 2048 + k * 1024); } while (0)
; #define PG8_MMA(ai, bj, At, Bt) do { __builtin_amdgcn_s_setprio(1); _Pragma("unroll") for (int m = 0; m < 4; ++m) _Pragma("unroll") for (int n = 0; n < 2; ++n) _Pragma("unroll") for (int k = 0; k < 2; ++k) \
;         acc[ai][bj][m][n] = __builtin_amdgcn_mfma_f32_16x16x32_bf16(Bt[n][k], At[m][k], acc[ai][bj][m][n], 0, 0, 0); __builtin_amdgcn_s_setprio(0); } while (0)
; #define PG8_WAIT_V(n) asm volatile("s_waitcnt vmcnt(" #n ")" ::: "memory")
; #define PG8_WAIT_L(n) asm volatile("s_waitcnt lgkmcnt(" #n ")" ::: "memory")
; #define PG8_BAR __builtin_amdgcn_s_barrier()
; #define PG8_SCHED __builtin_amdgcn_sched_barrier(0)
; template <class Epi, class Sched, bool ALIGN_EPI = false>
; __device__ __forceinline__ void gemm_phase(PG8_LAS unsigned char* lds, const Gemm g, const Sched& S, const Epi& E) {
;     ...
;             PG8_WAIT_V(8); PG8_WAIT_L(0); PG8_BAR; PG8_MMA(1, 0, At, B0); PG8_MMA(1, 1, At, B1); PG8_BAR; PG8_SCHED;
;             PG8_LDB(B0, 1, 0); PG8_LDB(B1, 1, 1); PG8_SCHED; PG8_LDA(At, 1, 0); PG8_STAGE(PG8_SA(0, 1), a2 + hstepA, w1);
;             PG8_WAIT_V(8); PG8_WAIT_L(0); PG8_BAR; PG8_MMA(0, 0, At, B0); PG8_MMA(0, 1, At, B1); PG8_BAR; PG8_SCHED;
	v_mfma_f32_16x16x32_bf16 v[54:57], v[166:169], v[198:201], v[54:57]
	v_mfma_f32_16x16x32_bf16 v[42:45], v[174:177], v[198:201], v[42:45]
	v_mfma_f32_16x16x32_bf16 v[30:33], v[166:169], v[206:209], v[30:33]
	v_mfma_f32_16x16x32_bf16 v[26:29], v[174:177], v[206:209], v[26:29]
	v_mfma_f32_16x16x32_bf16 v[14:17], v[166:169], v[214:217], v[14:17]
	v_mfma_f32_16x16x32_bf16 v[10:13], v[174:177], v[214:217], v[10:13]
	v_mfma_f32_16x16x32_bf16 v[6:9], v[166:169], v[222:225], v[6:9]
	v_mfma_f32_16x16x32_bf16 v[2:5], v[174:177], v[222:225], v[2:5]
	v_mfma_f32_16x16x32_bf16 v[54:57], v[170:173], v[202:205], v[54:57]
	v_mfma_f32_16x16x32_bf16 v[42:45], v[178:181], v[202:205], v[42:45]
	v_mfma_f32_16x16x32_bf16 v[30:33], v[170:173], v[210:213], v[30:33]
	v_mfma_f32_16x16x32_bf16 v[26:29], v[178:181], v[210:213], v[26:29]
	v_mfma_f32_16x16x32_bf16 v[14:17], v[170:173], v[218:221], v[14:17]
	v_mfma_f32_16x16x32_bf16 v[10:13], v[178:181], v[218:221], v[10:13]
	v_mfma_f32_16x16x32_bf16 v[6:9], v[170:173], v[226:229], v[6:9]
	v_mfma_f32_16x16x32_bf16 v[2:5], v[178:181], v[226:229], v[2:5]
	v_mfma_f32_16x16x32_bf16 v[66:69], v[182:185], v[198:201], v[66:69]
	v_mfma_f32_16x16x32_bf16 v[70:73], v[190:193], v[198:201], v[70:73]
	v_mfma_f32_16x16x32_bf16 v[46:49], v[182:185], v[206:209], v[46:49]
	v_mfma_f32_16x16x32_bf16 v[50:53], v[190:193], v[206:209], v[50:53]
	v_mfma_f32_16x16x32_bf16 v[34:37], v[182:185], v[214:217], v[34:37]
	v_mfma_f32_16x16x32_bf16 v[38:41], v[190:193], v[214:217], v[38:41]
	v_mfma_f32_16x16x32_bf16 v[18:21], v[182:185], v[222:225], v[18:21]
	v_mfma_f32_16x16x32_bf16 v[22:25], v[190:193], v[222:225], v[22:25]
	v_mfma_f32_16x16x32_bf16 v[66:69], v[186:189], v[202:205], v[66:69]
	v_mfma_f32_16x16x32_bf16 v[70:73], v[194:197], v[202:205], v[70:73]
	v_mfma_f32_16x16x32_bf16 v[46:49], v[186:189], v[210:213], v[46:49]
	v_mfma_f32_16x16x32_bf16 v[50:53], v[194:197], v[210:213], v[50:53]
	v_mfma_f32_16x16x32_bf16 v[34:37], v[186:189], v[218:221], v[34:37]
	v_mfma_f32_16x16x32_bf16 v[38:41], v[194:197], v[218:221], v[38:41]
	v_mfma_f32_16x16x32_bf16 v[18:21], v[186:189], v[226:229], v[18:21]
	v_mfma_f32_16x16x32_bf16 v[22:25], v[194:197], v[226:229], v[22:25]
	s_barrier
	s_add_i32 s84, 0, 0x18000
	s_add_i32 s85, 0, 0x1c000
	s_add_u32 s58, s58, 0x80000
	s_addc_u32 s59, s59, 0
	s_mov_b32 m0, s65
	v_lshl_add_u64 v[238:239], s[58:59], 0, v[130:131]
	global_load_lds_dwordx4 v[238:239], off
	v_lshl_add_u64 v[238:239], s[58:59], 0, v[134:135]
	s_mov_b32 m0, s66
	s_nop 0
	global_load_lds_dwordx4 v[238:239], off
	v_add_u32_e32 v138, s84, v149
	ds_read_b128 v[166:169], v138
	ds_read_b128 v[170:173], v138 offset:1024
	ds_read_b128 v[174:177], v138 offset:2048
	ds_read_b128 v[178:181], v138 offset:3072
	v_add_u32_e32 v138, s85, v149
	ds_read_b128 v[182:185], v138
	ds_read_b128 v[186:189], v138 offset:1024
	ds_read_b128 v[190:193], v138 offset:2048
	ds_read_b128 v[194:197], v138 offset:3072
	ds_read_b128 v[198:201], v159 offset:32768
	ds_read_b128 v[202:205], v159 offset:33792
	ds_read_b128 v[206:209], v159 offset:34816
	ds_read_b128 v[210:213], v159 offset:35840
	ds_read_b128 v[214:217], v159 offset:36864
	ds_read_b128 v[218:221], v159 offset:37888
	ds_read_b128 v[222:225], v159 offset:38912
	ds_read_b128 v[226:229], v159 offset:39936
	s_waitcnt vmcnt(8)
	s_waitcnt lgkmcnt(0)
	s_barrier
	v_mfma_f32_16x16x32_bf16 v[126:129], v[166:169], v[198:201], v[126:129]
	v_mfma_f32_16x16x32_bf16 v[122:125], v[174:177], v[198:201], v[122:125]
	v_mfma_f32_16x16x32_bf16 v[114:117], v[166:169], v[206:209], v[114:117]
	v_mfma_f32_16x16x32_bf16 v[106:109], v[174:177], v[206:209], v[106:109]
	v_mfma_f32_16x16x32_bf16 v[98:101], v[166:169], v[214:217], v[98:101]
	v_mfma_f32_16x16x32_bf16 v[90:93], v[174:177], v[214:217], v[90:93]
	v_mfma_f32_16x16x32_bf16 v[82:85], v[166:169], v[222:225], v[82:85]
	v_mfma_f32_16x16x32_bf16 v[74:77], v[174:177], v[222:225], v[74:77]
	v_mfma_f32_16x16x32_bf16 v[126:129], v[170:173], v[202:205], v[126:129]
	v_mfma_f32_16x16x32_bf16 v[122:125], v[178:181], v[202:205], v[122:125]
	v_mfma_f32_16x16x32_bf16 v[114:117], v[170:173], v[210:213], v[114:117]
	v_mfma_f32_16x16x32_bf16 v[106:109], v[178:181], v[210:213], v[106:109]
	v_mfma_f32_16x16x32_bf16 v[98:101], v[170:173], v[218:221], v[98:101]
	v_mfma_f32_16x16x32_bf16 v[90:93], v[178:181], v[218:221], v[90:93]
	v_mfma_f32_16x16x32_bf16 v[82:85], v[170:173], v[226:229], v[82:85]
	v_mfma_f32_16x16x32_bf16 v[74:77], v[178:181], v[226:229], v[74:77]
	v_mfma_f32_16x16x32_bf16 v[118:121], v[182:185], v[198:201], v[118:121]
	v_mfma_f32_16x16x32_bf16 v[110:113], v[190:193], v[198:201], v[110:113]
	v_mfma_f32_16x16x32_bf16 v[102:105], v[182:185], v[206:209], v[102:105]
	v_mfma_f32_16x16x32_bf16 v[94:97], v[190:193], v[206:209], v[94:97]
	v_mfma_f32_16x16x32_bf16 v[86:89], v[182:185], v[214:217], v[86:89]
	v_mfma_f32_16x16x32_bf16 v[78:81], v[190:193], v[214:217], v[78:81]
	v_mfma_f32_16x16x32_bf16 v[62:65], v[182:185], v[222:225], v[62:65]
	v_mfma_f32_16x16x32_bf16 v[58:61], v[190:193], v[222:225], v[58:61]
	v_mfma_f32_16x16x32_bf16 v[118:121], v[186:189], v[202:205], v[118:121]
	v_mfma_f32_16x16x32_bf16 v[110:113], v[194:197], v[202:205], v[110:113]
	v_mfma_f32_16x16x32_bf16 v[102:105], v[186:189], v[210:213], v[102:105]
	v_mfma_f32_16x16x32_bf16 v[94:97], v[194:197], v[210:213], v[94:97]
	v_mfma_f32_16x16x32_bf16 v[86:89], v[186:189], v[218:221], v[86:89]
	v_mfma_f32_16x16x32_bf16 v[78:81], v[194:197], v[218:221], v[78:81]
	v_mfma_f32_16x16x32_bf16 v[62:65], v[186:189], v[226:229], v[62:65]
	v_mfma_f32_16x16x32_bf16 v[58:61], v[194:197], v[226:229], v[58:61]
	s_barrier
; #define PG8_STAGE(bufoff, gbase, voff) do { _Pragma("unroll") for (int _i = 0; _i < 2; ++_i) \
;         __builtin_amdgcn_global_load_lds((const unsigned*)((const char*)(gbase) + (voff)[_i]), (PG8_LAS unsigned*)(lds + (bufoff) + ldsw + _i * 8192), 16, 0, 0); } while (0)
; #define PG8_LDA(dst, b, h) do { _Pragma("unroll") for (int m = 0; m < 4; ++m) _Pragma("unroll") for (int k = 0; k < 2; ++k) dst[m][k] = *(const PG8_LAS bf16x8*)(lds + PG8_SA(b, h) + aoff + m * 2048 + k * 1024); } while (0)
; #define PG8_MMA(ai, bj, At, Bt) do { __builtin_amdgcn_s_setprio(1); _Pragma("unroll") for (int m = 0; m < 4; ++m) _Pragma("unroll") for (int n = 0; n < 2; ++n) _Pragma("unroll") for (int k = 0; k < 2; ++k) \
;         acc[ai][bj][m][n] = __builtin_amdgcn_mfma_f32_16x16x32_bf16(Bt[n][k], At[m][k], acc[ai][bj][m][n], 0, 0, 0); __builtin_amdgcn_s_setprio(0); } while (0)
; #define PG8_WAIT_V(n) asm volatile("s_waitcnt vmcnt(" #n ")" ::: "memory")
; #define PG8_WAIT_L(n) asm volatile("s_waitcnt lgkmcnt(" #n ")" ::: "memory")
; #define PG8_BAR __builtin_amdgcn_s_barrier()
; #define PG8_SCHED __builtin_amdgcn_sched_barrier(0)
; template <class Epi, class Sched, bool ALIGN_EPI = false>
; __device__ __forceinline__ void gemm_phase(PG8_LAS unsigned char* lds, const Gemm g, const Sched& S, const Epi& E) {
;     ...
;             PG8_LDA(At, 1, 1); PG8_STAGE(PG8_SB(1, 0), b3, voffB); PG8_STAGE(PG8_SB(1, 1), b3 + hstep, voffB); PG8_STAGE(PG8_SA(1, 0), a3, w0);
;             PG8_WAIT_V(8); PG8_WAIT_L(0); PG8_BAR; PG8_MMA(1, 0, At, B0); PG8_MMA(1, 1, At, B1); PG8_BAR; PG8_SCHED;
;             if constexpr (Epi::KSCALE) { if (((t + 2) & 7) == 0 && t + 2 < nt) { E.kscale(acc, pf, ((t + 2) >> 3) - 1, wr, fr); PG8_SCHED; } }
;         }
;         if constexpr (ALIGN_EPI) { if (wr == 0) PG8_BAR; }
	s_add_i32 s58, s84, s61
	v_lshl_add_u64 v[230:231], v[230:231], 0, s[26:27]
	s_mov_b32 m0, s58
	s_nop 0
	global_load_lds_dwordx4 v[230:231], off
	s_add_i32 m0, s58, 0x2000
	s_add_u32 s56, s56, 0x80080
	v_lshl_add_u64 v[230:231], v[232:233], 0, s[26:27]
	s_addc_u32 s57, s57, 0
	s_add_i32 s58, s85, s61
	global_load_lds_dwordx4 v[230:231], off
	v_lshl_add_u64 v[230:231], s[56:57], 0, v[132:133]
	s_mov_b32 m0, s58
	s_nop 0
	global_load_lds_dwordx4 v[230:231], off
	v_lshl_add_u64 v[230:231], s[56:57], 0, v[136:137]
	s_add_i32 m0, s58, 0x2000
	s_nop 0
	global_load_lds_dwordx4 v[230:231], off
	v_lshl_add_u64 v[230:231], v[234:235], 0, s[26:27]
	s_mov_b32 m0, s69
	s_nop 0
	global_load_lds_dwordx4 v[230:231], off
	v_lshl_add_u64 v[230:231], v[236:237], 0, s[26:27]
	s_mov_b32 m0, s72
	s_nop 0
	global_load_lds_dwordx4 v[230:231], off
	ds_read_b128 v[198:201], v159 offset:49152
	ds_read_b128 v[202:205], v159 offset:50176
	ds_read_b128 v[206:209], v159 offset:51200
	ds_read_b128 v[210:213], v159 offset:52224
	ds_read_b128 v[214:217], v159 offset:53248
	ds_read_b128 v[218:221], v159 offset:54272
	ds_read_b128 v[222:225], v159 offset:55296
	ds_read_b128 v[226:229], v159 offset:56320
	s_waitcnt vmcnt(8)
	s_waitcnt lgkmcnt(0)
	s_barrier
	v_mfma_f32_16x16x32_bf16 v[54:57], v[166:169], v[198:201], v[54:57]
	v_mfma_f32_16x16x32_bf16 v[42:45], v[174:177], v[198:201], v[42:45]
	v_mfma_f32_16x16x32_bf16 v[30:33], v[166:169], v[206:209], v[30:33]
	v_mfma_f32_16x16x32_bf16 v[26:29], v[174:177], v[206:209], v[26:29]
	v_mfma_f32_16x16x32_bf16 v[14:17], v[166:169], v[214:217], v[14:17]
	v_mfma_f32_16x16x32_bf16 v[10:13], v[174:177], v[214:217], v[10:13]
	v_mfma_f32_16x16x32_bf16 v[6:9], v[166:169], v[222:225], v[6:9]
	v_mfma_f32_16x16x32_bf16 v[2:5], v[174:177], v[222:225], v[2:5]
	v_mfma_f32_16x16x32_bf16 v[54:57], v[170:173], v[202:205], v[54:57]
	v_mfma_f32_16x16x32_bf16 v[42:45], v[178:181], v[202:205], v[42:45]
	v_mfma_f32_16x16x32_bf16 v[30:33], v[170:173], v[210:213], v[30:33]
	v_mfma_f32_16x16x32_bf16 v[26:29], v[178:181], v[210:213], v[26:29]
	v_mfma_f32_16x16x32_bf16 v[14:17], v[170:173], v[218:221], v[14:17]
	v_mfma_f32_16x16x32_bf16 v[10:13], v[178:181], v[218:221], v[10:13]
	v_mfma_f32_16x16x32_bf16 v[6:9], v[170:173], v[226:229], v[6:9]
	v_mfma_f32_16x16x32_bf16 v[2:5], v[178:181], v[226:229], v[2:5]
	v_mfma_f32_16x16x32_bf16 v[66:69], v[182:185], v[198:201], v[66:69]
	v_mfma_f32_16x16x32_bf16 v[70:73], v[190:193], v[198:201], v[70:73]
	v_mfma_f32_16x16x32_bf16 v[46:49], v[182:185], v[206:209], v[46:49]
	v_mfma_f32_16x16x32_bf16 v[50:53], v[190:193], v[206:209], v[50:53]
	v_mfma_f32_16x16x32_bf16 v[34:37], v[182:185], v[214:217], v[34:37]
	v_mfma_f32_16x16x32_bf16 v[38:41], v[190:193], v[214:217], v[38:41]
	v_mfma_f32_16x16x32_bf16 v[18:21], v[182:185], v[222:225], v[18:21]
	v_mfma_f32_16x16x32_bf16 v[22:25], v[190:193], v[222:225], v[22:25]
	v_mfma_f32_16x16x32_bf16 v[66:69], v[186:189], v[202:205], v[66:69]
	v_mfma_f32_16x16x32_bf16 v[70:73], v[194:197], v[202:205], v[70:73]
	v_mfma_f32_16x16x32_bf16 v[46:49], v[186:189], v[210:213], v[46:49]
	v_mfma_f32_16x16x32_bf16 v[50:53], v[194:197], v[210:213], v[50:53]
	v_mfma_f32_16x16x32_bf16 v[34:37], v[186:189], v[218:221], v[34:37]
	v_mfma_f32_16x16x32_bf16 v[38:41], v[194:197], v[218:221], v[38:41]
	v_mfma_f32_16x16x32_bf16 v[18:21], v[186:189], v[226:229], v[18:21]
	v_mfma_f32_16x16x32_bf16 v[22:25], v[194:197], v[226:229], v[22:25]
	s_barrier
	s_add_i32 s83, s83, 2
	s_add_u32 s54, s54, 0x100
	s_addc_u32 s55, s55, 0
	s_add_u32 s81, s81, 0x100
	s_addc_u32 s82, s82, 0
	s_cmp_gt_u32 s83, 29
	s_cbranch_scc0 .LBB0_1055
	s_and_b64 vcc, exec, s[40:41]
	s_cbranch_vccz .LBB0_1058
	s_barrier

; #define PG8_STAGE(bufoff, gbase, voff) do { _Pragma("unroll") for (int _i = 0; _i < 2; ++_i) \
;         __builtin_amdgcn_global_load_lds((const unsigned*)((const char*)(gbase) + (voff)[_i]), (PG8_LAS unsigned*)(lds + (bufoff) + ldsw + _i * 8192), 16, 0, 0); } while (0)
; #define PG8_LDA(dst, b, h) do { _Pragma("unroll") for (int m = 0; m < 4; ++m) _Pragma("unroll") for (int k = 0; k < 2; ++k) dst[m][k] = *(const PG8_LAS bf16x8*)(lds + PG8_SA(b, h) + aoff + m * 2048 + k * 1024); } while (0)
; #define PG8_LDB(dst, b, h) do { _Pragma("unroll") for (int n = 0; n < 2; ++n) _Pragma("unroll") for (int k = 0; k < 2; ++k) dst[n][k] = *(const PG8_LAS bf16x8*)(lds + PG8_SB(b, h) + boff + n * 2048 + k * 1024); } while (0)
; #define PG8_MMA(ai, bj, At, Bt) do { __builtin_amdgcn_s_setprio(1); _Pragma("unroll") for (int m = 0; m < 4; ++m) _Pragma("unroll") for (int n = 0; n < 2; ++n) _Pragma("unroll") for (int k = 0; k < 2; ++k) \
;         acc[ai][bj][m][n] = __builtin_amdgcn_mfma_f32_16x16x32_bf16(Bt[n][k], At[m][k], acc[ai][bj][m][n], 0, 0, 0); __builtin_amdgcn_s_setprio(0); } while (0)
; #define PG8_WAIT_V(n) asm volatile("s_waitcnt vmcnt(" #n ")" ::: "memory")
; #define PG8_WAIT_L(n) asm volatile("s_waitcnt lgkmcnt(" #n ")" ::: "memory")
; template <class Epi, class Sched, bool ALIGN_EPI = false>
; __device__ __forceinline__ void gemm_phase(PG8_LAS unsigned char* lds, const Gemm g, const Sched& S, const Epi& E) {
;     ...
;             const bool last = (t == nt - 2);
;             const char* a1 = cA + (size_t)(t + 1) * kstep;
;             const char* a2 = last ? nA : cA + (size_t)(t + 2) * kstep; const char* b2 = last ? nB : cB + (size_t)(t + 2) * kstep;
;             const char* a3 = a2 + kstep; const char* b3 = b2 + kstep;
;             unsigned w0[2], w1[2];
; #pragma unroll
;             for (int i = 0; i < 2; ++i) { w0[i] = (Sched::GATHER && last) ? vn0[i] : vc0[i]; w1[i] = (Sched::GATHER && last) ? vn1[i] : vc1[i]; }
;             if (last && has_next) S.a_ready(nxt);
;             PG8_LDB(B0, 0, 0); PG8_LDB(B1, 0, 1); PG8_SCHED; PG8_LDA(At, 0, 0); PG8_STAGE(PG8_SA(1, 1), a1 + hstepA, vc1);
;             PG8_WAIT_V(8); PG8_WAIT_L(0); PG8_BAR; PG8_MMA(0, 0, At, B0); PG8_MMA(0, 1, At, B1); PG8_BAR; PG8_SCHED;
;             PG8_LDA(At, 0, 1); PG8_STAGE(PG8_SB(0, 0), b2, voffB); PG8_STAGE(PG8_SB(0, 1), b2 + hstep, voffB); PG8_STAGE(PG8_SA(0, 0), a2, w0);
.LBB0_1198:
	s_add_u32 s54, s52, 0xfff80080
	s_addc_u32 s55, s53, -1
	s_cmp_eq_u32 s78, 28
	s_cselect_b32 s57, s45, s55
	s_cselect_b32 s56, s74, s54
	s_cselect_b32 s55, s43, s77
	s_cselect_b32 s54, s75, s76
	v_lshl_add_u64 v[216:217], s[52:53], 0, v[146:147]
	s_add_i32 m0, s51, 0xc000
	s_nop 0
	global_load_lds_dwordx4 v[216:217], off
	v_lshl_add_u64 v[216:217], s[52:53], 0, v[148:149]
	s_add_i32 m0, s51, 0xe000
	s_nop 0
	global_load_lds_dwordx4 v[216:217], off
	ds_read_b128 v[130:133], v168
	ds_read_b128 v[134:137], v168 offset:1024
	ds_read_b128 v[154:157], v168 offset:2048
	ds_read_b128 v[158:161], v168 offset:3072
	ds_read_b128 v[162:165], v169
	ds_read_b128 v[172:175], v169 offset:1024
	ds_read_b128 v[176:179], v169 offset:2048
	ds_read_b128 v[180:183], v169 offset:3072
	ds_read_b128 v[184:187], v170
	ds_read_b128 v[188:191], v170 offset:1024
	ds_read_b128 v[192:195], v170 offset:2048
	ds_read_b128 v[196:199], v170 offset:3072
	ds_read_b128 v[200:203], v170 offset:4096
	ds_read_b128 v[204:207], v170 offset:5120
	ds_read_b128 v[208:211], v170 offset:6144
	ds_read_b128 v[212:215], v170 offset:7168
	s_waitcnt vmcnt(8)
	s_waitcnt lgkmcnt(0)
	s_barrier
	v_mfma_f32_16x16x32_bf16 v[126:129], v[130:133], v[184:187], v[126:129]
	v_mfma_f32_16x16x32_bf16 v[122:125], v[154:157], v[184:187], v[122:125]
	v_mfma_f32_16x16x32_bf16 v[118:121], v[130:133], v[192:195], v[118:121]
	v_mfma_f32_16x16x32_bf16 v[114:117], v[154:157], v[192:195], v[114:117]
	v_mfma_f32_16x16x32_bf16 v[94:97], v[130:133], v[200:203], v[94:97]
	v_mfma_f32_16x16x32_bf16 v[90:93], v[154:157], v[200:203], v[90:93]
	v_mfma_f32_16x16x32_bf16 v[78:81], v[130:133], v[208:211], v[78:81]
	v_mfma_f32_16x16x32_bf16 v[74:77], v[154:157], v[208:211], v[74:77]
	v_mfma_f32_16x16x32_bf16 v[126:129], v[134:137], v[188:191], v[126:129]
	v_mfma_f32_16x16x32_bf16 v[122:125], v[158:161], v[188:191], v[122:125]
	v_mfma_f32_16x16x32_bf16 v[118:121], v[134:137], v[196:199], v[118:121]
	v_mfma_f32_16x16x32_bf16 v[114:117], v[158:161], v[196:199], v[114:117]
	v_mfma_f32_16x16x32_bf16 v[94:97], v[134:137], v[204:207], v[94:97]
	v_mfma_f32_16x16x32_bf16 v[90:93], v[158:161], v[204:207], v[90:93]
	v_mfma_f32_16x16x32_bf16 v[78:81], v[134:137], v[212:215], v[78:81]
	v_mfma_f32_16x16x32_bf16 v[74:77], v[158:161], v[212:215], v[74:77]
	v_mfma_f32_16x16x32_bf16 v[110:113], v[162:165], v[184:187], v[110:113]
	v_mfma_f32_16x16x32_bf16 v[106:109], v[176:179], v[184:187], v[106:109]
	v_mfma_f32_16x16x32_bf16 v[102:105], v[162:165], v[192:195], v[102:105]
	v_mfma_f32_16x16x32_bf16 v[98:101], v[176:179], v[192:195], v[98:101]
	v_mfma_f32_16x16x32_bf16 v[86:89], v[162:165], v[200:203], v[86:89]
	v_mfma_f32_16x16x32_bf16 v[82:85], v[176:179], v[200:203], v[82:85]
	v_mfma_f32_16x16x32_bf16 v[70:73], v[162:165], v[208:211], v[70:73]
	v_mfma_f32_16x16x32_bf16 v[66:69], v[176:179], v[208:211], v[66:69]
	v_mfma_f32_16x16x32_bf16 v[110:113], v[172:175], v[188:191], v[110:113]
	v_mfma_f32_16x16x32_bf16 v[106:109], v[180:183], v[188:191], v[106:109]
	v_mfma_f32_16x16x32_bf16 v[102:105], v[172:175], v[196:199], v[102:105]
	v_mfma_f32_16x16x32_bf16 v[98:101], v[180:183], v[196:199], v[98:101]
	v_mfma_f32_16x16x32_bf16 v[86:89], v[172:175], v[204:207], v[86:89]
	v_mfma_f32_16x16x32_bf16 v[82:85], v[180:183], v[204:207], v[82:85]
	v_mfma_f32_16x16x32_bf16 v[70:73], v[172:175], v[212:215], v[70:73]
	v_mfma_f32_16x16x32_bf16 v[66:69], v[180:183], v[212:215], v[66:69]
	s_barrier
	s_add_i32 s79, s69, s61
	v_lshl_add_u64 v[216:217], s[54:55], 0, v[140:141]
	s_mov_b32 m0, s79
	s_nop 0
	global_load_lds_dwordx4 v[216:217], off
	s_add_i32 m0, s79, 0x2000
	s_add_u32 s80, s54, 0x80000
	v_lshl_add_u64 v[218:219], s[54:55], 0, v[144:145]
	s_addc_u32 s81, s55, 0
	s_add_i32 s79, s72, s61
	global_load_lds_dwordx4 v[218:219], off
	v_lshl_add_u64 v[220:221], s[80:81], 0, v[140:141]
	s_mov_b32 m0, s79
	v_lshl_add_u64 v[222:223], s[56:57], 0, v[142:143]
	global_load_lds_dwordx4 v[220:221], off
	v_lshl_add_u64 v[220:221], s[80:81], 0, v[144:145]
	s_add_i32 m0, s79, 0x2000
	s_nop 0
	global_load_lds_dwordx4 v[220:221], off
	v_lshl_add_u64 v[220:221], s[56:57], 0, v[138:139]
	s_mov_b32 m0, s51
	s_nop 0
	global_load_lds_dwordx4 v[220:221], off
	s_mov_b32 m0, s62
	s_nop 0
	global_load_lds_dwordx4 v[222:223], off
	ds_read_b128 v[184:187], v170 offset:16384
	ds_read_b128 v[188:191], v170 offset:17408
	ds_read_b128 v[192:195], v170 offset:18432
	ds_read_b128 v[196:199], v170 offset:19456
	ds_read_b128 v[200:203], v170 offset:20480
	ds_read_b128 v[204:207], v170 offset:21504
	ds_read_b128 v[208:211], v170 offset:22528
	ds_read_b128 v[212:215], v170 offset:23552
	s_waitcnt vmcnt(8)
	s_waitcnt lgkmcnt(0)
	s_barrier
; #define PG8_STAGE(bufoff, gbase, voff) do { _Pragma("unroll") for (int _i = 0; _i < 2; ++_i) \
;         __builtin_amdgcn_global_load_lds((const unsigned*)((const char*)(gbase) + (voff)[_i]), (PG8_LAS unsigned*)(lds + (bufoff) + ldsw + _i * 8192), 16, 0, 0); } while (0)
; #define PG8_LDA(dst, b, h) do { _Pragma("unroll") for (int m = 0; m < 4; ++m) _Pragma("unroll") for (int k = 0; k < 2; ++k) dst[m][k] = *(const PG8_LAS bf16x8*)(lds + PG8_SA(b, h) + aoff + m * 2048 + k * 1024); } while (0)
; #define PG8_LDB(dst, b, h) do { _Pragma("unroll") for (int n = 0; n < 2; ++n) _Pragma("unroll") for (int k = 0; k < 2; ++k) dst[n][k] = *(const PG8_LAS bf16x8*)(lds + PG8_SB(b, h) + boff + n * 2048 + k * 1024); } while (0)
; #define PG8_MMA(ai, bj, At, Bt) do { __builtin_amdgcn_s_setprio(1); _Pragma("unroll") for (int m = 0; m < 4; ++m) _Pragma("unroll") for (int n = 0; n < 2; ++n) _Pragma("unroll") for (int k = 0; k < 2; ++k) \
;         acc[ai][bj][m][n] = __builtin_amdgcn_mfma_f32_16x16x32_bf16(Bt[n][k], At[m][k], acc[ai][bj][m][n], 0, 0, 0); __builtin_amdgcn_s_setprio(0); } while (0)
; #define PG8_WAIT_V(n) asm volatile("s_waitcnt vmcnt(" #n ")" ::: "memory")
; #define PG8_WAIT_L(n) asm volatile("s_waitcnt lgkmcnt(" #n ")" ::: "memory")
; #define PG8_BAR __builtin_amdgcn_s_barrier()
; #define PG8_SCHED __builtin_amdgcn_sched_barrier(0)
; template <class Epi, class Sched, bool ALIGN_EPI = false>
; __device__ __forceinline__ void gemm_phase(PG8_LAS unsigned char* lds, const Gemm g, const Sched& S, const Epi& E) {
;     ...
;             PG8_WAIT_V(8); PG8_WAIT_L(0); PG8_BAR; PG8_MMA(1, 0, At, B0); PG8_MMA(1, 1, At, B1); PG8_BAR; PG8_SCHED;
;             PG8_LDB(B0, 1, 0); PG8_LDB(B1, 1, 1); PG8_SCHED; PG8_LDA(At, 1, 0); PG8_STAGE(PG8_SA(0, 1), a2 + hstepA, w1);
;             PG8_WAIT_V(8); PG8_WAIT_L(0); PG8_BAR; PG8_MMA(0, 0, At, B0); PG8_MMA(0, 1, At, B1); PG8_BAR; PG8_SCHED;
	v_mfma_f32_16x16x32_bf16 v[54:57], v[130:133], v[184:187], v[54:57]
	v_mfma_f32_16x16x32_bf16 v[50:53], v[154:157], v[184:187], v[50:53]
	v_mfma_f32_16x16x32_bf16 v[38:41], v[130:133], v[192:195], v[38:41]
	v_mfma_f32_16x16x32_bf16 v[34:37], v[154:157], v[192:195], v[34:37]
	v_mfma_f32_16x16x32_bf16 v[22:25], v[130:133], v[200:203], v[22:25]
	v_mfma_f32_16x16x32_bf16 v[18:21], v[154:157], v[200:203], v[18:21]
	v_mfma_f32_16x16x32_bf16 v[6:9], v[130:133], v[208:211], v[6:9]
	v_mfma_f32_16x16x32_bf16 v[2:5], v[154:157], v[208:211], v[2:5]
	v_mfma_f32_16x16x32_bf16 v[54:57], v[134:137], v[188:191], v[54:57]
	v_mfma_f32_16x16x32_bf16 v[50:53], v[158:161], v[188:191], v[50:53]
	v_mfma_f32_16x16x32_bf16 v[38:41], v[134:137], v[196:199], v[38:41]
	v_mfma_f32_16x16x32_bf16 v[34:37], v[158:161], v[196:199], v[34:37]
	v_mfma_f32_16x16x32_bf16 v[22:25], v[134:137], v[204:207], v[22:25]
	v_mfma_f32_16x16x32_bf16 v[18:21], v[158:161], v[204:207], v[18:21]
	v_mfma_f32_16x16x32_bf16 v[6:9], v[134:137], v[212:215], v[6:9]
	v_mfma_f32_16x16x32_bf16 v[2:5], v[158:161], v[212:215], v[2:5]
	v_mfma_f32_16x16x32_bf16 v[62:65], v[162:165], v[184:187], v[62:65]
	v_mfma_f32_16x16x32_bf16 v[58:61], v[176:179], v[184:187], v[58:61]
	v_mfma_f32_16x16x32_bf16 v[46:49], v[162:165], v[192:195], v[46:49]
	v_mfma_f32_16x16x32_bf16 v[42:45], v[176:179], v[192:195], v[42:45]
	v_mfma_f32_16x16x32_bf16 v[30:33], v[162:165], v[200:203], v[30:33]
	v_mfma_f32_16x16x32_bf16 v[26:29], v[176:179], v[200:203], v[26:29]
	v_mfma_f32_16x16x32_bf16 v[14:17], v[162:165], v[208:211], v[14:17]
	v_mfma_f32_16x16x32_bf16 v[10:13], v[176:179], v[208:211], v[10:13]
	v_mfma_f32_16x16x32_bf16 v[62:65], v[172:175], v[188:191], v[62:65]
	v_mfma_f32_16x16x32_bf16 v[58:61], v[180:183], v[188:191], v[58:61]
	v_mfma_f32_16x16x32_bf16 v[46:49], v[172:175], v[196:199], v[46:49]
	v_mfma_f32_16x16x32_bf16 v[42:45], v[180:183], v[196:199], v[42:45]
	v_mfma_f32_16x16x32_bf16 v[30:33], v[172:175], v[204:207], v[30:33]
	v_mfma_f32_16x16x32_bf16 v[26:29], v[180:183], v[204:207], v[26:29]
	v_mfma_f32_16x16x32_bf16 v[14:17], v[172:175], v[212:215], v[14:17]
	v_mfma_f32_16x16x32_bf16 v[10:13], v[180:183], v[212:215], v[10:13]
	s_barrier
	s_add_i32 s79, 0, 0x18000
	s_add_i32 s80, 0, 0x1c000
	s_add_u32 s56, s56, 0x80000
	s_addc_u32 s57, s57, 0
	s_mov_b32 m0, s63
	v_lshl_add_u64 v[224:225], s[56:57], 0, v[138:139]
	global_load_lds_dwordx4 v[224:225], off
	v_lshl_add_u64 v[224:225], s[56:57], 0, v[142:143]
	s_mov_b32 m0, s64
	s_nop 0
	global_load_lds_dwordx4 v[224:225], off
	v_add_u32_e32 v158, s79, v166
	v_add_u32_e32 v171, s80, v166
	ds_read_b128 v[130:133], v158
	ds_read_b128 v[134:137], v158 offset:1024
	ds_read_b128 v[154:157], v158 offset:2048
	ds_read_b128 v[158:161], v158 offset:3072
	ds_read_b128 v[162:165], v171
	ds_read_b128 v[172:175], v171 offset:1024
	ds_read_b128 v[176:179], v171 offset:2048
	ds_read_b128 v[180:183], v171 offset:3072
	ds_read_b128 v[184:187], v170 offset:32768
	ds_read_b128 v[188:191], v170 offset:33792
	ds_read_b128 v[192:195], v170 offset:34816
	ds_read_b128 v[196:199], v170 offset:35840
	ds_read_b128 v[200:203], v170 offset:36864
	ds_read_b128 v[204:207], v170 offset:37888
	ds_read_b128 v[208:211], v170 offset:38912
	ds_read_b128 v[212:215], v170 offset:39936
	s_waitcnt vmcnt(8)
	s_waitcnt lgkmcnt(0)
	s_barrier
	v_mfma_f32_16x16x32_bf16 v[126:129], v[130:133], v[184:187], v[126:129]
	v_mfma_f32_16x16x32_bf16 v[122:125], v[154:157], v[184:187], v[122:125]
	v_mfma_f32_16x16x32_bf16 v[118:121], v[130:133], v[192:195], v[118:121]
	v_mfma_f32_16x16x32_bf16 v[114:117], v[154:157], v[192:195], v[114:117]
	v_mfma_f32_16x16x32_bf16 v[94:97], v[130:133], v[200:203], v[94:97]
	v_mfma_f32_16x16x32_bf16 v[90:93], v[154:157], v[200:203], v[90:93]
	v_mfma_f32_16x16x32_bf16 v[78:81], v[130:133], v[208:211], v[78:81]
	v_mfma_f32_16x16x32_bf16 v[74:77], v[154:157], v[208:211], v[74:77]
	v_mfma_f32_16x16x32_bf16 v[126:129], v[134:137], v[188:191], v[126:129]
	v_mfma_f32_16x16x32_bf16 v[122:125], v[158:161], v[188:191], v[122:125]
	v_mfma_f32_16x16x32_bf16 v[118:121], v[134:137], v[196:199], v[118:121]
	v_mfma_f32_16x16x32_bf16 v[114:117], v[158:161], v[196:199], v[114:117]
	v_mfma_f32_16x16x32_bf16 v[94:97], v[134:137], v[204:207], v[94:97]
	v_mfma_f32_16x16x32_bf16 v[90:93], v[158:161], v[204:207], v[90:93]
	v_mfma_f32_16x16x32_bf16 v[78:81], v[134:137], v[212:215], v[78:81]
	v_mfma_f32_16x16x32_bf16 v[74:77], v[158:161], v[212:215], v[74:77]
	v_mfma_f32_16x16x32_bf16 v[110:113], v[162:165], v[184:187], v[110:113]
	v_mfma_f32_16x16x32_bf16 v[106:109], v[176:179], v[184:187], v[106:109]
	v_mfma_f32_16x16x32_bf16 v[102:105], v[162:165], v[192:195], v[102:105]
	v_mfma_f32_16x16x32_bf16 v[98:101], v[176:179], v[192:195], v[98:101]
	v_mfma_f32_16x16x32_bf16 v[86:89], v[162:165], v[200:203], v[86:89]
	v_mfma_f32_16x16x32_bf16 v[82:85], v[176:179], v[200:203], v[82:85]
	v_mfma_f32_16x16x32_bf16 v[70:73], v[162:165], v[208:211], v[70:73]
	v_mfma_f32_16x16x32_bf16 v[66:69], v[176:179], v[208:211], v[66:69]
	v_mfma_f32_16x16x32_bf16 v[110:113], v[172:175], v[188:191], v[110:113]
	v_mfma_f32_16x16x32_bf16 v[106:109], v[180:183], v[188:191], v[106:109]
	v_mfma_f32_16x16x32_bf16 v[102:105], v[172:175], v[196:199], v[102:105]
	v_mfma_f32_16x16x32_bf16 v[98:101], v[180:183], v[196:199], v[98:101]
	v_mfma_f32_16x16x32_bf16 v[86:89], v[172:175], v[204:207], v[86:89]
	v_mfma_f32_16x16x32_bf16 v[82:85], v[180:183], v[204:207], v[82:85]
	v_mfma_f32_16x16x32_bf16 v[70:73], v[172:175], v[212:215], v[70:73]
	v_mfma_f32_16x16x32_bf16 v[66:69], v[180:183], v[212:215], v[66:69]
	s_barrier
; #define PG8_STAGE(bufoff, gbase, voff) do { _Pragma("unroll") for (int _i = 0; _i < 2; ++_i) \
;         __builtin_amdgcn_global_load_lds((const unsigned*)((const char*)(gbase) + (voff)[_i]), (PG8_LAS unsigned*)(lds + (bufoff) + ldsw + _i * 8192), 16, 0, 0); } while (0)
; #define PG8_LDA(dst, b, h) do { _Pragma("unroll") for (int m = 0; m < 4; ++m) _Pragma("unroll") for (int k = 0; k < 2; ++k) dst[m][k] = *(const PG8_LAS bf16x8*)(lds + PG8_SA(b, h) + aoff + m * 2048 + k * 1024); } while (0)
; #define PG8_MMA(ai, bj, At, Bt) do { __builtin_amdgcn_s_setprio(1); _Pragma("unroll") for (int m = 0; m < 4; ++m) _Pragma("unroll") for (int n = 0; n < 2; ++n) _Pragma("unroll") for (int k = 0; k < 2; ++k) \
;         acc[ai][bj][m][n] = __builtin_amdgcn_mfma_f32_16x16x32_bf16(Bt[n][k], At[m][k], acc[ai][bj][m][n], 0, 0, 0); __builtin_amdgcn_s_setprio(0); } while (0)
; #define PG8_WAIT_V(n) asm volatile("s_waitcnt vmcnt(" #n ")" ::: "memory")
; #define PG8_WAIT_L(n) asm volatile("s_waitcnt lgkmcnt(" #n ")" ::: "memory")
; #define PG8_BAR __builtin_amdgcn_s_barrier()
; #define PG8_SCHED __builtin_amdgcn_sched_barrier(0)
; template <class Epi, class Sched, bool ALIGN_EPI = false>
; __device__ __forceinline__ void gemm_phase(PG8_LAS unsigned char* lds, const Gemm g, const Sched& S, const Epi& E) {
;     ...
;             PG8_LDA(At, 1, 1); PG8_STAGE(PG8_SB(1, 0), b3, voffB); PG8_STAGE(PG8_SB(1, 1), b3 + hstep, voffB); PG8_STAGE(PG8_SA(1, 0), a3, w0);
;             PG8_WAIT_V(8); PG8_WAIT_L(0); PG8_BAR; PG8_MMA(1, 0, At, B0); PG8_MMA(1, 1, At, B1); PG8_BAR; PG8_SCHED;
;             if constexpr (Epi::KSCALE) { if (((t + 2) & 7) == 0 && t + 2 < nt) { E.kscale(acc, pf, ((t + 2) >> 3) - 1, wr, fr); PG8_SCHED; } }
;         }
;         if constexpr (ALIGN_EPI) { if (wr == 0) PG8_BAR; }
	s_add_i32 s56, s79, s61
	v_lshl_add_u64 v[216:217], v[216:217], 0, s[18:19]
	s_mov_b32 m0, s56
	s_nop 0
	global_load_lds_dwordx4 v[216:217], off
	s_add_i32 m0, s56, 0x2000
	s_add_u32 s54, s54, 0x80080
	v_lshl_add_u64 v[216:217], v[218:219], 0, s[18:19]
	s_addc_u32 s55, s55, 0
	s_add_i32 s56, s80, s61
	global_load_lds_dwordx4 v[216:217], off
	v_lshl_add_u64 v[216:217], s[54:55], 0, v[140:141]
	s_mov_b32 m0, s56
	s_nop 0
	global_load_lds_dwordx4 v[216:217], off
	v_lshl_add_u64 v[216:217], s[54:55], 0, v[144:145]
	s_add_i32 m0, s56, 0x2000
	s_nop 0
	global_load_lds_dwordx4 v[216:217], off
	v_lshl_add_u64 v[216:217], v[220:221], 0, s[18:19]
	s_mov_b32 m0, s67
	s_nop 0
	global_load_lds_dwordx4 v[216:217], off
	v_lshl_add_u64 v[216:217], v[222:223], 0, s[18:19]
	s_mov_b32 m0, s68
	s_nop 0
	global_load_lds_dwordx4 v[216:217], off
	ds_read_b128 v[184:187], v170 offset:49152
	ds_read_b128 v[188:191], v170 offset:50176
	ds_read_b128 v[192:195], v170 offset:51200
	ds_read_b128 v[196:199], v170 offset:52224
	ds_read_b128 v[200:203], v170 offset:53248
	ds_read_b128 v[204:207], v170 offset:54272
	ds_read_b128 v[208:211], v170 offset:55296
	ds_read_b128 v[212:215], v170 offset:56320
	s_waitcnt vmcnt(8)
	s_waitcnt lgkmcnt(0)
	s_barrier
	v_mfma_f32_16x16x32_bf16 v[54:57], v[130:133], v[184:187], v[54:57]
	v_mfma_f32_16x16x32_bf16 v[50:53], v[154:157], v[184:187], v[50:53]
	v_mfma_f32_16x16x32_bf16 v[38:41], v[130:133], v[192:195], v[38:41]
	v_mfma_f32_16x16x32_bf16 v[34:37], v[154:157], v[192:195], v[34:37]
	v_mfma_f32_16x16x32_bf16 v[22:25], v[130:133], v[200:203], v[22:25]
	v_mfma_f32_16x16x32_bf16 v[18:21], v[154:157], v[200:203], v[18:21]
	v_mfma_f32_16x16x32_bf16 v[6:9], v[130:133], v[208:211], v[6:9]
	v_mfma_f32_16x16x32_bf16 v[2:5], v[154:157], v[208:211], v[2:5]
	v_mfma_f32_16x16x32_bf16 v[54:57], v[134:137], v[188:191], v[54:57]
	v_mfma_f32_16x16x32_bf16 v[50:53], v[158:161], v[188:191], v[50:53]
	v_mfma_f32_16x16x32_bf16 v[38:41], v[134:137], v[196:199], v[38:41]
	v_mfma_f32_16x16x32_bf16 v[34:37], v[158:161], v[196:199], v[34:37]
	v_mfma_f32_16x16x32_bf16 v[22:25], v[134:137], v[204:207], v[22:25]
	v_mfma_f32_16x16x32_bf16 v[18:21], v[158:161], v[204:207], v[18:21]
	v_mfma_f32_16x16x32_bf16 v[6:9], v[134:137], v[212:215], v[6:9]
	v_mfma_f32_16x16x32_bf16 v[2:5], v[158:161], v[212:215], v[2:5]
	v_mfma_f32_16x16x32_bf16 v[62:65], v[162:165], v[184:187], v[62:65]
	v_mfma_f32_16x16x32_bf16 v[58:61], v[176:179], v[184:187], v[58:61]
	v_mfma_f32_16x16x32_bf16 v[46:49], v[162:165], v[192:195], v[46:49]
	v_mfma_f32_16x16x32_bf16 v[42:45], v[176:179], v[192:195], v[42:45]
	v_mfma_f32_16x16x32_bf16 v[30:33], v[162:165], v[200:203], v[30:33]
	v_mfma_f32_16x16x32_bf16 v[26:29], v[176:179], v[200:203], v[26:29]
	v_mfma_f32_16x16x32_bf16 v[14:17], v[162:165], v[208:211], v[14:17]
	v_mfma_f32_16x16x32_bf16 v[10:13], v[176:179], v[208:211], v[10:13]
	v_mfma_f32_16x16x32_bf16 v[62:65], v[172:175], v[188:191], v[62:65]
	v_mfma_f32_16x16x32_bf16 v[58:61], v[180:183], v[188:191], v[58:61]
	v_mfma_f32_16x16x32_bf16 v[46:49], v[172:175], v[196:199], v[46:49]
	v_mfma_f32_16x16x32_bf16 v[42:45], v[180:183], v[196:199], v[42:45]
	v_mfma_f32_16x16x32_bf16 v[30:33], v[172:175], v[204:207], v[30:33]
	v_mfma_f32_16x16x32_bf16 v[26:29], v[180:183], v[204:207], v[26:29]
	v_mfma_f32_16x16x32_bf16 v[14:17], v[172:175], v[212:215], v[14:17]
	v_mfma_f32_16x16x32_bf16 v[10:13], v[180:183], v[212:215], v[10:13]
	s_barrier
	s_add_i32 s78, s78, 2
	s_add_u32 s52, s52, 0x100
	s_addc_u32 s53, s53, 0
	s_add_u32 s76, s76, 0x100
	s_addc_u32 s77, s77, 0
	s_cmp_gt_u32 s78, 29
	s_cbranch_scc0 .LBB0_1198
	s_and_b64 vcc, exec, s[22:23]
	s_cbranch_vccz .LBB0_1201
	s_barrier

; #define PG8_STAGE(bufoff, gbase, voff) do { _Pragma("unroll") for (int _i = 0; _i < 2; ++_i) \
;         __builtin_amdgcn_global_load_lds((const unsigned*)((const char*)(gbase) + (voff)[_i]), (PG8_LAS unsigned*)(lds + (bufoff) + ldsw + _i * 8192), 16, 0, 0); } while (0)
; #define PG8_LDA(dst, b, h) do { _Pragma("unroll") for (int m = 0; m < 4; ++m) _Pragma("unroll") for (int k = 0; k < 2; ++k) dst[m][k] = *(const PG8_LAS bf16x8*)(lds + PG8_SA(b, h) + aoff + m * 2048 + k * 1024); } while (0)
; #define PG8_LDB(dst, b, h) do { _Pragma("unroll") for (int n = 0; n < 2; ++n) _Pragma("unroll") for (int k = 0; k < 2; ++k) dst[n][k] = *(const PG8_LAS bf16x8*)(lds + PG8_SB(b, h) + boff + n * 2048 + k * 1024); } while (0)
; #define PG8_MMA(ai, bj, At, Bt) do { __builtin_amdgcn_s_setprio(1); _Pragma("unroll") for (int m = 0; m < 4; ++m) _Pragma("unroll") for (int n = 0; n < 2; ++n) _Pragma("unroll") for (int k = 0; k < 2; ++k) \
;         acc[ai][bj][m][n] = __builtin_amdgcn_mfma_f32_16x16x32_bf16(Bt[n][k], At[m][k], acc[ai][bj][m][n], 0, 0, 0); __builtin_amdgcn_s_setprio(0); } while (0)
; #define PG8_WAIT_V(n) asm volatile("s_waitcnt vmcnt(" #n ")" ::: "memory")
; #define PG8_WAIT_L(n) asm volatile("s_waitcnt lgkmcnt(" #n ")" ::: "memory")
; template <class Epi, class Sched, bool ALIGN_EPI = false>
; __device__ __forceinline__ void gemm_phase(PG8_LAS unsigned char* lds, const Gemm g, const Sched& S, const Epi& E) {
;     ...
;             const bool last = (t == nt - 2);
;             const char* a1 = cA + (size_t)(t + 1) * kstep;
;             const char* a2 = last ? nA : cA + (size_t)(t + 2) * kstep; const char* b2 = last ? nB : cB + (size_t)(t + 2) * kstep;
;             const char* a3 = a2 + kstep; const char* b3 = b2 + kstep;
;             unsigned w0[2], w1[2];
; #pragma unroll
;             for (int i = 0; i < 2; ++i) { w0[i] = (Sched::GATHER && last) ? vn0[i] : vc0[i]; w1[i] = (Sched::GATHER && last) ? vn1[i] : vc1[i]; }
;             if (last && has_next) S.a_ready(nxt);
;             PG8_LDB(B0, 0, 0); PG8_LDB(B1, 0, 1); PG8_SCHED; PG8_LDA(At, 0, 0); PG8_STAGE(PG8_SA(1, 1), a1 + hstepA, vc1);
;             PG8_WAIT_V(8); PG8_WAIT_L(0); PG8_BAR; PG8_MMA(0, 0, At, B0); PG8_MMA(0, 1, At, B1); PG8_BAR; PG8_SCHED;
;             PG8_LDA(At, 0, 1); PG8_STAGE(PG8_SB(0, 0), b2, voffB); PG8_STAGE(PG8_SB(0, 1), b2 + hstep, voffB); PG8_STAGE(PG8_SA(0, 0), a2, w0);
.LBB0_1414:
	s_add_u32 s56, s36, s54
	v_add_u32_e32 v155, s79, v143
	s_addc_u32 s57, s37, s55
	ds_read_b128 v[164:167], v155
	ds_read_b128 v[168:171], v155 offset:1024
	ds_read_b128 v[172:175], v155 offset:2048
	ds_read_b128 v[176:179], v155 offset:3072
	v_add_u32_e32 v155, s80, v143
	s_add_u32 s58, s56, 0x3c800100
	ds_read_b128 v[180:183], v155
	ds_read_b128 v[184:187], v155 offset:1024
	ds_read_b128 v[188:191], v155 offset:2048
	ds_read_b128 v[192:195], v155 offset:3072
	s_addc_u32 s59, s57, 0
	s_add_u32 s88, s47, s54
	s_addc_u32 s89, s86, s55
	s_cmpk_eq_i32 s54, 0xf00
	s_cselect_b64 vcc, -1, 0
	s_and_b64 s[56:57], vcc, exec
	v_cndmask_b32_e32 v134, v151, v149, vcc
	s_cselect_b32 s59, s21, s59
	s_cselect_b32 s58, s20, s58
	v_cndmask_b32_e32 v153, v152, v157, vcc
	v_cndmask_b32_e32 v228, v150, v162, vcc
	v_cndmask_b32_e32 v155, v154, v163, vcc
	s_cselect_b32 s57, s51, s89
	s_cselect_b32 s56, s50, s88
	v_lshl_add_u64 v[230:231], v[160:161], 0, s[54:55]
	s_add_i32 m0, s53, 0xc000
	ds_read_b128 v[196:199], v147
	ds_read_b128 v[200:203], v147 offset:1024
	ds_read_b128 v[204:207], v147 offset:2048
	ds_read_b128 v[208:211], v147 offset:3072
	ds_read_b128 v[212:215], v147 offset:4096
	ds_read_b128 v[216:219], v147 offset:5120
	ds_read_b128 v[220:223], v147 offset:6144
	ds_read_b128 v[224:227], v147 offset:7168
	global_load_lds_dwordx4 v[230:231], off
	v_lshl_add_u64 v[230:231], v[158:159], 0, s[54:55]
	s_add_i32 m0, s53, 0xe000
	s_nop 0
	global_load_lds_dwordx4 v[230:231], off
	s_waitcnt vmcnt(8)
	s_waitcnt lgkmcnt(0)
	s_barrier
	v_mfma_f32_16x16x32_bf16 v[126:129], v[164:167], v[196:199], v[126:129]
	v_mfma_f32_16x16x32_bf16 v[122:125], v[172:175], v[196:199], v[122:125]
	v_mfma_f32_16x16x32_bf16 v[110:113], v[164:167], v[204:207], v[110:113]
	v_mfma_f32_16x16x32_bf16 v[106:109], v[172:175], v[204:207], v[106:109]
	v_mfma_f32_16x16x32_bf16 v[94:97], v[164:167], v[212:215], v[94:97]
	v_mfma_f32_16x16x32_bf16 v[90:93], v[172:175], v[212:215], v[90:93]
	v_mfma_f32_16x16x32_bf16 v[78:81], v[164:167], v[220:223], v[78:81]
	v_mfma_f32_16x16x32_bf16 v[74:77], v[172:175], v[220:223], v[74:77]
	v_mfma_f32_16x16x32_bf16 v[126:129], v[168:171], v[200:203], v[126:129]
	v_mfma_f32_16x16x32_bf16 v[122:125], v[176:179], v[200:203], v[122:125]
	v_mfma_f32_16x16x32_bf16 v[110:113], v[168:171], v[208:211], v[110:113]
	v_mfma_f32_16x16x32_bf16 v[106:109], v[176:179], v[208:211], v[106:109]
	v_mfma_f32_16x16x32_bf16 v[94:97], v[168:171], v[216:219], v[94:97]
	v_mfma_f32_16x16x32_bf16 v[90:93], v[176:179], v[216:219], v[90:93]
	v_mfma_f32_16x16x32_bf16 v[78:81], v[168:171], v[224:227], v[78:81]
	v_mfma_f32_16x16x32_bf16 v[74:77], v[176:179], v[224:227], v[74:77]
	v_mfma_f32_16x16x32_bf16 v[118:121], v[180:183], v[196:199], v[118:121]
	v_mfma_f32_16x16x32_bf16 v[114:117], v[188:191], v[196:199], v[114:117]
	v_mfma_f32_16x16x32_bf16 v[102:105], v[180:183], v[204:207], v[102:105]
	v_mfma_f32_16x16x32_bf16 v[98:101], v[188:191], v[204:207], v[98:101]
	v_mfma_f32_16x16x32_bf16 v[86:89], v[180:183], v[212:215], v[86:89]
	v_mfma_f32_16x16x32_bf16 v[82:85], v[188:191], v[212:215], v[82:85]
	v_mfma_f32_16x16x32_bf16 v[70:73], v[180:183], v[220:223], v[70:73]
	v_mfma_f32_16x16x32_bf16 v[66:69], v[188:191], v[220:223], v[66:69]
	v_mfma_f32_16x16x32_bf16 v[118:121], v[184:187], v[200:203], v[118:121]
	v_mfma_f32_16x16x32_bf16 v[114:117], v[192:195], v[200:203], v[114:117]
	v_mfma_f32_16x16x32_bf16 v[102:105], v[184:187], v[208:211], v[102:105]
	v_mfma_f32_16x16x32_bf16 v[98:101], v[192:195], v[208:211], v[98:101]
	v_mfma_f32_16x16x32_bf16 v[86:89], v[184:187], v[216:219], v[86:89]
	v_mfma_f32_16x16x32_bf16 v[82:85], v[192:195], v[216:219], v[82:85]
	v_mfma_f32_16x16x32_bf16 v[70:73], v[184:187], v[224:227], v[70:73]
	v_mfma_f32_16x16x32_bf16 v[66:69], v[192:195], v[224:227], v[66:69]
	s_barrier
	s_add_i32 s88, s79, s71
	v_lshl_add_u64 v[230:231], s[56:57], 0, v[130:131]
	s_mov_b32 m0, s88
	s_nop 0
	global_load_lds_dwordx4 v[230:231], off
	s_add_i32 m0, s88, 0x2000
	s_add_u32 s88, s56, 0x80000
	v_lshl_add_u64 v[232:233], s[56:57], 0, v[132:133]
	s_addc_u32 s89, s57, 0
	s_add_i32 s90, s80, s71
	global_load_lds_dwordx4 v[232:233], off
	v_lshl_add_u64 v[234:235], s[88:89], 0, v[130:131]
	s_mov_b32 m0, s90
	v_mov_b32_e32 v229, v135
	global_load_lds_dwordx4 v[234:235], off
	v_lshl_add_u64 v[234:235], s[88:89], 0, v[132:133]
	s_add_i32 m0, s90, 0x2000
	s_nop 0
	global_load_lds_dwordx4 v[234:235], off
	s_mov_b32 m0, s53
	v_lshl_add_u64 v[234:235], s[58:59], 0, v[134:135]
	global_load_lds_dwordx4 v134, s[58:59]
	s_mov_b32 m0, s72
	s_nop 0
	global_load_lds_dwordx4 v228, s[58:59]
	ds_read_b128 v[196:199], v147 offset:16384
	ds_read_b128 v[200:203], v147 offset:17408
	ds_read_b128 v[204:207], v147 offset:18432
	ds_read_b128 v[208:211], v147 offset:19456
	ds_read_b128 v[212:215], v147 offset:20480
	ds_read_b128 v[216:219], v147 offset:21504
	ds_read_b128 v[220:223], v147 offset:22528
	ds_read_b128 v[224:227], v147 offset:23552
	s_waitcnt vmcnt(8)
	s_waitcnt lgkmcnt(0)
	v_lshl_add_u64 v[228:229], s[58:59], 0, v[228:229]
	s_barrier
; #define PG8_STAGE(bufoff, gbase, voff) do { _Pragma("unroll") for (int _i = 0; _i < 2; ++_i) \
;         __builtin_amdgcn_global_load_lds((const unsigned*)((const char*)(gbase) + (voff)[_i]), (PG8_LAS unsigned*)(lds + (bufoff) + ldsw + _i * 8192), 16, 0, 0); } while (0)
; #define PG8_LDA(dst, b, h) do { _Pragma("unroll") for (int m = 0; m < 4; ++m) _Pragma("unroll") for (int k = 0; k < 2; ++k) dst[m][k] = *(const PG8_LAS bf16x8*)(lds + PG8_SA(b, h) + aoff + m * 2048 + k * 1024); } while (0)
; #define PG8_LDB(dst, b, h) do { _Pragma("unroll") for (int n = 0; n < 2; ++n) _Pragma("unroll") for (int k = 0; k < 2; ++k) dst[n][k] = *(const PG8_LAS bf16x8*)(lds + PG8_SB(b, h) + boff + n * 2048 + k * 1024); } while (0)
; #define PG8_MMA(ai, bj, At, Bt) do { __builtin_amdgcn_s_setprio(1); _Pragma("unroll") for (int m = 0; m < 4; ++m) _Pragma("unroll") for (int n = 0; n < 2; ++n) _Pragma("unroll") for (int k = 0; k < 2; ++k) \
;         acc[ai][bj][m][n] = __builtin_amdgcn_mfma_f32_16x16x32_bf16(Bt[n][k], At[m][k], acc[ai][bj][m][n], 0, 0, 0); __builtin_amdgcn_s_setprio(0); } while (0)
; #define PG8_WAIT_V(n) asm volatile("s_waitcnt vmcnt(" #n ")" ::: "memory")
; #define PG8_WAIT_L(n) asm volatile("s_waitcnt lgkmcnt(" #n ")" ::: "memory")
; #define PG8_BAR __builtin_amdgcn_s_barrier()
; #define PG8_SCHED __builtin_amdgcn_sched_barrier(0)
; template <class Epi, class Sched, bool ALIGN_EPI = false>
; __device__ __forceinline__ void gemm_phase(PG8_LAS unsigned char* lds, const Gemm g, const Sched& S, const Epi& E) {
;     ...
;             PG8_WAIT_V(8); PG8_WAIT_L(0); PG8_BAR; PG8_MMA(1, 0, At, B0); PG8_MMA(1, 1, At, B1); PG8_BAR; PG8_SCHED;
;             PG8_LDB(B0, 1, 0); PG8_LDB(B1, 1, 1); PG8_SCHED; PG8_LDA(At, 1, 0); PG8_STAGE(PG8_SA(0, 1), a2 + hstepA, w1);
;             PG8_WAIT_V(8); PG8_WAIT_L(0); PG8_BAR; PG8_MMA(0, 0, At, B0); PG8_MMA(0, 1, At, B1); PG8_BAR; PG8_SCHED;
	v_mfma_f32_16x16x32_bf16 v[62:65], v[164:167], v[196:199], v[62:65]
	v_mfma_f32_16x16x32_bf16 v[58:61], v[172:175], v[196:199], v[58:61]
	v_mfma_f32_16x16x32_bf16 v[50:53], v[164:167], v[204:207], v[50:53]
	v_mfma_f32_16x16x32_bf16 v[42:45], v[172:175], v[204:207], v[42:45]
	v_mfma_f32_16x16x32_bf16 v[34:37], v[164:167], v[212:215], v[34:37]
	v_mfma_f32_16x16x32_bf16 v[30:33], v[172:175], v[212:215], v[30:33]
	v_mfma_f32_16x16x32_bf16 v[14:17], v[164:167], v[220:223], v[14:17]
	v_mfma_f32_16x16x32_bf16 v[2:5], v[172:175], v[220:223], v[2:5]
	v_mfma_f32_16x16x32_bf16 v[62:65], v[168:171], v[200:203], v[62:65]
	v_mfma_f32_16x16x32_bf16 v[58:61], v[176:179], v[200:203], v[58:61]
	v_mfma_f32_16x16x32_bf16 v[50:53], v[168:171], v[208:211], v[50:53]
	v_mfma_f32_16x16x32_bf16 v[42:45], v[176:179], v[208:211], v[42:45]
	v_mfma_f32_16x16x32_bf16 v[34:37], v[168:171], v[216:219], v[34:37]
	v_mfma_f32_16x16x32_bf16 v[30:33], v[176:179], v[216:219], v[30:33]
	v_mfma_f32_16x16x32_bf16 v[14:17], v[168:171], v[224:227], v[14:17]
	v_mfma_f32_16x16x32_bf16 v[2:5], v[176:179], v[224:227], v[2:5]
	v_mfma_f32_16x16x32_bf16 v[54:57], v[180:183], v[196:199], v[54:57]
	v_mfma_f32_16x16x32_bf16 v[46:49], v[188:191], v[196:199], v[46:49]
	v_mfma_f32_16x16x32_bf16 v[38:41], v[180:183], v[204:207], v[38:41]
	v_mfma_f32_16x16x32_bf16 v[26:29], v[188:191], v[204:207], v[26:29]
	v_mfma_f32_16x16x32_bf16 v[22:25], v[180:183], v[212:215], v[22:25]
	v_mfma_f32_16x16x32_bf16 v[18:21], v[188:191], v[212:215], v[18:21]
	v_mfma_f32_16x16x32_bf16 v[10:13], v[180:183], v[220:223], v[10:13]
	v_mfma_f32_16x16x32_bf16 v[6:9], v[188:191], v[220:223], v[6:9]
	v_mfma_f32_16x16x32_bf16 v[54:57], v[184:187], v[200:203], v[54:57]
	v_mfma_f32_16x16x32_bf16 v[46:49], v[192:195], v[200:203], v[46:49]
	v_mfma_f32_16x16x32_bf16 v[38:41], v[184:187], v[208:211], v[38:41]
	v_mfma_f32_16x16x32_bf16 v[26:29], v[192:195], v[208:211], v[26:29]
	v_mfma_f32_16x16x32_bf16 v[22:25], v[184:187], v[216:219], v[22:25]
	v_mfma_f32_16x16x32_bf16 v[18:21], v[192:195], v[216:219], v[18:21]
	v_mfma_f32_16x16x32_bf16 v[10:13], v[184:187], v[224:227], v[10:13]
	v_mfma_f32_16x16x32_bf16 v[6:9], v[192:195], v[224:227], v[6:9]
	s_barrier
	s_add_i32 s88, 0, 0x18000
	s_add_i32 s89, 0, 0x1c000
	s_mov_b32 m0, s73
	s_nop 0
	global_load_lds_dwordx4 v153, s[58:59]
	s_mov_b32 m0, s74
	s_nop 0
	global_load_lds_dwordx4 v155, s[58:59]
	v_add_u32_e32 v134, s88, v143
	ds_read_b128 v[164:167], v134
	ds_read_b128 v[168:171], v134 offset:1024
	ds_read_b128 v[172:175], v134 offset:2048
	ds_read_b128 v[176:179], v134 offset:3072
	v_add_u32_e32 v134, s89, v143
	ds_read_b128 v[180:183], v134
	ds_read_b128 v[184:187], v134 offset:1024
	ds_read_b128 v[188:191], v134 offset:2048
	ds_read_b128 v[192:195], v134 offset:3072
	ds_read_b128 v[196:199], v147 offset:32768
	ds_read_b128 v[200:203], v147 offset:33792
	ds_read_b128 v[204:207], v147 offset:34816
	ds_read_b128 v[208:211], v147 offset:35840
	ds_read_b128 v[212:215], v147 offset:36864
	ds_read_b128 v[216:219], v147 offset:37888
	ds_read_b128 v[220:223], v147 offset:38912
	ds_read_b128 v[224:227], v147 offset:39936
	s_waitcnt vmcnt(8)
	s_waitcnt lgkmcnt(0)
	s_barrier
	v_mfma_f32_16x16x32_bf16 v[126:129], v[164:167], v[196:199], v[126:129]
	v_mfma_f32_16x16x32_bf16 v[122:125], v[172:175], v[196:199], v[122:125]
	v_mfma_f32_16x16x32_bf16 v[110:113], v[164:167], v[204:207], v[110:113]
	v_mfma_f32_16x16x32_bf16 v[106:109], v[172:175], v[204:207], v[106:109]
	v_mfma_f32_16x16x32_bf16 v[94:97], v[164:167], v[212:215], v[94:97]
	v_mfma_f32_16x16x32_bf16 v[90:93], v[172:175], v[212:215], v[90:93]
	v_mfma_f32_16x16x32_bf16 v[78:81], v[164:167], v[220:223], v[78:81]
	v_mfma_f32_16x16x32_bf16 v[74:77], v[172:175], v[220:223], v[74:77]
	v_mfma_f32_16x16x32_bf16 v[126:129], v[168:171], v[200:203], v[126:129]
	v_mfma_f32_16x16x32_bf16 v[122:125], v[176:179], v[200:203], v[122:125]
	v_mfma_f32_16x16x32_bf16 v[110:113], v[168:171], v[208:211], v[110:113]
	v_mfma_f32_16x16x32_bf16 v[106:109], v[176:179], v[208:211], v[106:109]
	v_mfma_f32_16x16x32_bf16 v[94:97], v[168:171], v[216:219], v[94:97]
	v_mfma_f32_16x16x32_bf16 v[90:93], v[176:179], v[216:219], v[90:93]
	v_mfma_f32_16x16x32_bf16 v[78:81], v[168:171], v[224:227], v[78:81]
	v_mfma_f32_16x16x32_bf16 v[74:77], v[176:179], v[224:227], v[74:77]
	v_mfma_f32_16x16x32_bf16 v[118:121], v[180:183], v[196:199], v[118:121]
	v_mfma_f32_16x16x32_bf16 v[114:117], v[188:191], v[196:199], v[114:117]
	v_mfma_f32_16x16x32_bf16 v[102:105], v[180:183], v[204:207], v[102:105]
	v_mfma_f32_16x16x32_bf16 v[98:101], v[188:191], v[204:207], v[98:101]
	v_mfma_f32_16x16x32_bf16 v[86:89], v[180:183], v[212:215], v[86:89]
	v_mfma_f32_16x16x32_bf16 v[82:85], v[188:191], v[212:215], v[82:85]
	v_mfma_f32_16x16x32_bf16 v[70:73], v[180:183], v[220:223], v[70:73]
	v_mfma_f32_16x16x32_bf16 v[66:69], v[188:191], v[220:223], v[66:69]
	v_mfma_f32_16x16x32_bf16 v[118:121], v[184:187], v[200:203], v[118:121]
	v_mfma_f32_16x16x32_bf16 v[114:117], v[192:195], v[200:203], v[114:117]
	v_mfma_f32_16x16x32_bf16 v[102:105], v[184:187], v[208:211], v[102:105]
	v_mfma_f32_16x16x32_bf16 v[98:101], v[192:195], v[208:211], v[98:101]
	v_mfma_f32_16x16x32_bf16 v[86:89], v[184:187], v[216:219], v[86:89]
	v_mfma_f32_16x16x32_bf16 v[82:85], v[192:195], v[216:219], v[82:85]
	v_mfma_f32_16x16x32_bf16 v[70:73], v[184:187], v[224:227], v[70:73]
	v_mfma_f32_16x16x32_bf16 v[66:69], v[192:195], v[224:227], v[66:69]
	s_barrier
; #define PG8_STAGE(bufoff, gbase, voff) do { _Pragma("unroll") for (int _i = 0; _i < 2; ++_i) \
;         __builtin_amdgcn_global_load_lds((const unsigned*)((const char*)(gbase) + (voff)[_i]), (PG8_LAS unsigned*)(lds + (bufoff) + ldsw + _i * 8192), 16, 0, 0); } while (0)
; #define PG8_LDA(dst, b, h) do { _Pragma("unroll") for (int m = 0; m < 4; ++m) _Pragma("unroll") for (int k = 0; k < 2; ++k) dst[m][k] = *(const PG8_LAS bf16x8*)(lds + PG8_SA(b, h) + aoff + m * 2048 + k * 1024); } while (0)
; #define PG8_MMA(ai, bj, At, Bt) do { __builtin_amdgcn_s_setprio(1); _Pragma("unroll") for (int m = 0; m < 4; ++m) _Pragma("unroll") for (int n = 0; n < 2; ++n) _Pragma("unroll") for (int k = 0; k < 2; ++k) \
;         acc[ai][bj][m][n] = __builtin_amdgcn_mfma_f32_16x16x32_bf16(Bt[n][k], At[m][k], acc[ai][bj][m][n], 0, 0, 0); __builtin_amdgcn_s_setprio(0); } while (0)
; #define PG8_WAIT_V(n) asm volatile("s_waitcnt vmcnt(" #n ")" ::: "memory")
; #define PG8_WAIT_L(n) asm volatile("s_waitcnt lgkmcnt(" #n ")" ::: "memory")
; #define PG8_BAR __builtin_amdgcn_s_barrier()
; #define PG8_SCHED __builtin_amdgcn_sched_barrier(0)
; template <class Epi, class Sched, bool ALIGN_EPI = false>
; __device__ __forceinline__ void gemm_phase(PG8_LAS unsigned char* lds, const Gemm g, const Sched& S, const Epi& E) {
;     ...
;             PG8_LDA(At, 1, 1); PG8_STAGE(PG8_SB(1, 0), b3, voffB); PG8_STAGE(PG8_SB(1, 1), b3 + hstep, voffB); PG8_STAGE(PG8_SA(1, 0), a3, w0);
;             PG8_WAIT_V(8); PG8_WAIT_L(0); PG8_BAR; PG8_MMA(1, 0, At, B0); PG8_MMA(1, 1, At, B1); PG8_BAR; PG8_SCHED;
;             if constexpr (Epi::KSCALE) { if (((t + 2) & 7) == 0 && t + 2 < nt) { E.kscale(acc, pf, ((t + 2) >> 3) - 1, wr, fr); PG8_SCHED; } }
;         }
;         if constexpr (ALIGN_EPI) { if (wr == 0) PG8_BAR; }
	s_add_i32 s58, s88, s71
	v_lshl_add_u64 v[230:231], v[230:231], 0, s[42:43]
	s_mov_b32 m0, s58
	s_nop 0
	global_load_lds_dwordx4 v[230:231], off
	s_add_i32 m0, s58, 0x2000
	s_add_u32 s56, s56, 0x80080
	v_lshl_add_u64 v[230:231], v[232:233], 0, s[42:43]
	s_addc_u32 s57, s57, 0
	s_add_i32 s58, s89, s71
	global_load_lds_dwordx4 v[230:231], off
	v_lshl_add_u64 v[230:231], s[56:57], 0, v[130:131]
	s_mov_b32 m0, s58
	v_lshl_add_u64 v[228:229], v[228:229], 0, s[42:43]
	global_load_lds_dwordx4 v[230:231], off
	v_lshl_add_u64 v[230:231], s[56:57], 0, v[132:133]
	s_add_i32 m0, s58, 0x2000
	s_nop 0
	global_load_lds_dwordx4 v[230:231], off
	v_lshl_add_u64 v[230:231], v[234:235], 0, s[42:43]
	s_mov_b32 m0, s77
	s_nop 0
	global_load_lds_dwordx4 v[230:231], off
	s_mov_b32 m0, s78
	s_nop 0
	global_load_lds_dwordx4 v[228:229], off
	ds_read_b128 v[196:199], v147 offset:49152
	ds_read_b128 v[200:203], v147 offset:50176
	ds_read_b128 v[204:207], v147 offset:51200
	ds_read_b128 v[208:211], v147 offset:52224
	ds_read_b128 v[212:215], v147 offset:53248
	ds_read_b128 v[216:219], v147 offset:54272
	ds_read_b128 v[220:223], v147 offset:55296
	ds_read_b128 v[224:227], v147 offset:56320
	s_waitcnt vmcnt(8)
	s_waitcnt lgkmcnt(0)
	s_barrier
	v_mfma_f32_16x16x32_bf16 v[62:65], v[164:167], v[196:199], v[62:65]
	v_mfma_f32_16x16x32_bf16 v[58:61], v[172:175], v[196:199], v[58:61]
	v_mfma_f32_16x16x32_bf16 v[50:53], v[164:167], v[204:207], v[50:53]
	v_mfma_f32_16x16x32_bf16 v[42:45], v[172:175], v[204:207], v[42:45]
	v_mfma_f32_16x16x32_bf16 v[34:37], v[164:167], v[212:215], v[34:37]
	v_mfma_f32_16x16x32_bf16 v[30:33], v[172:175], v[212:215], v[30:33]
	v_mfma_f32_16x16x32_bf16 v[14:17], v[164:167], v[220:223], v[14:17]
	v_mfma_f32_16x16x32_bf16 v[2:5], v[172:175], v[220:223], v[2:5]
	v_mfma_f32_16x16x32_bf16 v[62:65], v[168:171], v[200:203], v[62:65]
	v_mfma_f32_16x16x32_bf16 v[58:61], v[176:179], v[200:203], v[58:61]
	v_mfma_f32_16x16x32_bf16 v[50:53], v[168:171], v[208:211], v[50:53]
	v_mfma_f32_16x16x32_bf16 v[42:45], v[176:179], v[208:211], v[42:45]
	v_mfma_f32_16x16x32_bf16 v[34:37], v[168:171], v[216:219], v[34:37]
	v_mfma_f32_16x16x32_bf16 v[30:33], v[176:179], v[216:219], v[30:33]
	v_mfma_f32_16x16x32_bf16 v[14:17], v[168:171], v[224:227], v[14:17]
	v_mfma_f32_16x16x32_bf16 v[2:5], v[176:179], v[224:227], v[2:5]
	v_mfma_f32_16x16x32_bf16 v[54:57], v[180:183], v[196:199], v[54:57]
	v_mfma_f32_16x16x32_bf16 v[46:49], v[188:191], v[196:199], v[46:49]
	v_mfma_f32_16x16x32_bf16 v[38:41], v[180:183], v[204:207], v[38:41]
	v_mfma_f32_16x16x32_bf16 v[26:29], v[188:191], v[204:207], v[26:29]
	v_mfma_f32_16x16x32_bf16 v[22:25], v[180:183], v[212:215], v[22:25]
	v_mfma_f32_16x16x32_bf16 v[18:21], v[188:191], v[212:215], v[18:21]
	v_mfma_f32_16x16x32_bf16 v[10:13], v[180:183], v[220:223], v[10:13]
	v_mfma_f32_16x16x32_bf16 v[6:9], v[188:191], v[220:223], v[6:9]
	v_mfma_f32_16x16x32_bf16 v[54:57], v[184:187], v[200:203], v[54:57]
	v_mfma_f32_16x16x32_bf16 v[46:49], v[192:195], v[200:203], v[46:49]
	v_mfma_f32_16x16x32_bf16 v[38:41], v[184:187], v[208:211], v[38:41]
	v_mfma_f32_16x16x32_bf16 v[26:29], v[192:195], v[208:211], v[26:29]
	v_mfma_f32_16x16x32_bf16 v[22:25], v[184:187], v[216:219], v[22:25]
	v_mfma_f32_16x16x32_bf16 v[18:21], v[192:195], v[216:219], v[18:21]
	v_mfma_f32_16x16x32_bf16 v[10:13], v[184:187], v[224:227], v[10:13]
	v_mfma_f32_16x16x32_bf16 v[6:9], v[192:195], v[224:227], v[6:9]
	s_barrier
	s_add_i32 s87, s87, 2
	s_add_u32 s54, s54, 0x100
	s_addc_u32 s55, s55, 0
	s_cmp_gt_u32 s87, 29
	s_cbranch_scc0 .LBB0_1414
	s_and_b64 vcc, exec, s[44:45]
	s_cbranch_vccz .LBB0_1417
	s_barrier

; #define PG8_STAGE(bufoff, gbase, voff) do { _Pragma("unroll") for (int _i = 0; _i < 2; ++_i) \
;         __builtin_amdgcn_global_load_lds((const unsigned*)((const char*)(gbase) + (voff)[_i]), (PG8_LAS unsigned*)(lds + (bufoff) + ldsw + _i * 8192), 16, 0, 0); } while (0)
; #define PG8_LDA(dst, b, h) do { _Pragma("unroll") for (int m = 0; m < 4; ++m) _Pragma("unroll") for (int k = 0; k < 2; ++k) dst[m][k] = *(const PG8_LAS bf16x8*)(lds + PG8_SA(b, h) + aoff + m * 2048 + k * 1024); } while (0)
; #define PG8_LDB(dst, b, h) do { _Pragma("unroll") for (int n = 0; n < 2; ++n) _Pragma("unroll") for (int k = 0; k < 2; ++k) dst[n][k] = *(const PG8_LAS bf16x8*)(lds + PG8_SB(b, h) + boff + n * 2048 + k * 1024); } while (0)
; #define PG8_MMA(ai, bj, At, Bt) do { __builtin_amdgcn_s_setprio(1); _Pragma("unroll") for (int m = 0; m < 4; ++m) _Pragma("unroll") for (int n = 0; n < 2; ++n) _Pragma("unroll") for (int k = 0; k < 2; ++k) \
;         acc[ai][bj][m][n] = __builtin_amdgcn_mfma_f32_16x16x32_bf16(Bt[n][k], At[m][k], acc[ai][bj][m][n], 0, 0, 0); __builtin_amdgcn_s_setprio(0); } while (0)
; #define PG8_WAIT_V(n) asm volatile("s_waitcnt vmcnt(" #n ")" ::: "memory")
; #define PG8_WAIT_L(n) asm volatile("s_waitcnt lgkmcnt(" #n ")" ::: "memory")
; template <class Epi, class Sched, bool ALIGN_EPI = false>
; __device__ __forceinline__ void gemm_phase(PG8_LAS unsigned char* lds, const Gemm g, const Sched& S, const Epi& E) {
;     ...
;             const bool last = (t == nt - 2);
;             const char* a1 = cA + (size_t)(t + 1) * kstep;
;             const char* a2 = last ? nA : cA + (size_t)(t + 2) * kstep; const char* b2 = last ? nB : cB + (size_t)(t + 2) * kstep;
;             const char* a3 = a2 + kstep; const char* b3 = b2 + kstep;
;             unsigned w0[2], w1[2];
; #pragma unroll
;             for (int i = 0; i < 2; ++i) { w0[i] = (Sched::GATHER && last) ? vn0[i] : vc0[i]; w1[i] = (Sched::GATHER && last) ? vn1[i] : vc1[i]; }
;             if (last && has_next) S.a_ready(nxt);
;             PG8_LDB(B0, 0, 0); PG8_LDB(B1, 0, 1); PG8_SCHED; PG8_LDA(At, 0, 0); PG8_STAGE(PG8_SA(1, 1), a1 + hstepA, vc1);
;             PG8_WAIT_V(8); PG8_WAIT_L(0); PG8_BAR; PG8_MMA(0, 0, At, B0); PG8_MMA(0, 1, At, B1); PG8_BAR; PG8_SCHED;
;             PG8_LDA(At, 0, 1); PG8_STAGE(PG8_SB(0, 0), b2, voffB); PG8_STAGE(PG8_SB(0, 1), b2 + hstep, voffB); PG8_STAGE(PG8_SA(0, 0), a2, w0);
.LBB0_1480:
	s_add_u32 s16, s14, 0x3c800100
	s_addc_u32 s17, s15, 0
	s_add_u32 s56, s14, s43
	s_addc_u32 s57, s15, s44
	s_cmp_eq_u32 s45, 28
	s_cselect_b32 s19, s21, s17
	s_cselect_b32 s18, s20, s16
	s_cselect_b32 s17, s11, s57
	s_cselect_b32 s16, s10, s56
	s_mov_b32 m0, s46
	v_lshl_add_u64 v[236:237], s[14:15], 0, v[160:161]
	global_load_lds_dwordx4 v[236:237], off
	v_lshl_add_u64 v[236:237], s[14:15], 0, v[158:159]
	s_mov_b32 m0, s47
	s_nop 0
	global_load_lds_dwordx4 v[236:237], off
	ds_read_b128 v[172:175], v167
	ds_read_b128 v[176:179], v167 offset:1024
	ds_read_b128 v[180:183], v167 offset:2048
	ds_read_b128 v[184:187], v167 offset:3072
	ds_read_b128 v[188:191], v168
	ds_read_b128 v[192:195], v168 offset:1024
	ds_read_b128 v[196:199], v168 offset:2048
	ds_read_b128 v[200:203], v168 offset:3072
	ds_read_b128 v[204:207], v169
	ds_read_b128 v[208:211], v169 offset:1024
	ds_read_b128 v[212:215], v169 offset:2048
	ds_read_b128 v[216:219], v169 offset:3072
	ds_read_b128 v[220:223], v169 offset:4096
	ds_read_b128 v[224:227], v169 offset:5120
	ds_read_b128 v[228:231], v169 offset:6144
	ds_read_b128 v[232:235], v169 offset:7168
	s_waitcnt vmcnt(8)
	s_waitcnt lgkmcnt(0)
	s_barrier
	v_mfma_f32_16x16x32_bf16 v[126:129], v[172:175], v[204:207], v[126:129]
	v_mfma_f32_16x16x32_bf16 v[122:125], v[180:183], v[204:207], v[122:125]
	v_mfma_f32_16x16x32_bf16 v[110:113], v[172:175], v[212:215], v[110:113]
	v_mfma_f32_16x16x32_bf16 v[106:109], v[180:183], v[212:215], v[106:109]
	v_mfma_f32_16x16x32_bf16 v[94:97], v[172:175], v[220:223], v[94:97]
	v_mfma_f32_16x16x32_bf16 v[90:93], v[180:183], v[220:223], v[90:93]
	v_mfma_f32_16x16x32_bf16 v[78:81], v[172:175], v[228:231], v[78:81]
	v_mfma_f32_16x16x32_bf16 v[74:77], v[180:183], v[228:231], v[74:77]
	v_mfma_f32_16x16x32_bf16 v[126:129], v[176:179], v[208:211], v[126:129]
	v_mfma_f32_16x16x32_bf16 v[122:125], v[184:187], v[208:211], v[122:125]
	v_mfma_f32_16x16x32_bf16 v[110:113], v[176:179], v[216:219], v[110:113]
	v_mfma_f32_16x16x32_bf16 v[106:109], v[184:187], v[216:219], v[106:109]
	v_mfma_f32_16x16x32_bf16 v[94:97], v[176:179], v[224:227], v[94:97]
	v_mfma_f32_16x16x32_bf16 v[90:93], v[184:187], v[224:227], v[90:93]
	v_mfma_f32_16x16x32_bf16 v[78:81], v[176:179], v[232:235], v[78:81]
	v_mfma_f32_16x16x32_bf16 v[74:77], v[184:187], v[232:235], v[74:77]
	v_mfma_f32_16x16x32_bf16 v[118:121], v[188:191], v[204:207], v[118:121]
	v_mfma_f32_16x16x32_bf16 v[114:117], v[196:199], v[204:207], v[114:117]
	v_mfma_f32_16x16x32_bf16 v[102:105], v[188:191], v[212:215], v[102:105]
	v_mfma_f32_16x16x32_bf16 v[98:101], v[196:199], v[212:215], v[98:101]
	v_mfma_f32_16x16x32_bf16 v[86:89], v[188:191], v[220:223], v[86:89]
	v_mfma_f32_16x16x32_bf16 v[82:85], v[196:199], v[220:223], v[82:85]
	v_mfma_f32_16x16x32_bf16 v[70:73], v[188:191], v[228:231], v[70:73]
	v_mfma_f32_16x16x32_bf16 v[66:69], v[196:199], v[228:231], v[66:69]
	v_mfma_f32_16x16x32_bf16 v[118:121], v[192:195], v[208:211], v[118:121]
	v_mfma_f32_16x16x32_bf16 v[114:117], v[200:203], v[208:211], v[114:117]
	v_mfma_f32_16x16x32_bf16 v[102:105], v[192:195], v[216:219], v[102:105]
	v_mfma_f32_16x16x32_bf16 v[98:101], v[200:203], v[216:219], v[98:101]
	v_mfma_f32_16x16x32_bf16 v[86:89], v[192:195], v[224:227], v[86:89]
	v_mfma_f32_16x16x32_bf16 v[82:85], v[200:203], v[224:227], v[82:85]
	v_mfma_f32_16x16x32_bf16 v[70:73], v[192:195], v[232:235], v[70:73]
	v_mfma_f32_16x16x32_bf16 v[66:69], v[200:203], v[232:235], v[66:69]
	s_barrier
	s_mov_b32 m0, s48
	v_lshl_add_u64 v[236:237], s[16:17], 0, v[146:147]
	s_add_u32 s56, s16, 0x80000
	global_load_lds_dwordx4 v[236:237], off
	v_lshl_add_u64 v[238:239], s[16:17], 0, v[144:145]
	s_mov_b32 m0, s49
	s_addc_u32 s57, s17, 0
	global_load_lds_dwordx4 v[238:239], off
	v_lshl_add_u64 v[240:241], s[56:57], 0, v[146:147]
	s_mov_b32 m0, s50
	v_lshl_add_u64 v[242:243], s[18:19], 0, v[150:151]
	global_load_lds_dwordx4 v[240:241], off
	v_lshl_add_u64 v[240:241], s[56:57], 0, v[144:145]
	s_mov_b32 m0, s51
	s_nop 0
	global_load_lds_dwordx4 v[240:241], off
	v_lshl_add_u64 v[240:241], s[18:19], 0, v[148:149]
	s_mov_b32 m0, s25
	s_nop 0
	global_load_lds_dwordx4 v[240:241], off
	s_mov_b32 m0, s26
	s_nop 0
	global_load_lds_dwordx4 v[242:243], off
	ds_read_b128 v[204:207], v169 offset:16384
	ds_read_b128 v[208:211], v169 offset:17408
	ds_read_b128 v[212:215], v169 offset:18432
	ds_read_b128 v[216:219], v169 offset:19456
	ds_read_b128 v[220:223], v169 offset:20480
	ds_read_b128 v[224:227], v169 offset:21504
	ds_read_b128 v[228:231], v169 offset:22528
	ds_read_b128 v[232:235], v169 offset:23552
	s_waitcnt vmcnt(8)
	s_waitcnt lgkmcnt(0)
	s_barrier
; #define PG8_STAGE(bufoff, gbase, voff) do { _Pragma("unroll") for (int _i = 0; _i < 2; ++_i) \
;         __builtin_amdgcn_global_load_lds((const unsigned*)((const char*)(gbase) + (voff)[_i]), (PG8_LAS unsigned*)(lds + (bufoff) + ldsw + _i * 8192), 16, 0, 0); } while (0)
; #define PG8_LDA(dst, b, h) do { _Pragma("unroll") for (int m = 0; m < 4; ++m) _Pragma("unroll") for (int k = 0; k < 2; ++k) dst[m][k] = *(const PG8_LAS bf16x8*)(lds + PG8_SA(b, h) + aoff + m * 2048 + k * 1024); } while (0)
; #define PG8_LDB(dst, b, h) do { _Pragma("unroll") for (int n = 0; n < 2; ++n) _Pragma("unroll") for (int k = 0; k < 2; ++k) dst[n][k] = *(const PG8_LAS bf16x8*)(lds + PG8_SB(b, h) + boff + n * 2048 + k * 1024); } while (0)
; #define PG8_MMA(ai, bj, At, Bt) do { __builtin_amdgcn_s_setprio(1); _Pragma("unroll") for (int m = 0; m < 4; ++m) _Pragma("unroll") for (int n = 0; n < 2; ++n) _Pragma("unroll") for (int k = 0; k < 2; ++k) \
;         acc[ai][bj][m][n] = __builtin_amdgcn_mfma_f32_16x16x32_bf16(Bt[n][k], At[m][k], acc[ai][bj][m][n], 0, 0, 0); __builtin_amdgcn_s_setprio(0); } while (0)
; #define PG8_WAIT_V(n) asm volatile("s_waitcnt vmcnt(" #n ")" ::: "memory")
; #define PG8_WAIT_L(n) asm volatile("s_waitcnt lgkmcnt(" #n ")" ::: "memory")
; #define PG8_BAR __builtin_amdgcn_s_barrier()
; #define PG8_SCHED __builtin_amdgcn_sched_barrier(0)
; template <class Epi, class Sched, bool ALIGN_EPI = false>
; __device__ __forceinline__ void gemm_phase(PG8_LAS unsigned char* lds, const Gemm g, const Sched& S, const Epi& E) {
;     ...
;             PG8_WAIT_V(8); PG8_WAIT_L(0); PG8_BAR; PG8_MMA(1, 0, At, B0); PG8_MMA(1, 1, At, B1); PG8_BAR; PG8_SCHED;
;             PG8_LDB(B0, 1, 0); PG8_LDB(B1, 1, 1); PG8_SCHED; PG8_LDA(At, 1, 0); PG8_STAGE(PG8_SA(0, 1), a2 + hstepA, w1);
;             PG8_WAIT_V(8); PG8_WAIT_L(0); PG8_BAR; PG8_MMA(0, 0, At, B0); PG8_MMA(0, 1, At, B1); PG8_BAR; PG8_SCHED;
	v_mfma_f32_16x16x32_bf16 v[62:65], v[172:175], v[204:207], v[62:65]
	v_mfma_f32_16x16x32_bf16 v[58:61], v[180:183], v[204:207], v[58:61]
	v_mfma_f32_16x16x32_bf16 v[50:53], v[172:175], v[212:215], v[50:53]
	v_mfma_f32_16x16x32_bf16 v[42:45], v[180:183], v[212:215], v[42:45]
	v_mfma_f32_16x16x32_bf16 v[34:37], v[172:175], v[220:223], v[34:37]
	v_mfma_f32_16x16x32_bf16 v[26:29], v[180:183], v[220:223], v[26:29]
	v_mfma_f32_16x16x32_bf16 v[14:17], v[172:175], v[228:231], v[14:17]
	v_mfma_f32_16x16x32_bf16 v[2:5], v[180:183], v[228:231], v[2:5]
	v_mfma_f32_16x16x32_bf16 v[62:65], v[176:179], v[208:211], v[62:65]
	v_mfma_f32_16x16x32_bf16 v[58:61], v[184:187], v[208:211], v[58:61]
	v_mfma_f32_16x16x32_bf16 v[50:53], v[176:179], v[216:219], v[50:53]
	v_mfma_f32_16x16x32_bf16 v[42:45], v[184:187], v[216:219], v[42:45]
	v_mfma_f32_16x16x32_bf16 v[34:37], v[176:179], v[224:227], v[34:37]
	v_mfma_f32_16x16x32_bf16 v[26:29], v[184:187], v[224:227], v[26:29]
	v_mfma_f32_16x16x32_bf16 v[14:17], v[176:179], v[232:235], v[14:17]
	v_mfma_f32_16x16x32_bf16 v[2:5], v[184:187], v[232:235], v[2:5]
	v_mfma_f32_16x16x32_bf16 v[54:57], v[188:191], v[204:207], v[54:57]
	v_mfma_f32_16x16x32_bf16 v[46:49], v[196:199], v[204:207], v[46:49]
	v_mfma_f32_16x16x32_bf16 v[38:41], v[188:191], v[212:215], v[38:41]
	v_mfma_f32_16x16x32_bf16 v[30:33], v[196:199], v[212:215], v[30:33]
	v_mfma_f32_16x16x32_bf16 v[22:25], v[188:191], v[220:223], v[22:25]
	v_mfma_f32_16x16x32_bf16 v[18:21], v[196:199], v[220:223], v[18:21]
	v_mfma_f32_16x16x32_bf16 v[10:13], v[188:191], v[228:231], v[10:13]
	v_mfma_f32_16x16x32_bf16 v[6:9], v[196:199], v[228:231], v[6:9]
	v_mfma_f32_16x16x32_bf16 v[54:57], v[192:195], v[208:211], v[54:57]
	v_mfma_f32_16x16x32_bf16 v[46:49], v[200:203], v[208:211], v[46:49]
	v_mfma_f32_16x16x32_bf16 v[38:41], v[192:195], v[216:219], v[38:41]
	v_mfma_f32_16x16x32_bf16 v[30:33], v[200:203], v[216:219], v[30:33]
	v_mfma_f32_16x16x32_bf16 v[22:25], v[192:195], v[224:227], v[22:25]
	v_mfma_f32_16x16x32_bf16 v[18:21], v[200:203], v[224:227], v[18:21]
	v_mfma_f32_16x16x32_bf16 v[10:13], v[192:195], v[232:235], v[10:13]
	v_mfma_f32_16x16x32_bf16 v[6:9], v[200:203], v[232:235], v[6:9]
	s_barrier
	s_mov_b32 m0, s27
	v_lshl_add_u64 v[244:245], s[18:19], 0, v[152:153]
	global_load_lds_dwordx4 v[244:245], off
	v_lshl_add_u64 v[244:245], s[18:19], 0, v[154:155]
	s_mov_b32 m0, s35
	s_nop 0
	global_load_lds_dwordx4 v[244:245], off
	ds_read_b128 v[172:175], v170
	ds_read_b128 v[176:179], v170 offset:1024
	ds_read_b128 v[180:183], v170 offset:2048
	ds_read_b128 v[184:187], v170 offset:3072
	ds_read_b128 v[188:191], v171
	ds_read_b128 v[192:195], v171 offset:1024
	ds_read_b128 v[196:199], v171 offset:2048
	ds_read_b128 v[200:203], v171 offset:3072
	ds_read_b128 v[204:207], v169 offset:32768
	ds_read_b128 v[208:211], v169 offset:33792
	ds_read_b128 v[212:215], v169 offset:34816
	ds_read_b128 v[216:219], v169 offset:35840
	ds_read_b128 v[220:223], v169 offset:36864
	ds_read_b128 v[224:227], v169 offset:37888
	ds_read_b128 v[228:231], v169 offset:38912
	ds_read_b128 v[232:235], v169 offset:39936
	s_waitcnt vmcnt(8)
	s_waitcnt lgkmcnt(0)
	s_barrier
	v_mfma_f32_16x16x32_bf16 v[126:129], v[172:175], v[204:207], v[126:129]
	v_mfma_f32_16x16x32_bf16 v[122:125], v[180:183], v[204:207], v[122:125]
	v_mfma_f32_16x16x32_bf16 v[110:113], v[172:175], v[212:215], v[110:113]
	v_mfma_f32_16x16x32_bf16 v[106:109], v[180:183], v[212:215], v[106:109]
	v_mfma_f32_16x16x32_bf16 v[94:97], v[172:175], v[220:223], v[94:97]
	v_mfma_f32_16x16x32_bf16 v[90:93], v[180:183], v[220:223], v[90:93]
	v_mfma_f32_16x16x32_bf16 v[78:81], v[172:175], v[228:231], v[78:81]
	v_mfma_f32_16x16x32_bf16 v[74:77], v[180:183], v[228:231], v[74:77]
	v_mfma_f32_16x16x32_bf16 v[126:129], v[176:179], v[208:211], v[126:129]
	v_mfma_f32_16x16x32_bf16 v[122:125], v[184:187], v[208:211], v[122:125]
	v_mfma_f32_16x16x32_bf16 v[110:113], v[176:179], v[216:219], v[110:113]
	v_mfma_f32_16x16x32_bf16 v[106:109], v[184:187], v[216:219], v[106:109]
	v_mfma_f32_16x16x32_bf16 v[94:97], v[176:179], v[224:227], v[94:97]
	v_mfma_f32_16x16x32_bf16 v[90:93], v[184:187], v[224:227], v[90:93]
	v_mfma_f32_16x16x32_bf16 v[78:81], v[176:179], v[232:235], v[78:81]
	v_mfma_f32_16x16x32_bf16 v[74:77], v[184:187], v[232:235], v[74:77]
	v_mfma_f32_16x16x32_bf16 v[118:121], v[188:191], v[204:207], v[118:121]
	v_mfma_f32_16x16x32_bf16 v[114:117], v[196:199], v[204:207], v[114:117]
	v_mfma_f32_16x16x32_bf16 v[102:105], v[188:191], v[212:215], v[102:105]
	v_mfma_f32_16x16x32_bf16 v[98:101], v[196:199], v[212:215], v[98:101]
	v_mfma_f32_16x16x32_bf16 v[86:89], v[188:191], v[220:223], v[86:89]
	v_mfma_f32_16x16x32_bf16 v[82:85], v[196:199], v[220:223], v[82:85]
	v_mfma_f32_16x16x32_bf16 v[70:73], v[188:191], v[228:231], v[70:73]
	v_mfma_f32_16x16x32_bf16 v[66:69], v[196:199], v[228:231], v[66:69]
	v_mfma_f32_16x16x32_bf16 v[118:121], v[192:195], v[208:211], v[118:121]
	v_mfma_f32_16x16x32_bf16 v[114:117], v[200:203], v[208:211], v[114:117]
	v_mfma_f32_16x16x32_bf16 v[102:105], v[192:195], v[216:219], v[102:105]
	v_mfma_f32_16x16x32_bf16 v[98:101], v[200:203], v[216:219], v[98:101]
	v_mfma_f32_16x16x32_bf16 v[86:89], v[192:195], v[224:227], v[86:89]
	v_mfma_f32_16x16x32_bf16 v[82:85], v[200:203], v[224:227], v[82:85]
	v_mfma_f32_16x16x32_bf16 v[70:73], v[192:195], v[232:235], v[70:73]
	v_mfma_f32_16x16x32_bf16 v[66:69], v[200:203], v[232:235], v[66:69]
	s_barrier
; #define PG8_STAGE(bufoff, gbase, voff) do { _Pragma("unroll") for (int _i = 0; _i < 2; ++_i) \
;         __builtin_amdgcn_global_load_lds((const unsigned*)((const char*)(gbase) + (voff)[_i]), (PG8_LAS unsigned*)(lds + (bufoff) + ldsw + _i * 8192), 16, 0, 0); } while (0)
; #define PG8_LDA(dst, b, h) do { _Pragma("unroll") for (int m = 0; m < 4; ++m) _Pragma("unroll") for (int k = 0; k < 2; ++k) dst[m][k] = *(const PG8_LAS bf16x8*)(lds + PG8_SA(b, h) + aoff + m * 2048 + k * 1024); } while (0)
; #define PG8_MMA(ai, bj, At, Bt) do { __builtin_amdgcn_s_setprio(1); _Pragma("unroll") for (int m = 0; m < 4; ++m) _Pragma("unroll") for (int n = 0; n < 2; ++n) _Pragma("unroll") for (int k = 0; k < 2; ++k) \
;         acc[ai][bj][m][n] = __builtin_amdgcn_mfma_f32_16x16x32_bf16(Bt[n][k], At[m][k], acc[ai][bj][m][n], 0, 0, 0); __builtin_amdgcn_s_setprio(0); } while (0)
; #define PG8_WAIT_V(n) asm volatile("s_waitcnt vmcnt(" #n ")" ::: "memory")
; #define PG8_WAIT_L(n) asm volatile("s_waitcnt lgkmcnt(" #n ")" ::: "memory")
; #define PG8_BAR __builtin_amdgcn_s_barrier()
; #define PG8_SCHED __builtin_amdgcn_sched_barrier(0)
; template <class Epi, class Sched, bool ALIGN_EPI = false>
; __device__ __forceinline__ void gemm_phase(PG8_LAS unsigned char* lds, const Gemm g, const Sched& S, const Epi& E) {
;     ...
;             PG8_LDA(At, 1, 1); PG8_STAGE(PG8_SB(1, 0), b3, voffB); PG8_STAGE(PG8_SB(1, 1), b3 + hstep, voffB); PG8_STAGE(PG8_SA(1, 0), a3, w0);
;             PG8_WAIT_V(8); PG8_WAIT_L(0); PG8_BAR; PG8_MMA(1, 0, At, B0); PG8_MMA(1, 1, At, B1); PG8_BAR; PG8_SCHED;
;             if constexpr (Epi::KSCALE) { if (((t + 2) & 7) == 0 && t + 2 < nt) { E.kscale(acc, pf, ((t + 2) >> 3) - 1, wr, fr); PG8_SCHED; } }
;         }
;         if constexpr (ALIGN_EPI) { if (wr == 0) PG8_BAR; }
	s_mov_b32 m0, s52
	v_lshl_add_u64 v[236:237], v[236:237], 0, s[12:13]
	s_add_u32 s16, s16, 0x80080
	global_load_lds_dwordx4 v[236:237], off
	v_lshl_add_u64 v[236:237], v[238:239], 0, s[12:13]
	s_mov_b32 m0, s53
	s_addc_u32 s17, s17, 0
	global_load_lds_dwordx4 v[236:237], off
	v_lshl_add_u64 v[236:237], s[16:17], 0, v[146:147]
	s_mov_b32 m0, s54
	s_nop 0
	global_load_lds_dwordx4 v[236:237], off
	v_lshl_add_u64 v[236:237], s[16:17], 0, v[144:145]
	s_mov_b32 m0, s55
	s_nop 0
	global_load_lds_dwordx4 v[236:237], off
	v_lshl_add_u64 v[236:237], v[240:241], 0, s[12:13]
	s_mov_b32 m0, s41
	s_nop 0
	global_load_lds_dwordx4 v[236:237], off
	v_lshl_add_u64 v[236:237], v[242:243], 0, s[12:13]
	s_mov_b32 m0, s42
	s_nop 0
	global_load_lds_dwordx4 v[236:237], off
	ds_read_b128 v[204:207], v169 offset:49152
	ds_read_b128 v[208:211], v169 offset:50176
	ds_read_b128 v[212:215], v169 offset:51200
	ds_read_b128 v[216:219], v169 offset:52224
	ds_read_b128 v[220:223], v169 offset:53248
	ds_read_b128 v[224:227], v169 offset:54272
	ds_read_b128 v[228:231], v169 offset:55296
	ds_read_b128 v[232:235], v169 offset:56320
	s_waitcnt vmcnt(8)
	s_waitcnt lgkmcnt(0)
	s_barrier
	v_mfma_f32_16x16x32_bf16 v[62:65], v[172:175], v[204:207], v[62:65]
	v_mfma_f32_16x16x32_bf16 v[58:61], v[180:183], v[204:207], v[58:61]
	v_mfma_f32_16x16x32_bf16 v[50:53], v[172:175], v[212:215], v[50:53]
	v_mfma_f32_16x16x32_bf16 v[42:45], v[180:183], v[212:215], v[42:45]
	v_mfma_f32_16x16x32_bf16 v[34:37], v[172:175], v[220:223], v[34:37]
	v_mfma_f32_16x16x32_bf16 v[26:29], v[180:183], v[220:223], v[26:29]
	v_mfma_f32_16x16x32_bf16 v[14:17], v[172:175], v[228:231], v[14:17]
	v_mfma_f32_16x16x32_bf16 v[2:5], v[180:183], v[228:231], v[2:5]
	v_mfma_f32_16x16x32_bf16 v[62:65], v[176:179], v[208:211], v[62:65]
	v_mfma_f32_16x16x32_bf16 v[58:61], v[184:187], v[208:211], v[58:61]
	v_mfma_f32_16x16x32_bf16 v[50:53], v[176:179], v[216:219], v[50:53]
	v_mfma_f32_16x16x32_bf16 v[42:45], v[184:187], v[216:219], v[42:45]
	v_mfma_f32_16x16x32_bf16 v[34:37], v[176:179], v[224:227], v[34:37]
	v_mfma_f32_16x16x32_bf16 v[26:29], v[184:187], v[224:227], v[26:29]
	v_mfma_f32_16x16x32_bf16 v[14:17], v[176:179], v[232:235], v[14:17]
	v_mfma_f32_16x16x32_bf16 v[2:5], v[184:187], v[232:235], v[2:5]
	v_mfma_f32_16x16x32_bf16 v[54:57], v[188:191], v[204:207], v[54:57]
	v_mfma_f32_16x16x32_bf16 v[46:49], v[196:199], v[204:207], v[46:49]
	v_mfma_f32_16x16x32_bf16 v[38:41], v[188:191], v[212:215], v[38:41]
	v_mfma_f32_16x16x32_bf16 v[30:33], v[196:199], v[212:215], v[30:33]
	v_mfma_f32_16x16x32_bf16 v[22:25], v[188:191], v[220:223], v[22:25]
	v_mfma_f32_16x16x32_bf16 v[18:21], v[196:199], v[220:223], v[18:21]
	v_mfma_f32_16x16x32_bf16 v[10:13], v[188:191], v[228:231], v[10:13]
	v_mfma_f32_16x16x32_bf16 v[6:9], v[196:199], v[228:231], v[6:9]
	v_mfma_f32_16x16x32_bf16 v[54:57], v[192:195], v[208:211], v[54:57]
	v_mfma_f32_16x16x32_bf16 v[46:49], v[200:203], v[208:211], v[46:49]
	v_mfma_f32_16x16x32_bf16 v[38:41], v[192:195], v[216:219], v[38:41]
	v_mfma_f32_16x16x32_bf16 v[30:33], v[200:203], v[216:219], v[30:33]
	v_mfma_f32_16x16x32_bf16 v[22:25], v[192:195], v[224:227], v[22:25]
	v_mfma_f32_16x16x32_bf16 v[18:21], v[200:203], v[224:227], v[18:21]
	v_mfma_f32_16x16x32_bf16 v[10:13], v[192:195], v[232:235], v[10:13]
	v_mfma_f32_16x16x32_bf16 v[6:9], v[200:203], v[232:235], v[6:9]
	s_barrier
	s_add_i32 s45, s45, 2
	s_add_u32 s14, s14, 0x100
	s_addc_u32 s15, s15, 0
	s_cmp_gt_u32 s45, 29
	s_cbranch_scc0 .LBB0_1480
	s_cmpk_lt_u32 s22, 0x100
	s_cbranch_scc0 .LBB0_1483
	s_barrier

; #define PG8_STAGE(bufoff, gbase, voff) do { _Pragma("unroll") for (int _i = 0; _i < 2; ++_i) \
;         __builtin_amdgcn_global_load_lds((const unsigned*)((const char*)(gbase) + (voff)[_i]), (PG8_LAS unsigned*)(lds + (bufoff) + ldsw + _i * 8192), 16, 0, 0); } while (0)
; #define PG8_LDA(dst, b, h) do { _Pragma("unroll") for (int m = 0; m < 4; ++m) _Pragma("unroll") for (int k = 0; k < 2; ++k) dst[m][k] = *(const PG8_LAS bf16x8*)(lds + PG8_SA(b, h) + aoff + m * 2048 + k * 1024); } while (0)
; #define PG8_LDB(dst, b, h) do { _Pragma("unroll") for (int n = 0; n < 2; ++n) _Pragma("unroll") for (int k = 0; k < 2; ++k) dst[n][k] = *(const PG8_LAS bf16x8*)(lds + PG8_SB(b, h) + boff + n * 2048 + k * 1024); } while (0)
; #define PG8_MMA(ai, bj, At, Bt) do { __builtin_amdgcn_s_setprio(1); _Pragma("unroll") for (int m = 0; m < 4; ++m) _Pragma("unroll") for (int n = 0; n < 2; ++n) _Pragma("unroll") for (int k = 0; k < 2; ++k) \
;         acc[ai][bj][m][n] = __builtin_amdgcn_mfma_f32_16x16x32_bf16(Bt[n][k], At[m][k], acc[ai][bj][m][n], 0, 0, 0); __builtin_amdgcn_s_setprio(0); } while (0)
; #define PG8_WAIT_V(n) asm volatile("s_waitcnt vmcnt(" #n ")" ::: "memory")
; #define PG8_WAIT_L(n) asm volatile("s_waitcnt lgkmcnt(" #n ")" ::: "memory")
; template <class Epi, class Sched, bool ALIGN_EPI = false>
; __device__ __forceinline__ void gemm_phase(PG8_LAS unsigned char* lds, const Gemm g, const Sched& S, const Epi& E) {
;     ...
;             const bool last = (t == nt - 2);
;             const char* a1 = cA + (size_t)(t + 1) * kstep;
;             const char* a2 = last ? nA : cA + (size_t)(t + 2) * kstep; const char* b2 = last ? nB : cB + (size_t)(t + 2) * kstep;
;             const char* a3 = a2 + kstep; const char* b3 = b2 + kstep;
;             unsigned w0[2], w1[2];
; #pragma unroll
;             for (int i = 0; i < 2; ++i) { w0[i] = (Sched::GATHER && last) ? vn0[i] : vc0[i]; w1[i] = (Sched::GATHER && last) ? vn1[i] : vc1[i]; }
;             if (last && has_next) S.a_ready(nxt);
;             PG8_LDB(B0, 0, 0); PG8_LDB(B1, 0, 1); PG8_SCHED; PG8_LDA(At, 0, 0); PG8_STAGE(PG8_SA(1, 1), a1 + hstepA, vc1);
;             PG8_WAIT_V(8); PG8_WAIT_L(0); PG8_BAR; PG8_MMA(0, 0, At, B0); PG8_MMA(0, 1, At, B1); PG8_BAR; PG8_SCHED;
;             PG8_LDA(At, 0, 1); PG8_STAGE(PG8_SB(0, 0), b2, voffB); PG8_STAGE(PG8_SB(0, 1), b2 + hstep, voffB); PG8_STAGE(PG8_SA(0, 0), a2, w0);
.LBB0_1498:
	s_add_u32 s58, s56, 0xfffe0080
	s_addc_u32 s59, s57, -1
	s_cmp_eq_u32 s87, 4
	s_cselect_b32 s61, s41, s59
	s_cselect_b32 s60, s53, s58
	s_cselect_b32 s59, s43, s86
	s_cselect_b32 s58, s84, s85
	v_lshl_add_u64 v[218:219], s[56:57], 0, v[140:141]
	s_add_i32 m0, s55, 0xc000
	s_nop 0
	global_load_lds_dwordx4 v[218:219], off
	v_lshl_add_u64 v[218:219], s[56:57], 0, v[138:139]
	s_add_i32 m0, s55, 0xe000
	s_nop 0
	global_load_lds_dwordx4 v[218:219], off
	ds_read_b128 v[142:145], v1
	ds_read_b128 v[158:161], v1 offset:1024
	ds_read_b128 v[162:165], v1 offset:2048
	ds_read_b128 v[166:169], v1 offset:3072
	ds_read_b128 v[170:173], v156
	ds_read_b128 v[174:177], v156 offset:1024
	ds_read_b128 v[178:181], v156 offset:2048
	ds_read_b128 v[182:185], v156 offset:3072
	ds_read_b128 v[186:189], v157
	ds_read_b128 v[190:193], v157 offset:1024
	ds_read_b128 v[194:197], v157 offset:2048
	ds_read_b128 v[198:201], v157 offset:3072
	ds_read_b128 v[202:205], v157 offset:4096
	ds_read_b128 v[206:209], v157 offset:5120
	ds_read_b128 v[210:213], v157 offset:6144
	ds_read_b128 v[214:217], v157 offset:7168
	s_waitcnt vmcnt(8)
	s_waitcnt lgkmcnt(0)
	s_barrier
	v_mfma_f32_16x16x32_bf16 v[126:129], v[142:145], v[186:189], v[126:129]
	v_mfma_f32_16x16x32_bf16 v[122:125], v[162:165], v[186:189], v[122:125]
	v_mfma_f32_16x16x32_bf16 v[114:117], v[142:145], v[194:197], v[114:117]
	v_mfma_f32_16x16x32_bf16 v[106:109], v[162:165], v[194:197], v[106:109]
	v_mfma_f32_16x16x32_bf16 v[98:101], v[142:145], v[202:205], v[98:101]
	v_mfma_f32_16x16x32_bf16 v[90:93], v[162:165], v[202:205], v[90:93]
	v_mfma_f32_16x16x32_bf16 v[82:85], v[142:145], v[210:213], v[82:85]
	v_mfma_f32_16x16x32_bf16 v[74:77], v[162:165], v[210:213], v[74:77]
	v_mfma_f32_16x16x32_bf16 v[126:129], v[158:161], v[190:193], v[126:129]
	v_mfma_f32_16x16x32_bf16 v[122:125], v[166:169], v[190:193], v[122:125]
	v_mfma_f32_16x16x32_bf16 v[114:117], v[158:161], v[198:201], v[114:117]
	v_mfma_f32_16x16x32_bf16 v[106:109], v[166:169], v[198:201], v[106:109]
	v_mfma_f32_16x16x32_bf16 v[98:101], v[158:161], v[206:209], v[98:101]
	v_mfma_f32_16x16x32_bf16 v[90:93], v[166:169], v[206:209], v[90:93]
	v_mfma_f32_16x16x32_bf16 v[82:85], v[158:161], v[214:217], v[82:85]
	v_mfma_f32_16x16x32_bf16 v[74:77], v[166:169], v[214:217], v[74:77]
	v_mfma_f32_16x16x32_bf16 v[118:121], v[170:173], v[186:189], v[118:121]
	v_mfma_f32_16x16x32_bf16 v[110:113], v[178:181], v[186:189], v[110:113]
	v_mfma_f32_16x16x32_bf16 v[102:105], v[170:173], v[194:197], v[102:105]
	v_mfma_f32_16x16x32_bf16 v[94:97], v[178:181], v[194:197], v[94:97]
	v_mfma_f32_16x16x32_bf16 v[86:89], v[170:173], v[202:205], v[86:89]
	v_mfma_f32_16x16x32_bf16 v[78:81], v[178:181], v[202:205], v[78:81]
	v_mfma_f32_16x16x32_bf16 v[62:65], v[170:173], v[210:213], v[62:65]
	v_mfma_f32_16x16x32_bf16 v[58:61], v[178:181], v[210:213], v[58:61]
	v_mfma_f32_16x16x32_bf16 v[118:121], v[174:177], v[190:193], v[118:121]
	v_mfma_f32_16x16x32_bf16 v[110:113], v[182:185], v[190:193], v[110:113]
	v_mfma_f32_16x16x32_bf16 v[102:105], v[174:177], v[198:201], v[102:105]
	v_mfma_f32_16x16x32_bf16 v[94:97], v[182:185], v[198:201], v[94:97]
	v_mfma_f32_16x16x32_bf16 v[86:89], v[174:177], v[206:209], v[86:89]
	v_mfma_f32_16x16x32_bf16 v[78:81], v[182:185], v[206:209], v[78:81]
	v_mfma_f32_16x16x32_bf16 v[62:65], v[174:177], v[214:217], v[62:65]
	v_mfma_f32_16x16x32_bf16 v[58:61], v[182:185], v[214:217], v[58:61]
	s_barrier
	s_add_i32 s88, s74, s62
	v_lshl_add_u64 v[218:219], s[58:59], 0, v[132:133]
	s_mov_b32 m0, s88
	s_nop 0
	global_load_lds_dwordx4 v[218:219], off
	s_add_i32 m0, s88, 0x2000
	s_add_u32 s88, s58, 0x20000
	v_lshl_add_u64 v[220:221], s[58:59], 0, v[136:137]
	s_addc_u32 s89, s59, 0
	s_add_i32 s90, s75, s62
	global_load_lds_dwordx4 v[220:221], off
	v_lshl_add_u64 v[222:223], s[88:89], 0, v[132:133]
	s_mov_b32 m0, s90
	v_lshl_add_u64 v[224:225], s[60:61], 0, v[134:135]
	global_load_lds_dwordx4 v[222:223], off
	v_lshl_add_u64 v[222:223], s[88:89], 0, v[136:137]
	s_add_i32 m0, s90, 0x2000
	s_nop 0
	global_load_lds_dwordx4 v[222:223], off
	v_lshl_add_u64 v[222:223], s[60:61], 0, v[130:131]
	s_mov_b32 m0, s55
	s_nop 0
	global_load_lds_dwordx4 v[222:223], off
	s_mov_b32 m0, s63
	s_nop 0
	global_load_lds_dwordx4 v[224:225], off
	ds_read_b128 v[186:189], v157 offset:16384
	ds_read_b128 v[190:193], v157 offset:17408
	ds_read_b128 v[194:197], v157 offset:18432
	ds_read_b128 v[198:201], v157 offset:19456
	ds_read_b128 v[202:205], v157 offset:20480
	ds_read_b128 v[206:209], v157 offset:21504
	ds_read_b128 v[210:213], v157 offset:22528
	ds_read_b128 v[214:217], v157 offset:23552
	s_waitcnt vmcnt(8)
	s_waitcnt lgkmcnt(0)
	s_barrier
; #define PG8_STAGE(bufoff, gbase, voff) do { _Pragma("unroll") for (int _i = 0; _i < 2; ++_i) \
;         __builtin_amdgcn_global_load_lds((const unsigned*)((const char*)(gbase) + (voff)[_i]), (PG8_LAS unsigned*)(lds + (bufoff) + ldsw + _i * 8192), 16, 0, 0); } while (0)
; #define PG8_LDA(dst, b, h) do { _Pragma("unroll") for (int m = 0; m < 4; ++m) _Pragma("unroll") for (int k = 0; k < 2; ++k) dst[m][k] = *(const PG8_LAS bf16x8*)(lds + PG8_SA(b, h) + aoff + m * 2048 + k * 1024); } while (0)
; #define PG8_LDB(dst, b, h) do { _Pragma("unroll") for (int n = 0; n < 2; ++n) _Pragma("unroll") for (int k = 0; k < 2; ++k) dst[n][k] = *(const PG8_LAS bf16x8*)(lds + PG8_SB(b, h) + boff + n * 2048 + k * 1024); } while (0)
; #define PG8_MMA(ai, bj, At, Bt) do { __builtin_amdgcn_s_setprio(1); _Pragma("unroll") for (int m = 0; m < 4; ++m) _Pragma("unroll") for (int n = 0; n < 2; ++n) _Pragma("unroll") for (int k = 0; k < 2; ++k) \
;         acc[ai][bj][m][n] = __builtin_amdgcn_mfma_f32_16x16x32_bf16(Bt[n][k], At[m][k], acc[ai][bj][m][n], 0, 0, 0); __builtin_amdgcn_s_setprio(0); } while (0)
; #define PG8_WAIT_V(n) asm volatile("s_waitcnt vmcnt(" #n ")" ::: "memory")
; #define PG8_WAIT_L(n) asm volatile("s_waitcnt lgkmcnt(" #n ")" ::: "memory")
; #define PG8_BAR __builtin_amdgcn_s_barrier()
; #define PG8_SCHED __builtin_amdgcn_sched_barrier(0)
; template <class Epi, class Sched, bool ALIGN_EPI = false>
; __device__ __forceinline__ void gemm_phase(PG8_LAS unsigned char* lds, const Gemm g, const Sched& S, const Epi& E) {
;     ...
;             PG8_WAIT_V(8); PG8_WAIT_L(0); PG8_BAR; PG8_MMA(1, 0, At, B0); PG8_MMA(1, 1, At, B1); PG8_BAR; PG8_SCHED;
;             PG8_LDB(B0, 1, 0); PG8_LDB(B1, 1, 1); PG8_SCHED; PG8_LDA(At, 1, 0); PG8_STAGE(PG8_SA(0, 1), a2 + hstepA, w1);
;             PG8_WAIT_V(8); PG8_WAIT_L(0); PG8_BAR; PG8_MMA(0, 0, At, B0); PG8_MMA(0, 1, At, B1); PG8_BAR; PG8_SCHED;
	v_mfma_f32_16x16x32_bf16 v[54:57], v[142:145], v[186:189], v[54:57]
	v_mfma_f32_16x16x32_bf16 v[42:45], v[162:165], v[186:189], v[42:45]
	v_mfma_f32_16x16x32_bf16 v[30:33], v[142:145], v[194:197], v[30:33]
	v_mfma_f32_16x16x32_bf16 v[26:29], v[162:165], v[194:197], v[26:29]
	v_mfma_f32_16x16x32_bf16 v[14:17], v[142:145], v[202:205], v[14:17]
	v_mfma_f32_16x16x32_bf16 v[10:13], v[162:165], v[202:205], v[10:13]
	v_mfma_f32_16x16x32_bf16 v[6:9], v[142:145], v[210:213], v[6:9]
	v_mfma_f32_16x16x32_bf16 v[2:5], v[162:165], v[210:213], v[2:5]
	v_mfma_f32_16x16x32_bf16 v[54:57], v[158:161], v[190:193], v[54:57]
	v_mfma_f32_16x16x32_bf16 v[42:45], v[166:169], v[190:193], v[42:45]
	v_mfma_f32_16x16x32_bf16 v[30:33], v[158:161], v[198:201], v[30:33]
	v_mfma_f32_16x16x32_bf16 v[26:29], v[166:169], v[198:201], v[26:29]
	v_mfma_f32_16x16x32_bf16 v[14:17], v[158:161], v[206:209], v[14:17]
	v_mfma_f32_16x16x32_bf16 v[10:13], v[166:169], v[206:209], v[10:13]
	v_mfma_f32_16x16x32_bf16 v[6:9], v[158:161], v[214:217], v[6:9]
	v_mfma_f32_16x16x32_bf16 v[2:5], v[166:169], v[214:217], v[2:5]
	v_mfma_f32_16x16x32_bf16 v[70:73], v[170:173], v[186:189], v[70:73]
	v_mfma_f32_16x16x32_bf16 v[66:69], v[178:181], v[186:189], v[66:69]
	v_mfma_f32_16x16x32_bf16 v[50:53], v[170:173], v[194:197], v[50:53]
	v_mfma_f32_16x16x32_bf16 v[46:49], v[178:181], v[194:197], v[46:49]
	v_mfma_f32_16x16x32_bf16 v[38:41], v[170:173], v[202:205], v[38:41]
	v_mfma_f32_16x16x32_bf16 v[34:37], v[178:181], v[202:205], v[34:37]
	v_mfma_f32_16x16x32_bf16 v[22:25], v[170:173], v[210:213], v[22:25]
	v_mfma_f32_16x16x32_bf16 v[18:21], v[178:181], v[210:213], v[18:21]
	v_mfma_f32_16x16x32_bf16 v[70:73], v[174:177], v[190:193], v[70:73]
	v_mfma_f32_16x16x32_bf16 v[66:69], v[182:185], v[190:193], v[66:69]
	v_mfma_f32_16x16x32_bf16 v[50:53], v[174:177], v[198:201], v[50:53]
	v_mfma_f32_16x16x32_bf16 v[46:49], v[182:185], v[198:201], v[46:49]
	v_mfma_f32_16x16x32_bf16 v[38:41], v[174:177], v[206:209], v[38:41]
	v_mfma_f32_16x16x32_bf16 v[34:37], v[182:185], v[206:209], v[34:37]
	v_mfma_f32_16x16x32_bf16 v[22:25], v[174:177], v[214:217], v[22:25]
	v_mfma_f32_16x16x32_bf16 v[18:21], v[182:185], v[214:217], v[18:21]
	s_barrier
	s_add_i32 s88, 0, 0x18000
	s_add_i32 s89, 0, 0x1c000
	s_add_u32 s60, s60, 0x20000
	s_addc_u32 s61, s61, 0
	s_mov_b32 m0, s64
	v_lshl_add_u64 v[226:227], s[60:61], 0, v[130:131]
	global_load_lds_dwordx4 v[226:227], off
	v_lshl_add_u64 v[226:227], s[60:61], 0, v[134:135]
	s_mov_b32 m0, s65
	s_nop 0
	global_load_lds_dwordx4 v[226:227], off
	v_add_u32_e32 v166, s88, v147
	v_add_u32_e32 v182, s89, v147
	ds_read_b128 v[142:145], v166
	ds_read_b128 v[158:161], v166 offset:1024
	ds_read_b128 v[162:165], v166 offset:2048
	ds_read_b128 v[166:169], v166 offset:3072
	ds_read_b128 v[170:173], v182
	ds_read_b128 v[174:177], v182 offset:1024
	ds_read_b128 v[178:181], v182 offset:2048
	ds_read_b128 v[182:185], v182 offset:3072
	ds_read_b128 v[186:189], v157 offset:32768
	ds_read_b128 v[190:193], v157 offset:33792
	ds_read_b128 v[194:197], v157 offset:34816
	ds_read_b128 v[198:201], v157 offset:35840
	ds_read_b128 v[202:205], v157 offset:36864
	ds_read_b128 v[206:209], v157 offset:37888
	ds_read_b128 v[210:213], v157 offset:38912
	ds_read_b128 v[214:217], v157 offset:39936
	s_waitcnt vmcnt(8)
	s_waitcnt lgkmcnt(0)
	s_barrier
	v_mfma_f32_16x16x32_bf16 v[126:129], v[142:145], v[186:189], v[126:129]
	v_mfma_f32_16x16x32_bf16 v[122:125], v[162:165], v[186:189], v[122:125]
	v_mfma_f32_16x16x32_bf16 v[114:117], v[142:145], v[194:197], v[114:117]
	v_mfma_f32_16x16x32_bf16 v[106:109], v[162:165], v[194:197], v[106:109]
	v_mfma_f32_16x16x32_bf16 v[98:101], v[142:145], v[202:205], v[98:101]
	v_mfma_f32_16x16x32_bf16 v[90:93], v[162:165], v[202:205], v[90:93]
	v_mfma_f32_16x16x32_bf16 v[82:85], v[142:145], v[210:213], v[82:85]
	v_mfma_f32_16x16x32_bf16 v[74:77], v[162:165], v[210:213], v[74:77]
	v_mfma_f32_16x16x32_bf16 v[126:129], v[158:161], v[190:193], v[126:129]
	v_mfma_f32_16x16x32_bf16 v[122:125], v[166:169], v[190:193], v[122:125]
	v_mfma_f32_16x16x32_bf16 v[114:117], v[158:161], v[198:201], v[114:117]
	v_mfma_f32_16x16x32_bf16 v[106:109], v[166:169], v[198:201], v[106:109]
	v_mfma_f32_16x16x32_bf16 v[98:101], v[158:161], v[206:209], v[98:101]
	v_mfma_f32_16x16x32_bf16 v[90:93], v[166:169], v[206:209], v[90:93]
	v_mfma_f32_16x16x32_bf16 v[82:85], v[158:161], v[214:217], v[82:85]
	v_mfma_f32_16x16x32_bf16 v[74:77], v[166:169], v[214:217], v[74:77]
	v_mfma_f32_16x16x32_bf16 v[118:121], v[170:173], v[186:189], v[118:121]
	v_mfma_f32_16x16x32_bf16 v[110:113], v[178:181], v[186:189], v[110:113]
	v_mfma_f32_16x16x32_bf16 v[102:105], v[170:173], v[194:197], v[102:105]
	v_mfma_f32_16x16x32_bf16 v[94:97], v[178:181], v[194:197], v[94:97]
	v_mfma_f32_16x16x32_bf16 v[86:89], v[170:173], v[202:205], v[86:89]
	v_mfma_f32_16x16x32_bf16 v[78:81], v[178:181], v[202:205], v[78:81]
	v_mfma_f32_16x16x32_bf16 v[62:65], v[170:173], v[210:213], v[62:65]
	v_mfma_f32_16x16x32_bf16 v[58:61], v[178:181], v[210:213], v[58:61]
	v_mfma_f32_16x16x32_bf16 v[118:121], v[174:177], v[190:193], v[118:121]
	v_mfma_f32_16x16x32_bf16 v[110:113], v[182:185], v[190:193], v[110:113]
	v_mfma_f32_16x16x32_bf16 v[102:105], v[174:177], v[198:201], v[102:105]
	v_mfma_f32_16x16x32_bf16 v[94:97], v[182:185], v[198:201], v[94:97]
	v_mfma_f32_16x16x32_bf16 v[86:89], v[174:177], v[206:209], v[86:89]
	v_mfma_f32_16x16x32_bf16 v[78:81], v[182:185], v[206:209], v[78:81]
	v_mfma_f32_16x16x32_bf16 v[62:65], v[174:177], v[214:217], v[62:65]
	v_mfma_f32_16x16x32_bf16 v[58:61], v[182:185], v[214:217], v[58:61]
	s_barrier
; #define PG8_STAGE(bufoff, gbase, voff) do { _Pragma("unroll") for (int _i = 0; _i < 2; ++_i) \
;         __builtin_amdgcn_global_load_lds((const unsigned*)((const char*)(gbase) + (voff)[_i]), (PG8_LAS unsigned*)(lds + (bufoff) + ldsw + _i * 8192), 16, 0, 0); } while (0)
; #define PG8_LDA(dst, b, h) do { _Pragma("unroll") for (int m = 0; m < 4; ++m) _Pragma("unroll") for (int k = 0; k < 2; ++k) dst[m][k] = *(const PG8_LAS bf16x8*)(lds + PG8_SA(b, h) + aoff + m * 2048 + k * 1024); } while (0)
; #define PG8_MMA(ai, bj, At, Bt) do { __builtin_amdgcn_s_setprio(1); _Pragma("unroll") for (int m = 0; m < 4; ++m) _Pragma("unroll") for (int n = 0; n < 2; ++n) _Pragma("unroll") for (int k = 0; k < 2; ++k) \
;         acc[ai][bj][m][n] = __builtin_amdgcn_mfma_f32_16x16x32_bf16(Bt[n][k], At[m][k], acc[ai][bj][m][n], 0, 0, 0); __builtin_amdgcn_s_setprio(0); } while (0)
; #define PG8_WAIT_V(n) asm volatile("s_waitcnt vmcnt(" #n ")" ::: "memory")
; #define PG8_WAIT_L(n) asm volatile("s_waitcnt lgkmcnt(" #n ")" ::: "memory")
; #define PG8_BAR __builtin_amdgcn_s_barrier()
; #define PG8_SCHED __builtin_amdgcn_sched_barrier(0)
; template <class Epi, class Sched, bool ALIGN_EPI = false>
; __device__ __forceinline__ void gemm_phase(PG8_LAS unsigned char* lds, const Gemm g, const Sched& S, const Epi& E) {
;     ...
;             PG8_LDA(At, 1, 1); PG8_STAGE(PG8_SB(1, 0), b3, voffB); PG8_STAGE(PG8_SB(1, 1), b3 + hstep, voffB); PG8_STAGE(PG8_SA(1, 0), a3, w0);
;             PG8_WAIT_V(8); PG8_WAIT_L(0); PG8_BAR; PG8_MMA(1, 0, At, B0); PG8_MMA(1, 1, At, B1); PG8_BAR; PG8_SCHED;
;             if constexpr (Epi::KSCALE) { if (((t + 2) & 7) == 0 && t + 2 < nt) { E.kscale(acc, pf, ((t + 2) >> 3) - 1, wr, fr); PG8_SCHED; } }
;         }
;         if constexpr (ALIGN_EPI) { if (wr == 0) PG8_BAR; }
	s_add_i32 s60, s88, s62
	v_lshl_add_u64 v[218:219], v[218:219], 0, s[16:17]
	s_mov_b32 m0, s60
	s_nop 0
	global_load_lds_dwordx4 v[218:219], off
	s_add_i32 m0, s60, 0x2000
	s_add_u32 s58, s58, 0x20080
	v_lshl_add_u64 v[218:219], v[220:221], 0, s[16:17]
	s_addc_u32 s59, s59, 0
	s_add_i32 s60, s89, s62
	global_load_lds_dwordx4 v[218:219], off
	v_lshl_add_u64 v[218:219], s[58:59], 0, v[132:133]
	s_mov_b32 m0, s60
	s_nop 0
	global_load_lds_dwordx4 v[218:219], off
	v_lshl_add_u64 v[218:219], s[58:59], 0, v[136:137]
	s_add_i32 m0, s60, 0x2000
	s_nop 0
	global_load_lds_dwordx4 v[218:219], off
	v_lshl_add_u64 v[218:219], v[222:223], 0, s[16:17]
	s_mov_b32 m0, s67
	s_nop 0
	global_load_lds_dwordx4 v[218:219], off
	v_lshl_add_u64 v[218:219], v[224:225], 0, s[16:17]
	s_mov_b32 m0, s68
	s_nop 0
	global_load_lds_dwordx4 v[218:219], off
	ds_read_b128 v[186:189], v157 offset:49152
	ds_read_b128 v[190:193], v157 offset:50176
	ds_read_b128 v[194:197], v157 offset:51200
	ds_read_b128 v[198:201], v157 offset:52224
	ds_read_b128 v[202:205], v157 offset:53248
	ds_read_b128 v[206:209], v157 offset:54272
	ds_read_b128 v[210:213], v157 offset:55296
	ds_read_b128 v[214:217], v157 offset:56320
	s_waitcnt vmcnt(8)
	s_waitcnt lgkmcnt(0)
	s_barrier
	v_mfma_f32_16x16x32_bf16 v[54:57], v[142:145], v[186:189], v[54:57]
	v_mfma_f32_16x16x32_bf16 v[42:45], v[162:165], v[186:189], v[42:45]
	v_mfma_f32_16x16x32_bf16 v[30:33], v[142:145], v[194:197], v[30:33]
	v_mfma_f32_16x16x32_bf16 v[26:29], v[162:165], v[194:197], v[26:29]
	v_mfma_f32_16x16x32_bf16 v[14:17], v[142:145], v[202:205], v[14:17]
	v_mfma_f32_16x16x32_bf16 v[10:13], v[162:165], v[202:205], v[10:13]
	v_mfma_f32_16x16x32_bf16 v[6:9], v[142:145], v[210:213], v[6:9]
	v_mfma_f32_16x16x32_bf16 v[2:5], v[162:165], v[210:213], v[2:5]
	v_mfma_f32_16x16x32_bf16 v[54:57], v[158:161], v[190:193], v[54:57]
	v_mfma_f32_16x16x32_bf16 v[42:45], v[166:169], v[190:193], v[42:45]
	v_mfma_f32_16x16x32_bf16 v[30:33], v[158:161], v[198:201], v[30:33]
	v_mfma_f32_16x16x32_bf16 v[26:29], v[166:169], v[198:201], v[26:29]
	v_mfma_f32_16x16x32_bf16 v[14:17], v[158:161], v[206:209], v[14:17]
	v_mfma_f32_16x16x32_bf16 v[10:13], v[166:169], v[206:209], v[10:13]
	v_mfma_f32_16x16x32_bf16 v[6:9], v[158:161], v[214:217], v[6:9]
	v_mfma_f32_16x16x32_bf16 v[2:5], v[166:169], v[214:217], v[2:5]
	v_mfma_f32_16x16x32_bf16 v[70:73], v[170:173], v[186:189], v[70:73]
	v_mfma_f32_16x16x32_bf16 v[66:69], v[178:181], v[186:189], v[66:69]
	v_mfma_f32_16x16x32_bf16 v[50:53], v[170:173], v[194:197], v[50:53]
	v_mfma_f32_16x16x32_bf16 v[46:49], v[178:181], v[194:197], v[46:49]
	v_mfma_f32_16x16x32_bf16 v[38:41], v[170:173], v[202:205], v[38:41]
	v_mfma_f32_16x16x32_bf16 v[34:37], v[178:181], v[202:205], v[34:37]
	v_mfma_f32_16x16x32_bf16 v[22:25], v[170:173], v[210:213], v[22:25]
	v_mfma_f32_16x16x32_bf16 v[18:21], v[178:181], v[210:213], v[18:21]
	v_mfma_f32_16x16x32_bf16 v[70:73], v[174:177], v[190:193], v[70:73]
	v_mfma_f32_16x16x32_bf16 v[66:69], v[182:185], v[190:193], v[66:69]
	v_mfma_f32_16x16x32_bf16 v[50:53], v[174:177], v[198:201], v[50:53]
	v_mfma_f32_16x16x32_bf16 v[46:49], v[182:185], v[198:201], v[46:49]
	v_mfma_f32_16x16x32_bf16 v[38:41], v[174:177], v[206:209], v[38:41]
	v_mfma_f32_16x16x32_bf16 v[34:37], v[182:185], v[206:209], v[34:37]
	v_mfma_f32_16x16x32_bf16 v[22:25], v[174:177], v[214:217], v[22:25]
	v_mfma_f32_16x16x32_bf16 v[18:21], v[182:185], v[214:217], v[18:21]
	s_barrier
	s_add_i32 s87, s87, 2
	s_add_u32 s85, s85, 0x100
	s_addc_u32 s86, s86, 0
	s_add_u32 s56, s56, 0x100
	s_addc_u32 s57, s57, 0
	s_cmp_gt_u32 s87, 5
	s_cbranch_scc0 .LBB0_1498
	s_and_b64 vcc, exec, s[18:19]
	s_cbranch_vccz .LBB0_1501
	s_barrier

; #define PG8_STAGE(bufoff, gbase, voff) do { _Pragma("unroll") for (int _i = 0; _i < 2; ++_i) \
;         __builtin_amdgcn_global_load_lds((const unsigned*)((const char*)(gbase) + (voff)[_i]), (PG8_LAS unsigned*)(lds + (bufoff) + ldsw + _i * 8192), 16, 0, 0); } while (0)
; #define PG8_LDA(dst, b, h) do { _Pragma("unroll") for (int m = 0; m < 4; ++m) _Pragma("unroll") for (int k = 0; k < 2; ++k) dst[m][k] = *(const PG8_LAS bf16x8*)(lds + PG8_SA(b, h) + aoff + m * 2048 + k * 1024); } while (0)
; #define PG8_LDB(dst, b, h) do { _Pragma("unroll") for (int n = 0; n < 2; ++n) _Pragma("unroll") for (int k = 0; k < 2; ++k) dst[n][k] = *(const PG8_LAS bf16x8*)(lds + PG8_SB(b, h) + boff + n * 2048 + k * 1024); } while (0)
; #define PG8_MMA(ai, bj, At, Bt) do { __builtin_amdgcn_s_setprio(1); _Pragma("unroll") for (int m = 0; m < 4; ++m) _Pragma("unroll") for (int n = 0; n < 2; ++n) _Pragma("unroll") for (int k = 0; k < 2; ++k) \
;         acc[ai][bj][m][n] = __builtin_amdgcn_mfma_f32_16x16x32_bf16(Bt[n][k], At[m][k], acc[ai][bj][m][n], 0, 0, 0); __builtin_amdgcn_s_setprio(0); } while (0)
; #define PG8_WAIT_V(n) asm volatile("s_waitcnt vmcnt(" #n ")" ::: "memory")
; #define PG8_WAIT_L(n) asm volatile("s_waitcnt lgkmcnt(" #n ")" ::: "memory")
; template <class Epi, class Sched, bool ALIGN_EPI = false>
; __device__ __forceinline__ void gemm_phase(PG8_LAS unsigned char* lds, const Gemm g, const Sched& S, const Epi& E) {
;     ...
;             const bool last = (t == nt - 2);
;             const char* a1 = cA + (size_t)(t + 1) * kstep;
;             const char* a2 = last ? nA : cA + (size_t)(t + 2) * kstep; const char* b2 = last ? nB : cB + (size_t)(t + 2) * kstep;
;             const char* a3 = a2 + kstep; const char* b3 = b2 + kstep;
;             unsigned w0[2], w1[2];
; #pragma unroll
;             for (int i = 0; i < 2; ++i) { w0[i] = (Sched::GATHER && last) ? vn0[i] : vc0[i]; w1[i] = (Sched::GATHER && last) ? vn1[i] : vc1[i]; }
;             if (last && has_next) S.a_ready(nxt);
;             PG8_LDB(B0, 0, 0); PG8_LDB(B1, 0, 1); PG8_SCHED; PG8_LDA(At, 0, 0); PG8_STAGE(PG8_SA(1, 1), a1 + hstepA, vc1);
;             PG8_WAIT_V(8); PG8_WAIT_L(0); PG8_BAR; PG8_MMA(0, 0, At, B0); PG8_MMA(0, 1, At, B1); PG8_BAR; PG8_SCHED;
;             PG8_LDA(At, 0, 1); PG8_STAGE(PG8_SB(0, 0), b2, voffB); PG8_STAGE(PG8_SB(0, 1), b2 + hstep, voffB); PG8_STAGE(PG8_SA(0, 0), a2, w0);
.LBB0_1601:
	s_add_u32 s54, s52, 0xfffe0080
	s_addc_u32 s55, s53, -1
	s_cmp_eq_u32 s87, 4
	s_cselect_b32 s57, s25, s55
	s_cselect_b32 s56, s43, s54
	s_cselect_b32 s55, s27, s86
	s_cselect_b32 s54, s84, s85
	v_lshl_add_u64 v[220:221], s[52:53], 0, v[142:143]
	s_add_i32 m0, s45, 0xc000
	s_nop 0
	global_load_lds_dwordx4 v[220:221], off
	v_lshl_add_u64 v[220:221], s[52:53], 0, v[140:141]
	s_add_i32 m0, s45, 0xe000
	s_nop 0
	global_load_lds_dwordx4 v[220:221], off
	ds_read_b128 v[144:147], v157
	ds_read_b128 v[160:163], v157 offset:1024
	ds_read_b128 v[164:167], v157 offset:2048
	ds_read_b128 v[168:171], v157 offset:3072
	ds_read_b128 v[172:175], v158
	ds_read_b128 v[176:179], v158 offset:1024
	ds_read_b128 v[180:183], v158 offset:2048
	ds_read_b128 v[184:187], v158 offset:3072
	ds_read_b128 v[188:191], v159
	ds_read_b128 v[192:195], v159 offset:1024
	ds_read_b128 v[196:199], v159 offset:2048
	ds_read_b128 v[200:203], v159 offset:3072
	ds_read_b128 v[204:207], v159 offset:4096
	ds_read_b128 v[208:211], v159 offset:5120
	ds_read_b128 v[212:215], v159 offset:6144
	ds_read_b128 v[216:219], v159 offset:7168
	s_waitcnt vmcnt(8)
	s_waitcnt lgkmcnt(0)
	s_barrier
	v_mfma_f32_16x16x32_bf16 v[126:129], v[144:147], v[188:191], v[126:129]
	v_mfma_f32_16x16x32_bf16 v[122:125], v[164:167], v[188:191], v[122:125]
	v_mfma_f32_16x16x32_bf16 v[114:117], v[144:147], v[196:199], v[114:117]
	v_mfma_f32_16x16x32_bf16 v[106:109], v[164:167], v[196:199], v[106:109]
	v_mfma_f32_16x16x32_bf16 v[98:101], v[144:147], v[204:207], v[98:101]
	v_mfma_f32_16x16x32_bf16 v[90:93], v[164:167], v[204:207], v[90:93]
	v_mfma_f32_16x16x32_bf16 v[82:85], v[144:147], v[212:215], v[82:85]
	v_mfma_f32_16x16x32_bf16 v[74:77], v[164:167], v[212:215], v[74:77]
	v_mfma_f32_16x16x32_bf16 v[126:129], v[160:163], v[192:195], v[126:129]
	v_mfma_f32_16x16x32_bf16 v[122:125], v[168:171], v[192:195], v[122:125]
	v_mfma_f32_16x16x32_bf16 v[114:117], v[160:163], v[200:203], v[114:117]
	v_mfma_f32_16x16x32_bf16 v[106:109], v[168:171], v[200:203], v[106:109]
	v_mfma_f32_16x16x32_bf16 v[98:101], v[160:163], v[208:211], v[98:101]
	v_mfma_f32_16x16x32_bf16 v[90:93], v[168:171], v[208:211], v[90:93]
	v_mfma_f32_16x16x32_bf16 v[82:85], v[160:163], v[216:219], v[82:85]
	v_mfma_f32_16x16x32_bf16 v[74:77], v[168:171], v[216:219], v[74:77]
	v_mfma_f32_16x16x32_bf16 v[118:121], v[172:175], v[188:191], v[118:121]
	v_mfma_f32_16x16x32_bf16 v[110:113], v[180:183], v[188:191], v[110:113]
	v_mfma_f32_16x16x32_bf16 v[102:105], v[172:175], v[196:199], v[102:105]
	v_mfma_f32_16x16x32_bf16 v[94:97], v[180:183], v[196:199], v[94:97]
	v_mfma_f32_16x16x32_bf16 v[86:89], v[172:175], v[204:207], v[86:89]
	v_mfma_f32_16x16x32_bf16 v[78:81], v[180:183], v[204:207], v[78:81]
	v_mfma_f32_16x16x32_bf16 v[62:65], v[172:175], v[212:215], v[62:65]
	v_mfma_f32_16x16x32_bf16 v[58:61], v[180:183], v[212:215], v[58:61]
	v_mfma_f32_16x16x32_bf16 v[118:121], v[176:179], v[192:195], v[118:121]
	v_mfma_f32_16x16x32_bf16 v[110:113], v[184:187], v[192:195], v[110:113]
	v_mfma_f32_16x16x32_bf16 v[102:105], v[176:179], v[200:203], v[102:105]
	v_mfma_f32_16x16x32_bf16 v[94:97], v[184:187], v[200:203], v[94:97]
	v_mfma_f32_16x16x32_bf16 v[86:89], v[176:179], v[208:211], v[86:89]
	v_mfma_f32_16x16x32_bf16 v[78:81], v[184:187], v[208:211], v[78:81]
	v_mfma_f32_16x16x32_bf16 v[62:65], v[176:179], v[216:219], v[62:65]
	v_mfma_f32_16x16x32_bf16 v[58:61], v[184:187], v[216:219], v[58:61]
	s_barrier
	s_add_i32 s88, s74, s62
	v_lshl_add_u64 v[220:221], s[54:55], 0, v[134:135]
	s_mov_b32 m0, s88
	s_nop 0
	global_load_lds_dwordx4 v[220:221], off
	s_add_i32 m0, s88, 0x2000
	s_add_u32 s88, s54, 0x20000
	v_lshl_add_u64 v[222:223], s[54:55], 0, v[138:139]
	s_addc_u32 s89, s55, 0
	s_add_i32 s90, s75, s62
	global_load_lds_dwordx4 v[222:223], off
	v_lshl_add_u64 v[224:225], s[88:89], 0, v[134:135]
	s_mov_b32 m0, s90
	v_lshl_add_u64 v[226:227], s[56:57], 0, v[136:137]
	global_load_lds_dwordx4 v[224:225], off
	v_lshl_add_u64 v[224:225], s[88:89], 0, v[138:139]
	s_add_i32 m0, s90, 0x2000
	s_nop 0
	global_load_lds_dwordx4 v[224:225], off
	v_lshl_add_u64 v[224:225], s[56:57], 0, v[132:133]
	s_mov_b32 m0, s45
	s_nop 0
	global_load_lds_dwordx4 v[224:225], off
	s_mov_b32 m0, s63
	s_nop 0
	global_load_lds_dwordx4 v[226:227], off
	ds_read_b128 v[188:191], v159 offset:16384
	ds_read_b128 v[192:195], v159 offset:17408
	ds_read_b128 v[196:199], v159 offset:18432
	ds_read_b128 v[200:203], v159 offset:19456
	ds_read_b128 v[204:207], v159 offset:20480
	ds_read_b128 v[208:211], v159 offset:21504
	ds_read_b128 v[212:215], v159 offset:22528
	ds_read_b128 v[216:219], v159 offset:23552
	s_waitcnt vmcnt(8)
	s_waitcnt lgkmcnt(0)
	s_barrier
; #define PG8_STAGE(bufoff, gbase, voff) do { _Pragma("unroll") for (int _i = 0; _i < 2; ++_i) \
;         __builtin_amdgcn_global_load_lds((const unsigned*)((const char*)(gbase) + (voff)[_i]), (PG8_LAS unsigned*)(lds + (bufoff) + ldsw + _i * 8192), 16, 0, 0); } while (0)
; #define PG8_LDA(dst, b, h) do { _Pragma("unroll") for (int m = 0; m < 4; ++m) _Pragma("unroll") for (int k = 0; k < 2; ++k) dst[m][k] = *(const PG8_LAS bf16x8*)(lds + PG8_SA(b, h) + aoff + m * 2048 + k * 1024); } while (0)
; #define PG8_LDB(dst, b, h) do { _Pragma("unroll") for (int n = 0; n < 2; ++n) _Pragma("unroll") for (int k = 0; k < 2; ++k) dst[n][k] = *(const PG8_LAS bf16x8*)(lds + PG8_SB(b, h) + boff + n * 2048 + k * 1024); } while (0)
; #define PG8_MMA(ai, bj, At, Bt) do { __builtin_amdgcn_s_setprio(1); _Pragma("unroll") for (int m = 0; m < 4; ++m) _Pragma("unroll") for (int n = 0; n < 2; ++n) _Pragma("unroll") for (int k = 0; k < 2; ++k) \
;         acc[ai][bj][m][n] = __builtin_amdgcn_mfma_f32_16x16x32_bf16(Bt[n][k], At[m][k], acc[ai][bj][m][n], 0, 0, 0); __builtin_amdgcn_s_setprio(0); } while (0)
; #define PG8_WAIT_V(n) asm volatile("s_waitcnt vmcnt(" #n ")" ::: "memory")
; #define PG8_WAIT_L(n) asm volatile("s_waitcnt lgkmcnt(" #n ")" ::: "memory")
; #define PG8_BAR __builtin_amdgcn_s_barrier()
; #define PG8_SCHED __builtin_amdgcn_sched_barrier(0)
; template <class Epi, class Sched, bool ALIGN_EPI = false>
; __device__ __forceinline__ void gemm_phase(PG8_LAS unsigned char* lds, const Gemm g, const Sched& S, const Epi& E) {
;     ...
;             PG8_WAIT_V(8); PG8_WAIT_L(0); PG8_BAR; PG8_MMA(1, 0, At, B0); PG8_MMA(1, 1, At, B1); PG8_BAR; PG8_SCHED;
;             PG8_LDB(B0, 1, 0); PG8_LDB(B1, 1, 1); PG8_SCHED; PG8_LDA(At, 1, 0); PG8_STAGE(PG8_SA(0, 1), a2 + hstepA, w1);
;             PG8_WAIT_V(8); PG8_WAIT_L(0); PG8_BAR; PG8_MMA(0, 0, At, B0); PG8_MMA(0, 1, At, B1); PG8_BAR; PG8_SCHED;
	v_mfma_f32_16x16x32_bf16 v[54:57], v[144:147], v[188:191], v[54:57]
	v_mfma_f32_16x16x32_bf16 v[42:45], v[164:167], v[188:191], v[42:45]
	v_mfma_f32_16x16x32_bf16 v[30:33], v[144:147], v[196:199], v[30:33]
	v_mfma_f32_16x16x32_bf16 v[26:29], v[164:167], v[196:199], v[26:29]
	v_mfma_f32_16x16x32_bf16 v[14:17], v[144:147], v[204:207], v[14:17]
	v_mfma_f32_16x16x32_bf16 v[10:13], v[164:167], v[204:207], v[10:13]
	v_mfma_f32_16x16x32_bf16 v[6:9], v[144:147], v[212:215], v[6:9]
	v_mfma_f32_16x16x32_bf16 v[2:5], v[164:167], v[212:215], v[2:5]
	v_mfma_f32_16x16x32_bf16 v[54:57], v[160:163], v[192:195], v[54:57]
	v_mfma_f32_16x16x32_bf16 v[42:45], v[168:171], v[192:195], v[42:45]
	v_mfma_f32_16x16x32_bf16 v[30:33], v[160:163], v[200:203], v[30:33]
	v_mfma_f32_16x16x32_bf16 v[26:29], v[168:171], v[200:203], v[26:29]
	v_mfma_f32_16x16x32_bf16 v[14:17], v[160:163], v[208:211], v[14:17]
	v_mfma_f32_16x16x32_bf16 v[10:13], v[168:171], v[208:211], v[10:13]
	v_mfma_f32_16x16x32_bf16 v[6:9], v[160:163], v[216:219], v[6:9]
	v_mfma_f32_16x16x32_bf16 v[2:5], v[168:171], v[216:219], v[2:5]
	v_mfma_f32_16x16x32_bf16 v[70:73], v[172:175], v[188:191], v[70:73]
	v_mfma_f32_16x16x32_bf16 v[66:69], v[180:183], v[188:191], v[66:69]
	v_mfma_f32_16x16x32_bf16 v[50:53], v[172:175], v[196:199], v[50:53]
	v_mfma_f32_16x16x32_bf16 v[46:49], v[180:183], v[196:199], v[46:49]
	v_mfma_f32_16x16x32_bf16 v[38:41], v[172:175], v[204:207], v[38:41]
	v_mfma_f32_16x16x32_bf16 v[34:37], v[180:183], v[204:207], v[34:37]
	v_mfma_f32_16x16x32_bf16 v[22:25], v[172:175], v[212:215], v[22:25]
	v_mfma_f32_16x16x32_bf16 v[18:21], v[180:183], v[212:215], v[18:21]
	v_mfma_f32_16x16x32_bf16 v[70:73], v[176:179], v[192:195], v[70:73]
	v_mfma_f32_16x16x32_bf16 v[66:69], v[184:187], v[192:195], v[66:69]
	v_mfma_f32_16x16x32_bf16 v[50:53], v[176:179], v[200:203], v[50:53]
	v_mfma_f32_16x16x32_bf16 v[46:49], v[184:187], v[200:203], v[46:49]
	v_mfma_f32_16x16x32_bf16 v[38:41], v[176:179], v[208:211], v[38:41]
	v_mfma_f32_16x16x32_bf16 v[34:37], v[184:187], v[208:211], v[34:37]
	v_mfma_f32_16x16x32_bf16 v[22:25], v[176:179], v[216:219], v[22:25]
	v_mfma_f32_16x16x32_bf16 v[18:21], v[184:187], v[216:219], v[18:21]
	s_barrier
	s_add_i32 s88, 0, 0x18000
	s_add_i32 s89, 0, 0x1c000
	s_add_u32 s56, s56, 0x20000
	s_addc_u32 s57, s57, 0
	s_mov_b32 m0, s64
	v_lshl_add_u64 v[228:229], s[56:57], 0, v[132:133]
	global_load_lds_dwordx4 v[228:229], off
	v_lshl_add_u64 v[228:229], s[56:57], 0, v[136:137]
	s_mov_b32 m0, s65
	s_nop 0
	global_load_lds_dwordx4 v[228:229], off
	v_add_u32_e32 v168, s88, v148
	v_add_u32_e32 v184, s89, v148
	ds_read_b128 v[144:147], v168
	ds_read_b128 v[160:163], v168 offset:1024
	ds_read_b128 v[164:167], v168 offset:2048
	ds_read_b128 v[168:171], v168 offset:3072
	ds_read_b128 v[172:175], v184
	ds_read_b128 v[176:179], v184 offset:1024
	ds_read_b128 v[180:183], v184 offset:2048
	ds_read_b128 v[184:187], v184 offset:3072
	ds_read_b128 v[188:191], v159 offset:32768
	ds_read_b128 v[192:195], v159 offset:33792
	ds_read_b128 v[196:199], v159 offset:34816
	ds_read_b128 v[200:203], v159 offset:35840
	ds_read_b128 v[204:207], v159 offset:36864
	ds_read_b128 v[208:211], v159 offset:37888
	ds_read_b128 v[212:215], v159 offset:38912
	ds_read_b128 v[216:219], v159 offset:39936
	s_waitcnt vmcnt(8)
	s_waitcnt lgkmcnt(0)
	s_barrier
	v_mfma_f32_16x16x32_bf16 v[126:129], v[144:147], v[188:191], v[126:129]
	v_mfma_f32_16x16x32_bf16 v[122:125], v[164:167], v[188:191], v[122:125]
	v_mfma_f32_16x16x32_bf16 v[114:117], v[144:147], v[196:199], v[114:117]
	v_mfma_f32_16x16x32_bf16 v[106:109], v[164:167], v[196:199], v[106:109]
	v_mfma_f32_16x16x32_bf16 v[98:101], v[144:147], v[204:207], v[98:101]
	v_mfma_f32_16x16x32_bf16 v[90:93], v[164:167], v[204:207], v[90:93]
	v_mfma_f32_16x16x32_bf16 v[82:85], v[144:147], v[212:215], v[82:85]
	v_mfma_f32_16x16x32_bf16 v[74:77], v[164:167], v[212:215], v[74:77]
	v_mfma_f32_16x16x32_bf16 v[126:129], v[160:163], v[192:195], v[126:129]
	v_mfma_f32_16x16x32_bf16 v[122:125], v[168:171], v[192:195], v[122:125]
	v_mfma_f32_16x16x32_bf16 v[114:117], v[160:163], v[200:203], v[114:117]
	v_mfma_f32_16x16x32_bf16 v[106:109], v[168:171], v[200:203], v[106:109]
	v_mfma_f32_16x16x32_bf16 v[98:101], v[160:163], v[208:211], v[98:101]
	v_mfma_f32_16x16x32_bf16 v[90:93], v[168:171], v[208:211], v[90:93]
	v_mfma_f32_16x16x32_bf16 v[82:85], v[160:163], v[216:219], v[82:85]
	v_mfma_f32_16x16x32_bf16 v[74:77], v[168:171], v[216:219], v[74:77]
	v_mfma_f32_16x16x32_bf16 v[118:121], v[172:175], v[188:191], v[118:121]
	v_mfma_f32_16x16x32_bf16 v[110:113], v[180:183], v[188:191], v[110:113]
	v_mfma_f32_16x16x32_bf16 v[102:105], v[172:175], v[196:199], v[102:105]
	v_mfma_f32_16x16x32_bf16 v[94:97], v[180:183], v[196:199], v[94:97]
	v_mfma_f32_16x16x32_bf16 v[86:89], v[172:175], v[204:207], v[86:89]
	v_mfma_f32_16x16x32_bf16 v[78:81], v[180:183], v[204:207], v[78:81]
	v_mfma_f32_16x16x32_bf16 v[62:65], v[172:175], v[212:215], v[62:65]
	v_mfma_f32_16x16x32_bf16 v[58:61], v[180:183], v[212:215], v[58:61]
	v_mfma_f32_16x16x32_bf16 v[118:121], v[176:179], v[192:195], v[118:121]
	v_mfma_f32_16x16x32_bf16 v[110:113], v[184:187], v[192:195], v[110:113]
	v_mfma_f32_16x16x32_bf16 v[102:105], v[176:179], v[200:203], v[102:105]
	v_mfma_f32_16x16x32_bf16 v[94:97], v[184:187], v[200:203], v[94:97]
	v_mfma_f32_16x16x32_bf16 v[86:89], v[176:179], v[208:211], v[86:89]
	v_mfma_f32_16x16x32_bf16 v[78:81], v[184:187], v[208:211], v[78:81]
	v_mfma_f32_16x16x32_bf16 v[62:65], v[176:179], v[216:219], v[62:65]
	v_mfma_f32_16x16x32_bf16 v[58:61], v[184:187], v[216:219], v[58:61]
	s_barrier
; #define PG8_STAGE(bufoff, gbase, voff) do { _Pragma("unroll") for (int _i = 0; _i < 2; ++_i) \
;         __builtin_amdgcn_global_load_lds((const unsigned*)((const char*)(gbase) + (voff)[_i]), (PG8_LAS unsigned*)(lds + (bufoff) + ldsw + _i * 8192), 16, 0, 0); } while (0)
; #define PG8_LDA(dst, b, h) do { _Pragma("unroll") for (int m = 0; m < 4; ++m) _Pragma("unroll") for (int k = 0; k < 2; ++k) dst[m][k] = *(const PG8_LAS bf16x8*)(lds + PG8_SA(b, h) + aoff + m * 2048 + k * 1024); } while (0)
; #define PG8_MMA(ai, bj, At, Bt) do { __builtin_amdgcn_s_setprio(1); _Pragma("unroll") for (int m = 0; m < 4; ++m) _Pragma("unroll") for (int n = 0; n < 2; ++n) _Pragma("unroll") for (int k = 0; k < 2; ++k) \
;         acc[ai][bj][m][n] = __builtin_amdgcn_mfma_f32_16x16x32_bf16(Bt[n][k], At[m][k], acc[ai][bj][m][n], 0, 0, 0); __builtin_amdgcn_s_setprio(0); } while (0)
; #define PG8_WAIT_V(n) asm volatile("s_waitcnt vmcnt(" #n ")" ::: "memory")
; #define PG8_WAIT_L(n) asm volatile("s_waitcnt lgkmcnt(" #n ")" ::: "memory")
; #define PG8_BAR __builtin_amdgcn_s_barrier()
; #define PG8_SCHED __builtin_amdgcn_sched_barrier(0)
; template <class Epi, class Sched, bool ALIGN_EPI = false>
; __device__ __forceinline__ void gemm_phase(PG8_LAS unsigned char* lds, const Gemm g, const Sched& S, const Epi& E) {
;     ...
;             PG8_LDA(At, 1, 1); PG8_STAGE(PG8_SB(1, 0), b3, voffB); PG8_STAGE(PG8_SB(1, 1), b3 + hstep, voffB); PG8_STAGE(PG8_SA(1, 0), a3, w0);
;             PG8_WAIT_V(8); PG8_WAIT_L(0); PG8_BAR; PG8_MMA(1, 0, At, B0); PG8_MMA(1, 1, At, B1); PG8_BAR; PG8_SCHED;
;             if constexpr (Epi::KSCALE) { if (((t + 2) & 7) == 0 && t + 2 < nt) { E.kscale(acc, pf, ((t + 2) >> 3) - 1, wr, fr); PG8_SCHED; } }
;         }
;         if constexpr (ALIGN_EPI) { if (wr == 0) PG8_BAR; }
	s_add_i32 s56, s88, s62
	v_lshl_add_u64 v[220:221], v[220:221], 0, s[12:13]
	s_mov_b32 m0, s56
	s_nop 0
	global_load_lds_dwordx4 v[220:221], off
	s_add_i32 m0, s56, 0x2000
	s_add_u32 s54, s54, 0x20080
	v_lshl_add_u64 v[220:221], v[222:223], 0, s[12:13]
	s_addc_u32 s55, s55, 0
	s_add_i32 s56, s89, s62
	global_load_lds_dwordx4 v[220:221], off
	v_lshl_add_u64 v[220:221], s[54:55], 0, v[134:135]
	s_mov_b32 m0, s56
	s_nop 0
	global_load_lds_dwordx4 v[220:221], off
	v_lshl_add_u64 v[220:221], s[54:55], 0, v[138:139]
	s_add_i32 m0, s56, 0x2000
	s_nop 0
	global_load_lds_dwordx4 v[220:221], off
	v_lshl_add_u64 v[220:221], v[224:225], 0, s[12:13]
	s_mov_b32 m0, s68
	s_nop 0
	global_load_lds_dwordx4 v[220:221], off
	v_lshl_add_u64 v[220:221], v[226:227], 0, s[12:13]
	s_mov_b32 m0, s69
	s_nop 0
	global_load_lds_dwordx4 v[220:221], off
	ds_read_b128 v[188:191], v159 offset:49152
	ds_read_b128 v[192:195], v159 offset:50176
	ds_read_b128 v[196:199], v159 offset:51200
	ds_read_b128 v[200:203], v159 offset:52224
	ds_read_b128 v[204:207], v159 offset:53248
	ds_read_b128 v[208:211], v159 offset:54272
	ds_read_b128 v[212:215], v159 offset:55296
	ds_read_b128 v[216:219], v159 offset:56320
	s_waitcnt vmcnt(8)
	s_waitcnt lgkmcnt(0)
	s_barrier
	v_mfma_f32_16x16x32_bf16 v[54:57], v[144:147], v[188:191], v[54:57]
	v_mfma_f32_16x16x32_bf16 v[42:45], v[164:167], v[188:191], v[42:45]
	v_mfma_f32_16x16x32_bf16 v[30:33], v[144:147], v[196:199], v[30:33]
	v_mfma_f32_16x16x32_bf16 v[26:29], v[164:167], v[196:199], v[26:29]
	v_mfma_f32_16x16x32_bf16 v[14:17], v[144:147], v[204:207], v[14:17]
	v_mfma_f32_16x16x32_bf16 v[10:13], v[164:167], v[204:207], v[10:13]
	v_mfma_f32_16x16x32_bf16 v[6:9], v[144:147], v[212:215], v[6:9]
	v_mfma_f32_16x16x32_bf16 v[2:5], v[164:167], v[212:215], v[2:5]
	v_mfma_f32_16x16x32_bf16 v[54:57], v[160:163], v[192:195], v[54:57]
	v_mfma_f32_16x16x32_bf16 v[42:45], v[168:171], v[192:195], v[42:45]
	v_mfma_f32_16x16x32_bf16 v[30:33], v[160:163], v[200:203], v[30:33]
	v_mfma_f32_16x16x32_bf16 v[26:29], v[168:171], v[200:203], v[26:29]
	v_mfma_f32_16x16x32_bf16 v[14:17], v[160:163], v[208:211], v[14:17]
	v_mfma_f32_16x16x32_bf16 v[10:13], v[168:171], v[208:211], v[10:13]
	v_mfma_f32_16x16x32_bf16 v[6:9], v[160:163], v[216:219], v[6:9]
	v_mfma_f32_16x16x32_bf16 v[2:5], v[168:171], v[216:219], v[2:5]
	v_mfma_f32_16x16x32_bf16 v[70:73], v[172:175], v[188:191], v[70:73]
	v_mfma_f32_16x16x32_bf16 v[66:69], v[180:183], v[188:191], v[66:69]
	v_mfma_f32_16x16x32_bf16 v[50:53], v[172:175], v[196:199], v[50:53]
	v_mfma_f32_16x16x32_bf16 v[46:49], v[180:183], v[196:199], v[46:49]
	v_mfma_f32_16x16x32_bf16 v[38:41], v[172:175], v[204:207], v[38:41]
	v_mfma_f32_16x16x32_bf16 v[34:37], v[180:183], v[204:207], v[34:37]
	v_mfma_f32_16x16x32_bf16 v[22:25], v[172:175], v[212:215], v[22:25]
	v_mfma_f32_16x16x32_bf16 v[18:21], v[180:183], v[212:215], v[18:21]
	v_mfma_f32_16x16x32_bf16 v[70:73], v[176:179], v[192:195], v[70:73]
	v_mfma_f32_16x16x32_bf16 v[66:69], v[184:187], v[192:195], v[66:69]
	v_mfma_f32_16x16x32_bf16 v[50:53], v[176:179], v[200:203], v[50:53]
	v_mfma_f32_16x16x32_bf16 v[46:49], v[184:187], v[200:203], v[46:49]
	v_mfma_f32_16x16x32_bf16 v[38:41], v[176:179], v[208:211], v[38:41]
	v_mfma_f32_16x16x32_bf16 v[34:37], v[184:187], v[208:211], v[34:37]
	v_mfma_f32_16x16x32_bf16 v[22:25], v[176:179], v[216:219], v[22:25]
	v_mfma_f32_16x16x32_bf16 v[18:21], v[184:187], v[216:219], v[18:21]
	s_barrier
	s_add_i32 s87, s87, 2
	s_add_u32 s85, s85, 0x100
	s_addc_u32 s86, s86, 0
	s_add_u32 s52, s52, 0x100
	s_addc_u32 s53, s53, 0
	s_cmp_gt_u32 s87, 5
	s_cbranch_scc0 .LBB0_1601
	s_and_b64 vcc, exec, s[14:15]
	s_cbranch_vccz .LBB0_1604
	s_barrier
